# speedup vs baseline: 1.0105x; 1.0013x over previous
_Z8k_stageAPKfS0_S0_S0_PDF16_PKDF16_S0_S1_ii:
	v_readfirstlane_b32 s94, v0
	s_nop 0
	s_lshr_b32 s94, s94, 6
	s_load_dwordx8 s[4:11], s[0:1], 0x0
	v_readfirstlane_b32 s14, v0
	s_lshr_b32 s15, s2, 5
	s_lshl_b32 s2, s2, 7
	s_lshr_b32 s20, s14, 6
	s_and_b32 s12, s2, 0xf80
	s_lshl_b32 s13, s15, 12
	s_mov_b32 s18, s3
	s_cmpk_lt_u32 s14, 0x100
	s_waitcnt lgkmcnt(0)
	s_cselect_b32 s2, s4, s6
	s_cselect_b32 s3, s5, s7
	s_cselect_b32 s4, s8, s10
	s_cselect_b32 s5, s9, s11
	s_cmp_eq_u32 s18, 0
	s_cselect_b32 s3, s3, s5
	s_cselect_b32 s2, s2, s4
	s_lshr_b32 s5, s14, 1
	s_lshl_b32 s4, s15, 7
	s_and_b32 s5, s5, 0x60
	v_bfe_u32 v1, v0, 5, 1
	s_or_b32 s4, s5, s4
	v_lshl_or_b32 v82, v1, 3, s4
	v_mov_b32_e32 v83, 0
	v_lshlrev_b64 v[2:3], 14, v[82:83]
	v_lshlrev_b32_e32 v78, 2, v0
	s_mov_b32 s17, 0
	v_lshl_add_u64 v[2:3], s[2:3], 0, v[2:3]
	s_lshl_b32 s16, s12, 2
	v_and_b32_e32 v79, 0x7c, v78
	v_lshl_add_u64 v[2:3], v[2:3], 0, s[16:17]
	v_lshlrev_b32_e32 v82, 2, v79
	v_lshl_add_u64 v[42:43], v[2:3], 0, v[82:83]
	s_movk_i32 s21, 0x4000
	v_add_co_u32_e32 v10, vcc, s21, v42
	s_mov_b32 s2, 0x8000
	s_nop 0
	v_addc_co_u32_e32 v11, vcc, 0, v43, vcc
	v_add_co_u32_e32 v18, vcc, s2, v42
	s_mov_b32 s2, 0xc000
	s_nop 0
	v_addc_co_u32_e32 v19, vcc, 0, v43, vcc
	v_add_co_u32_e32 v20, vcc, s2, v42
	s_mov_b32 s14, 0x10000
	s_nop 0
	v_addc_co_u32_e32 v21, vcc, 0, v43, vcc
	v_add_co_u32_e32 v26, vcc, s14, v42
	s_mov_b32 s2, 0x14000
	s_nop 0
	v_addc_co_u32_e32 v27, vcc, 0, v43, vcc
	v_add_co_u32_e32 v28, vcc, s2, v42
	s_mov_b32 s2, 0x18000
	s_nop 0
	v_addc_co_u32_e32 v29, vcc, 0, v43, vcc
	v_add_co_u32_e32 v34, vcc, s2, v42
	s_mov_b32 s2, 0x1c000
	s_nop 0
	v_addc_co_u32_e32 v35, vcc, 0, v43, vcc
	v_add_co_u32_e32 v36, vcc, s2, v42
	s_mov_b32 s2, 0x40000
	s_nop 0
	v_addc_co_u32_e32 v37, vcc, 0, v43, vcc
	v_add_co_u32_e32 v66, vcc, s2, v42
	s_mov_b32 s2, 0x44000
	s_nop 0
	v_addc_co_u32_e32 v67, vcc, 0, v43, vcc
	v_add_co_u32_e32 v68, vcc, s2, v42
	s_mov_b32 s2, 0x48000
	s_nop 0
	v_addc_co_u32_e32 v69, vcc, 0, v43, vcc
	global_load_dwordx4 v[2:5], v[42:43], off nt
	global_load_dwordx4 v[6:9], v[10:11], off nt
	v_add_co_u32_e32 v44, vcc, s2, v42
	global_load_dwordx4 v[10:13], v[18:19], off nt
	global_load_dwordx4 v[14:17], v[20:21], off nt
	s_nop 0
	global_load_dwordx4 v[18:21], v[26:27], off nt
	global_load_dwordx4 v[22:25], v[28:29], off nt
	s_nop 0
	global_load_dwordx4 v[26:29], v[34:35], off nt
	global_load_dwordx4 v[30:33], v[36:37], off nt
	v_addc_co_u32_e32 v45, vcc, 0, v43, vcc
	s_mov_b32 s2, 0x4c000
	v_add_co_u32_e32 v46, vcc, s2, v42
	s_mov_b32 s2, 0x50000
	s_nop 0
	v_addc_co_u32_e32 v47, vcc, 0, v43, vcc
	v_add_co_u32_e32 v70, vcc, s2, v42
	s_mov_b32 s2, 0x54000
	s_nop 0
	v_addc_co_u32_e32 v71, vcc, 0, v43, vcc
	v_add_co_u32_e32 v72, vcc, s2, v42
	s_mov_b32 s2, 0x58000
	s_nop 0
	v_addc_co_u32_e32 v73, vcc, 0, v43, vcc
	v_add_co_u32_e32 v74, vcc, s2, v42
	s_mov_b32 s2, 0x5c000
	s_nop 0
	v_addc_co_u32_e32 v75, vcc, 0, v43, vcc
	v_add_co_u32_e32 v76, vcc, s2, v42
	global_load_dwordx4 v[34:37], v[44:45], off nt
	global_load_dwordx4 v[38:41], v[46:47], off nt
	v_addc_co_u32_e32 v77, vcc, 0, v43, vcc
	global_load_dwordx4 v[42:45], v[74:75], off nt
	global_load_dwordx4 v[46:49], v[76:77], off nt
	global_load_dwordx4 v[50:53], v[70:71], off nt
	global_load_dwordx4 v[54:57], v[72:73], off nt
	global_load_dwordx4 v[58:61], v[66:67], off nt
	global_load_dwordx4 v[62:65], v[68:69], off nt
	v_lshl_or_b32 v1, s20, 2, v1
	v_lshrrev_b32_e32 v70, 5, v0
	v_or_b32_e32 v141, 0x200, v0
	v_or_b32_e32 v142, 0x600, v0
	s_or_b32 s16, s13, s12
	s_ashr_i32 s19, s18, 31
	s_lshl_b64 s[12:13], s[16:17], 9
	s_mov_b32 s15, 0x20000
	v_or_b32_e32 v144, 0xa00, v0
	v_bfe_u32 v140, v0, 4, 2
	v_and_b32_e32 v145, 15, v0
	v_lshlrev_b32_e32 v220, 9, v145
	s_waitcnt vmcnt(14)
	v_cvt_pk_f16_f32 v66, v2, v6
	v_lshlrev_b32_e32 v6, 9, v79
	v_bitop3_b32 v2, v78, v1, 12 bitop3:0x6c
	s_waitcnt vmcnt(12)
	v_cvt_pk_f16_f32 v67, v10, v14
	s_waitcnt vmcnt(10)
	v_cvt_pk_f16_f32 v68, v18, v22
	s_waitcnt vmcnt(8)
	v_cvt_pk_f16_f32 v69, v26, v30
	v_lshl_add_u32 v2, v2, 4, v6
	ds_write_b128 v2, v[66:69]
	v_cvt_pk_f16_f32 v66, v3, v7
	v_or_b32_e32 v7, 1, v79
	v_lshlrev_b32_e32 v10, 9, v7
	v_bitop3_b32 v2, v7, v1, 13 bitop3:0x6c
	v_cvt_pk_f16_f32 v69, v27, v31
	v_cvt_pk_f16_f32 v68, v19, v23
	v_cvt_pk_f16_f32 v67, v11, v15
	v_lshl_add_u32 v2, v2, 4, v10
	ds_write_b128 v2, v[66:69]
	v_cvt_pk_f16_f32 v66, v4, v8
	v_or_b32_e32 v8, 2, v79
	v_lshlrev_b32_e32 v11, 9, v8
	v_bitop3_b32 v2, v8, v1, 14 bitop3:0x6c
	v_cvt_pk_f16_f32 v69, v28, v32
	v_cvt_pk_f16_f32 v68, v20, v24
	v_cvt_pk_f16_f32 v67, v12, v16
	v_lshl_add_u32 v2, v2, 4, v11
	v_cvt_pk_f16_f32 v12, v5, v9
	v_or_b32_e32 v9, 3, v79
	ds_write_b128 v2, v[66:69]
	v_lshlrev_b32_e32 v16, 9, v9
	v_bitop3_b32 v2, v9, v1, 15 bitop3:0x6c
	v_cvt_pk_f16_f32 v15, v29, v33
	v_cvt_pk_f16_f32 v14, v21, v25
	v_cvt_pk_f16_f32 v13, v13, v17
	v_lshl_add_u32 v2, v2, 4, v16
	v_or_b32_e32 v1, 2, v1
	ds_write_b128 v2, v[12:15]
	v_bitop3_b32 v12, v78, v1, 12 bitop3:0x6c
	s_waitcnt vmcnt(4)
	v_cvt_pk_f16_f32 v5, v42, v46
	s_waitcnt vmcnt(2)
	v_cvt_pk_f16_f32 v4, v50, v54
	v_cvt_pk_f16_f32 v3, v34, v38
	s_waitcnt vmcnt(0)
	v_cvt_pk_f16_f32 v2, v58, v62
	v_lshl_add_u32 v6, v12, 4, v6
	ds_write_b128 v6, v[2:5]
	v_bitop3_b32 v6, v7, v1, 13 bitop3:0x6c
	v_cvt_pk_f16_f32 v5, v43, v47
	v_cvt_pk_f16_f32 v4, v51, v55
	v_cvt_pk_f16_f32 v3, v35, v39
	v_cvt_pk_f16_f32 v2, v59, v63
	v_lshl_add_u32 v6, v6, 4, v10
	ds_write_b128 v6, v[2:5]
	v_bitop3_b32 v6, v8, v1, 14 bitop3:0x6c
	v_cvt_pk_f16_f32 v5, v44, v48
	v_cvt_pk_f16_f32 v4, v52, v56
	v_cvt_pk_f16_f32 v3, v36, v40
	v_cvt_pk_f16_f32 v2, v60, v64
	v_lshl_add_u32 v6, v6, 4, v11
	v_bitop3_b32 v1, v9, v1, 15 bitop3:0x6c
	ds_write_b128 v6, v[2:5]
	v_cvt_pk_f16_f32 v5, v45, v49
	v_cvt_pk_f16_f32 v4, v53, v57
	v_cvt_pk_f16_f32 v3, v37, v41
	v_cvt_pk_f16_f32 v2, v61, v65
	v_lshl_add_u32 v1, v1, 4, v16
	ds_write_b128 v1, v[2:5]
	v_bitop3_b32 v2, v70, v0, 31 bitop3:0x78
	v_lshlrev_b32_e32 v1, 9, v70
	v_lshlrev_b32_e32 v22, 4, v2
	v_or_b32_e32 v10, v22, v1
	s_waitcnt lgkmcnt(0)
	s_barrier
	ds_read_b128 v[2:5], v10
	s_load_dwordx8 s[4:11], s[0:1], 0x20
	s_load_dwordx2 s[2:3], s[0:1], 0x40
	v_lshlrev_b32_e32 v24, 4, v0
	v_and_b32_e32 v25, 0x1e00, v24
	v_or_b32_e32 v26, v22, v25
	s_waitcnt lgkmcnt(0)
	v_pk_max_f16 v6, v5, v5
	v_and_b32_e32 v18, 31, v0
	v_pk_max_f16 v9, v6, 0
	v_pk_max_f16 v6, v4, v4
	v_lshlrev_b32_e32 v29, 4, v18
	v_pk_max_f16 v8, v6, 0
	v_pk_max_f16 v6, v3, v3
	s_lshl_b64 s[0:1], s[18:19], 23
	v_pk_max_f16 v7, v6, 0
	v_pk_max_f16 v6, v2, v2
	s_add_u32 s0, s4, s0
	v_pk_max_f16 v6, v6, 0
	ds_write_b128 v10, v[6:9]
	v_lshlrev_b32_e32 v6, 4, v141
	v_and_b32_e32 v23, 0x3e00, v6
	v_or_b32_e32 v14, v22, v23
	ds_read_b128 v[6:9], v14
	s_addc_u32 s1, s5, s1
	s_add_u32 s12, s0, s12
	s_addc_u32 s0, s1, s13
	s_and_b32 s13, s0, 0xffff
	s_waitcnt lgkmcnt(0)
	v_pk_max_f16 v10, v9, v9
	v_or_b32_e32 v1, v1, v29
	v_pk_max_f16 v13, v10, 0
	v_pk_max_f16 v10, v8, v8
	buffer_store_dwordx4 v[2:5], v1, s[12:15], 0 offen sc1
	v_pk_max_f16 v12, v10, 0
	v_pk_max_f16 v10, v7, v7
	v_or_b32_e32 v1, v23, v29
	v_pk_max_f16 v11, v10, 0
	v_pk_max_f16 v10, v6, v6
	buffer_store_dwordx4 v[6:9], v1, s[12:15], 0 offen sc1
	v_pk_max_f16 v10, v10, 0
	ds_write_b128 v14, v[10:13]
	ds_read_b128 v[10:13], v26 offset:16384
	v_or_b32_e32 v25, v25, v29
	v_or_b32_e32 v6, 0x4000, v25
	s_mov_b32 s0, 0xfe00
	s_waitcnt lgkmcnt(0)
	v_pk_max_f16 v14, v13, v13
	s_nop 0
	v_pk_max_f16 v17, v14, 0
	v_pk_max_f16 v14, v12, v12
	buffer_store_dwordx4 v[10:13], v6, s[12:15], 0 offen sc1
	v_pk_max_f16 v16, v14, 0
	v_pk_max_f16 v14, v11, v11
	s_nop 0
	v_pk_max_f16 v15, v14, 0
	v_pk_max_f16 v14, v10, v10
	s_nop 0
	v_pk_max_f16 v14, v14, 0
	ds_write_b128 v26, v[14:17] offset:16384
	v_lshlrev_b32_e32 v14, 4, v142
	v_and_b32_e32 v27, 0x7e00, v14
	v_or_b32_e32 v28, v22, v27
	ds_read_b128 v[14:17], v28
	v_or_b32_e32 v10, v27, v29
	s_waitcnt lgkmcnt(0)
	v_pk_max_f16 v18, v17, v17
	s_nop 0
	v_pk_max_f16 v21, v18, 0
	v_pk_max_f16 v18, v16, v16
	buffer_store_dwordx4 v[14:17], v10, s[12:15], 0 offen sc1
	v_pk_max_f16 v20, v18, 0
	v_pk_max_f16 v18, v15, v15
	v_or_b32_e32 v10, 0x8000, v25
	v_pk_max_f16 v19, v18, 0
	v_pk_max_f16 v18, v14, v14
	s_nop 0
	v_pk_max_f16 v18, v18, 0
	ds_write_b128 v28, v[18:21]
	ds_read_b128 v[18:21], v26 offset:32768
	s_waitcnt lgkmcnt(0)
	v_pk_max_f16 v1, v21, v21
	s_nop 0
	v_pk_max_f16 v5, v1, 0
	v_pk_max_f16 v1, v20, v20
	buffer_store_dwordx4 v[18:21], v10, s[12:15], 0 offen sc1
	v_pk_max_f16 v4, v1, 0
	v_pk_max_f16 v1, v19, v19
	s_nop 0
	v_pk_max_f16 v3, v1, 0
	v_pk_max_f16 v1, v18, v18
	s_nop 0
	v_pk_max_f16 v2, v1, 0
	v_lshlrev_b32_e32 v1, 4, v144
	v_and_b32_e32 v1, 0xbe00, v1
	ds_write_b128 v26, v[2:5] offset:32768
	v_or_b32_e32 v23, v22, v1
	ds_read_b128 v[2:5], v23
	v_or_b32_e32 v1, v1, v29
	s_waitcnt lgkmcnt(0)
	v_pk_max_f16 v6, v5, v5
	s_nop 0
	v_pk_max_f16 v9, v6, 0
	v_pk_max_f16 v6, v4, v4
	buffer_store_dwordx4 v[2:5], v1, s[12:15], 0 offen sc1
	v_pk_max_f16 v8, v6, 0
	v_pk_max_f16 v6, v3, v3
	v_or_b32_e32 v1, 0xc000, v25
	v_pk_max_f16 v7, v6, 0
	v_pk_max_f16 v6, v2, v2
	s_nop 0
	v_pk_max_f16 v6, v6, 0
	ds_write_b128 v23, v[6:9]
	ds_read_b128 v[6:9], v26 offset:49152
	s_waitcnt lgkmcnt(0)
	v_pk_max_f16 v10, v9, v9
	s_nop 0
	v_pk_max_f16 v13, v10, 0
	v_pk_max_f16 v10, v8, v8
	buffer_store_dwordx4 v[6:9], v1, s[12:15], 0 offen sc1
	v_pk_max_f16 v12, v10, 0
	v_pk_max_f16 v10, v7, v7
	s_nop 0
	v_pk_max_f16 v11, v10, 0
	v_pk_max_f16 v10, v6, v6
	s_nop 0
	v_pk_max_f16 v10, v10, 0
	ds_write_b128 v26, v[10:13] offset:49152
	v_mov_b32_e32 v10, 0xe000
	v_bitop3_b32 v14, v24, s0, v10 bitop3:0xc8
	s_mul_i32 s0, s3, s18
	v_or_b32_e32 v15, v22, v14
	s_add_i32 s0, s0, s2
	ds_read_b128 v[10:13], v15
	s_mul_i32 s2, s0, 0x60000
	s_mul_hi_i32 s1, s0, 0x60000
	s_add_u32 s2, s6, s2
	s_mulk_i32 s0, 0x300
	s_addc_u32 s3, s7, s1
	s_ashr_i32 s1, s0, 31
	s_lshl_b64 s[0:1], s[0:1], 2
	v_or_b32_e32 v1, v14, v29
	s_add_u32 s4, s8, s0
	s_waitcnt lgkmcnt(0)
	buffer_store_dwordx4 v[10:13], v1, s[12:15], 0 offen sc1
	v_pk_max_f16 v1, v13, v13
	s_addc_u32 s5, s9, s1
	s_mul_i32 s0, s18, 0x1800000
	v_pk_max_f16 v5, v1, 0
	v_pk_max_f16 v1, v12, v12
	s_mul_hi_i32 s1, s18, 0x1800000
	s_add_u32 s0, s10, s0
	v_pk_max_f16 v4, v1, 0
	v_pk_max_f16 v1, v11, v11
	s_addc_u32 s1, s11, s1
	v_pk_max_f16 v3, v1, 0
	v_pk_max_f16 v1, v10, v10
	s_and_b32 s1, s1, 0xffff
	s_mul_i32 s7, s20, 0x6000
	v_pk_max_f16 v2, v1, 0
	v_and_b32_e32 v1, 63, v0
	s_mul_hi_u32 s6, s20, 0x6000
	s_add_u32 s2, s2, s7
	s_addc_u32 s3, s3, s6
	v_lshlrev_b32_e32 v82, 4, v1
	v_lshl_add_u64 v[118:119], s[2:3], 0, v[82:83]
	s_movk_i32 s6, 0x1000
	v_add_co_u32_e32 v50, vcc, s6, v118
	s_movk_i32 s6, 0x2000
	s_nop 0
	v_addc_co_u32_e32 v51, vcc, 0, v119, vcc
	ds_write_b128 v15, v[2:5]
	v_add_co_u32_e32 v52, vcc, s6, v118
	global_load_dwordx4 v[2:5], v82, s[2:3] offset:1024
	global_load_dwordx4 v[6:9], v82, s[2:3] offset:2048
	v_addc_co_u32_e32 v53, vcc, 0, v119, vcc
	global_load_dwordx4 v[10:13], v82, s[2:3] offset:3072
	global_load_dwordx4 v[14:17], v[52:53], off offset:-4096
	global_load_dwordx4 v[18:21], v[50:51], off offset:1024
	global_load_dwordx4 v[22:25], v[50:51], off offset:2048
	global_load_dwordx4 v[26:29], v82, s[2:3]
	global_load_dwordx4 v[30:33], v[50:51], off offset:3072
	global_load_dwordx4 v[34:37], v[52:53], off
	global_load_dwordx4 v[38:41], v[52:53], off offset:1024
	global_load_dwordx4 v[42:45], v[52:53], off offset:2048
	global_load_dwordx4 v[46:49], v[52:53], off offset:3072
	s_movk_i32 s2, 0x3000
	v_add_co_u32_e32 v116, vcc, s2, v118
	s_waitcnt lgkmcnt(0)
	s_nop 0
	v_addc_co_u32_e32 v117, vcc, 0, v119, vcc
	v_add_co_u32_e32 v132, vcc, s21, v118
	s_barrier
	s_cmp_lt_u32 s94, 4
	s_cbranch_scc1 .Lmystag1_2
	s_sleep 7
.Lmystag1_2:
	s_nop 0
	v_addc_co_u32_e32 v133, vcc, 0, v119, vcc
	global_load_dwordx4 v[50:53], v[132:133], off offset:-4096
	global_load_dwordx4 v[54:57], v[116:117], off offset:1024
	global_load_dwordx4 v[58:61], v[116:117], off offset:2048
	v_bitop3_b32 v1, v140, v0, 15 bitop3:0x78
	v_lshl_or_b32 v134, v1, 4, v220
	ds_read_b128 v[62:65], v134
	ds_read_b128 v[66:69], v134 offset:8192
	ds_read_b128 v[70:73], v134 offset:16384
	ds_read_b128 v[74:77], v134 offset:24576
	ds_read_b128 v[78:81], v134 offset:32768
	ds_read_b128 v[84:87], v134 offset:40960
	ds_read_b128 v[88:91], v134 offset:49152
	ds_read_b128 v[92:95], v134 offset:57344
	s_mul_i32 s7, s20, 48
	v_lshl_or_b32 v82, v140, 2, s7
	s_mul_i32 s7, s20, 0x60
	s_add_i32 s7, s7, 0x10000
	v_mul_u32_u24_e32 v1, 0x556, v0
	v_lshl_or_b32 v250, v140, 3, s7
	s_or_b32 s7, s16, 64
	v_lshrrev_b32_e32 v143, 16, v1
	s_movk_i32 s6, 0x600
	s_mov_b32 s2, 0x1800000
	s_mov_b32 s3, s15
	v_or_b32_e32 v139, s7, v143
	s_waitcnt vmcnt(8) lgkmcnt(7)
	v_mfma_f32_16x16x32_f16 v[96:99], v[26:29], v[62:65], 0
	s_waitcnt lgkmcnt(6)
	v_mfma_f32_16x16x32_f16 v[100:103], v[26:29], v[66:69], 0
	s_waitcnt lgkmcnt(5)
	v_mfma_f32_16x16x32_f16 v[104:107], v[26:29], v[70:73], 0
	s_waitcnt lgkmcnt(4)
	v_mfma_f32_16x16x32_f16 v[108:111], v[26:29], v[74:77], 0
	s_waitcnt lgkmcnt(3)
	v_mfma_f32_16x16x32_f16 v[112:115], v[26:29], v[78:81], 0
	s_waitcnt lgkmcnt(2)
	v_mfma_f32_16x16x32_f16 v[120:123], v[26:29], v[84:87], 0
	s_waitcnt lgkmcnt(1)
	v_mfma_f32_16x16x32_f16 v[124:127], v[26:29], v[88:91], 0
	s_waitcnt lgkmcnt(0)
	v_mfma_f32_16x16x32_f16 v[26:29], v[26:29], v[92:95], 0
	v_mfma_f32_16x16x32_f16 v[128:131], v[2:5], v[62:65], 0
	v_mfma_f32_16x16x32_f16 v[146:149], v[2:5], v[66:69], 0
	v_mfma_f32_16x16x32_f16 v[150:153], v[2:5], v[70:73], 0
	v_mfma_f32_16x16x32_f16 v[154:157], v[2:5], v[74:77], 0
	v_mfma_f32_16x16x32_f16 v[158:161], v[2:5], v[78:81], 0
	v_mfma_f32_16x16x32_f16 v[162:165], v[2:5], v[84:87], 0
	v_mfma_f32_16x16x32_f16 v[166:169], v[2:5], v[88:91], 0
	v_mfma_f32_16x16x32_f16 v[2:5], v[2:5], v[92:95], 0
	v_mfma_f32_16x16x32_f16 v[62:65], v[6:9], v[62:65], 0
	v_mfma_f32_16x16x32_f16 v[66:69], v[6:9], v[66:69], 0
	v_mfma_f32_16x16x32_f16 v[70:73], v[6:9], v[70:73], 0
	v_mfma_f32_16x16x32_f16 v[74:77], v[6:9], v[74:77], 0
	v_mfma_f32_16x16x32_f16 v[78:81], v[6:9], v[78:81], 0
	v_mfma_f32_16x16x32_f16 v[84:87], v[6:9], v[84:87], 0
	v_mfma_f32_16x16x32_f16 v[88:91], v[6:9], v[88:91], 0
	v_mfma_f32_16x16x32_f16 v[6:9], v[6:9], v[92:95], 0
	global_load_dwordx4 v[92:95], v[116:117], off offset:3072
	global_load_dwordx4 v[170:173], v[132:133], off
	global_load_dwordx4 v[174:177], v[132:133], off offset:1024
	v_bitop3_b32 v1, v140, v145, 4 bitop3:0x36
	v_lshl_or_b32 v1, v1, 4, v220
	ds_read_b128 v[178:181], v1
	ds_read_b128 v[182:185], v1 offset:8192
	ds_read_b128 v[186:189], v1 offset:16384
	ds_read_b128 v[190:193], v1 offset:24576
	ds_read_b128 v[194:197], v1 offset:32768
	ds_read_b128 v[198:201], v1 offset:40960
	ds_read_b128 v[202:205], v1 offset:49152
	ds_read_b128 v[206:209], v1 offset:57344
	s_waitcnt lgkmcnt(7)
	v_mfma_f32_16x16x32_f16 v[96:99], v[10:13], v[178:181], v[96:99]
	s_waitcnt lgkmcnt(6)
	v_mfma_f32_16x16x32_f16 v[100:103], v[10:13], v[182:185], v[100:103]
	s_waitcnt lgkmcnt(5)
	v_mfma_f32_16x16x32_f16 v[104:107], v[10:13], v[186:189], v[104:107]
	s_waitcnt lgkmcnt(4)
	v_mfma_f32_16x16x32_f16 v[108:111], v[10:13], v[190:193], v[108:111]
	s_waitcnt lgkmcnt(3)
	v_mfma_f32_16x16x32_f16 v[112:115], v[10:13], v[194:197], v[112:115]
	s_waitcnt lgkmcnt(2)
	v_mfma_f32_16x16x32_f16 v[120:123], v[10:13], v[198:201], v[120:123]
	s_waitcnt lgkmcnt(1)
	v_mfma_f32_16x16x32_f16 v[124:127], v[10:13], v[202:205], v[124:127]
	s_waitcnt lgkmcnt(0)
	v_mfma_f32_16x16x32_f16 v[10:13], v[10:13], v[206:209], v[26:29]
	v_mfma_f32_16x16x32_f16 v[26:29], v[14:17], v[178:181], v[128:131]
	v_mfma_f32_16x16x32_f16 v[128:131], v[14:17], v[182:185], v[146:149]
	v_mfma_f32_16x16x32_f16 v[146:149], v[14:17], v[186:189], v[150:153]
	v_mfma_f32_16x16x32_f16 v[150:153], v[14:17], v[190:193], v[154:157]
	v_mfma_f32_16x16x32_f16 v[154:157], v[14:17], v[194:197], v[158:161]
	v_mfma_f32_16x16x32_f16 v[158:161], v[14:17], v[198:201], v[162:165]
	v_mfma_f32_16x16x32_f16 v[162:165], v[14:17], v[202:205], v[166:169]
	v_mfma_f32_16x16x32_f16 v[2:5], v[14:17], v[206:209], v[2:5]
	v_mfma_f32_16x16x32_f16 v[14:17], v[18:21], v[178:181], v[62:65]
	v_mfma_f32_16x16x32_f16 v[62:65], v[18:21], v[182:185], v[66:69]
	v_mfma_f32_16x16x32_f16 v[66:69], v[18:21], v[186:189], v[70:73]
	v_mfma_f32_16x16x32_f16 v[70:73], v[18:21], v[190:193], v[74:77]
	v_mfma_f32_16x16x32_f16 v[74:77], v[18:21], v[194:197], v[78:81]
	v_mfma_f32_16x16x32_f16 v[78:81], v[18:21], v[198:201], v[84:87]
	v_mfma_f32_16x16x32_f16 v[84:87], v[18:21], v[202:205], v[88:91]
	v_mfma_f32_16x16x32_f16 v[6:9], v[18:21], v[206:209], v[6:9]
	s_movk_i32 s8, 0x5000
	v_add_co_u32_e32 v116, vcc, s8, v118
	global_load_dwordx4 v[88:91], v[132:133], off offset:2048
	global_load_dwordx4 v[166:169], v[132:133], off offset:3072
	v_addc_co_u32_e32 v117, vcc, 0, v119, vcc
	global_load_dwordx4 v[178:181], v[116:117], off
	v_bitop3_b32 v18, v140, v145, 8 bitop3:0x36
	v_lshl_or_b32 v133, v18, 4, v220
	ds_read_b128 v[18:21], v133
	ds_read_b128 v[182:185], v133 offset:8192
	ds_read_b128 v[186:189], v133 offset:16384
	ds_read_b128 v[190:193], v133 offset:24576
	ds_read_b128 v[194:197], v133 offset:32768
	ds_read_b128 v[198:201], v133 offset:40960
	ds_read_b128 v[202:205], v133 offset:49152
	ds_read_b128 v[206:209], v133 offset:57344
	s_waitcnt lgkmcnt(7)
	v_mfma_f32_16x16x32_f16 v[96:99], v[22:25], v[18:21], v[96:99]
	s_waitcnt lgkmcnt(6)
	v_mfma_f32_16x16x32_f16 v[100:103], v[22:25], v[182:185], v[100:103]
	s_waitcnt lgkmcnt(5)
	v_mfma_f32_16x16x32_f16 v[104:107], v[22:25], v[186:189], v[104:107]
	s_waitcnt lgkmcnt(4)
	v_mfma_f32_16x16x32_f16 v[108:111], v[22:25], v[190:193], v[108:111]
	s_waitcnt lgkmcnt(3)
	v_mfma_f32_16x16x32_f16 v[112:115], v[22:25], v[194:197], v[112:115]
	s_waitcnt lgkmcnt(2)
	v_mfma_f32_16x16x32_f16 v[120:123], v[22:25], v[198:201], v[120:123]
	s_waitcnt lgkmcnt(1)
	v_mfma_f32_16x16x32_f16 v[124:127], v[22:25], v[202:205], v[124:127]
	s_waitcnt lgkmcnt(0)
	v_mfma_f32_16x16x32_f16 v[10:13], v[22:25], v[206:209], v[10:13]
	s_waitcnt vmcnt(13)
	v_mfma_f32_16x16x32_f16 v[22:25], v[30:33], v[18:21], v[26:29]
	v_mfma_f32_16x16x32_f16 v[26:29], v[30:33], v[182:185], v[128:131]
	v_mfma_f32_16x16x32_f16 v[128:131], v[30:33], v[186:189], v[146:149]
	v_mfma_f32_16x16x32_f16 v[146:149], v[30:33], v[190:193], v[150:153]
	v_mfma_f32_16x16x32_f16 v[150:153], v[30:33], v[194:197], v[154:157]
	v_mfma_f32_16x16x32_f16 v[154:157], v[30:33], v[198:201], v[158:161]
	v_mfma_f32_16x16x32_f16 v[158:161], v[30:33], v[202:205], v[162:165]
	v_mfma_f32_16x16x32_f16 v[2:5], v[30:33], v[206:209], v[2:5]
	s_waitcnt vmcnt(12)
	v_mfma_f32_16x16x32_f16 v[14:17], v[34:37], v[18:21], v[14:17]
	v_mfma_f32_16x16x32_f16 v[18:21], v[34:37], v[182:185], v[62:65]
	v_mfma_f32_16x16x32_f16 v[30:33], v[34:37], v[186:189], v[66:69]
	v_mfma_f32_16x16x32_f16 v[62:65], v[34:37], v[190:193], v[70:73]
	v_mfma_f32_16x16x32_f16 v[66:69], v[34:37], v[194:197], v[74:77]
	v_mfma_f32_16x16x32_f16 v[70:73], v[34:37], v[198:201], v[78:81]
	v_mfma_f32_16x16x32_f16 v[74:77], v[34:37], v[202:205], v[84:87]
	v_mfma_f32_16x16x32_f16 v[6:9], v[34:37], v[206:209], v[6:9]
	s_nop 0
	global_load_dwordx4 v[78:81], v[116:117], off offset:1024
	global_load_dwordx4 v[162:165], v[116:117], off offset:2048
	global_load_dwordx4 v[182:185], v[116:117], off offset:3072
	v_bitop3_b32 v34, v140, v145, 12 bitop3:0x36
	v_lshl_or_b32 v135, v34, 4, v220
	ds_read_b128 v[34:37], v135
	ds_read_b128 v[84:87], v135 offset:8192
	ds_read_b128 v[186:189], v135 offset:16384
	ds_read_b128 v[190:193], v135 offset:24576
	ds_read_b128 v[194:197], v135 offset:32768
	ds_read_b128 v[198:201], v135 offset:40960
	ds_read_b128 v[202:205], v135 offset:49152
	ds_read_b128 v[206:209], v135 offset:57344
	s_waitcnt vmcnt(14) lgkmcnt(7)
	v_mfma_f32_16x16x32_f16 v[96:99], v[38:41], v[34:37], v[96:99]
	s_waitcnt lgkmcnt(6)
	v_mfma_f32_16x16x32_f16 v[100:103], v[38:41], v[84:87], v[100:103]
	s_waitcnt lgkmcnt(5)
	v_mfma_f32_16x16x32_f16 v[104:107], v[38:41], v[186:189], v[104:107]
	s_waitcnt lgkmcnt(4)
	v_mfma_f32_16x16x32_f16 v[108:111], v[38:41], v[190:193], v[108:111]
	s_waitcnt lgkmcnt(3)
	v_mfma_f32_16x16x32_f16 v[112:115], v[38:41], v[194:197], v[112:115]
	s_waitcnt lgkmcnt(2)
	v_mfma_f32_16x16x32_f16 v[120:123], v[38:41], v[198:201], v[120:123]
	s_waitcnt lgkmcnt(1)
	v_mfma_f32_16x16x32_f16 v[124:127], v[38:41], v[202:205], v[124:127]
	s_waitcnt lgkmcnt(0)
	v_mfma_f32_16x16x32_f16 v[210:213], v[38:41], v[206:209], v[10:13]
	s_waitcnt vmcnt(13)
	v_mfma_f32_16x16x32_f16 v[22:25], v[42:45], v[34:37], v[22:25]
	v_mfma_f32_16x16x32_f16 v[214:217], v[42:45], v[84:87], v[26:29]
	v_mfma_f32_16x16x32_f16 v[128:131], v[42:45], v[186:189], v[128:131]
	v_mfma_f32_16x16x32_f16 v[146:149], v[42:45], v[190:193], v[146:149]
	v_mfma_f32_16x16x32_f16 v[150:153], v[42:45], v[194:197], v[150:153]
	v_mfma_f32_16x16x32_f16 v[154:157], v[42:45], v[198:201], v[154:157]
	v_mfma_f32_16x16x32_f16 v[158:161], v[42:45], v[202:205], v[158:161]
	v_mfma_f32_16x16x32_f16 v[2:5], v[42:45], v[206:209], v[2:5]
	s_waitcnt vmcnt(12)
	v_mfma_f32_16x16x32_f16 v[14:17], v[46:49], v[34:37], v[14:17]
	v_mfma_f32_16x16x32_f16 v[18:21], v[46:49], v[84:87], v[18:21]
	v_mfma_f32_16x16x32_f16 v[30:33], v[46:49], v[186:189], v[30:33]
	v_mfma_f32_16x16x32_f16 v[34:37], v[46:49], v[190:193], v[62:65]
	v_mfma_f32_16x16x32_f16 v[42:45], v[46:49], v[194:197], v[66:69]
	v_mfma_f32_16x16x32_f16 v[62:65], v[46:49], v[198:201], v[70:73]
	v_mfma_f32_16x16x32_f16 v[66:69], v[46:49], v[202:205], v[74:77]
	v_mfma_f32_16x16x32_f16 v[6:9], v[46:49], v[206:209], v[6:9]
	s_mov_b32 s8, 0x30000
	v_add_co_u32_e32 v116, vcc, s8, v118
	s_mov_b32 s8, 0x31000
	s_nop 0
	v_addc_co_u32_e32 v117, vcc, 0, v119, vcc
	v_add_co_u32_e32 v218, vcc, s8, v118
	v_bitop3_b32 v46, v140, v145, 16 bitop3:0x36
	s_nop 0
	v_addc_co_u32_e32 v219, vcc, 0, v119, vcc
	global_load_dwordx4 v[38:41], v[218:219], off offset:-4096
	global_load_dwordx4 v[26:29], v[116:117], off offset:1024
	global_load_dwordx4 v[10:13], v[116:117], off offset:2048
	v_lshl_or_b32 v136, v46, 4, v220
	ds_read_b128 v[46:49], v136
	ds_read_b128 v[70:73], v136 offset:8192
	ds_read_b128 v[74:77], v136 offset:16384
	ds_read_b128 v[84:87], v136 offset:24576
	ds_read_b128 v[186:189], v136 offset:32768
	ds_read_b128 v[190:193], v136 offset:40960
	ds_read_b128 v[194:197], v136 offset:49152
	ds_read_b128 v[198:201], v136 offset:57344
	s_waitcnt vmcnt(14) lgkmcnt(7)
	v_mfma_f32_16x16x32_f16 v[96:99], v[50:53], v[46:49], v[96:99]
	s_waitcnt lgkmcnt(6)
	v_mfma_f32_16x16x32_f16 v[100:103], v[50:53], v[70:73], v[100:103]
	s_waitcnt lgkmcnt(5)
	v_mfma_f32_16x16x32_f16 v[104:107], v[50:53], v[74:77], v[104:107]
	s_waitcnt lgkmcnt(4)
	v_mfma_f32_16x16x32_f16 v[108:111], v[50:53], v[84:87], v[108:111]
	s_waitcnt lgkmcnt(3)
	v_mfma_f32_16x16x32_f16 v[112:115], v[50:53], v[186:189], v[112:115]
	s_waitcnt lgkmcnt(2)
	v_mfma_f32_16x16x32_f16 v[120:123], v[50:53], v[190:193], v[120:123]
	s_waitcnt lgkmcnt(1)
	v_mfma_f32_16x16x32_f16 v[124:127], v[50:53], v[194:197], v[124:127]
	s_waitcnt lgkmcnt(0)
	v_mfma_f32_16x16x32_f16 v[50:53], v[50:53], v[198:201], v[210:213]
	s_waitcnt vmcnt(13)
	v_mfma_f32_16x16x32_f16 v[202:205], v[54:57], v[46:49], v[22:25]
	v_mfma_f32_16x16x32_f16 v[206:209], v[54:57], v[70:73], v[214:217]
	v_mfma_f32_16x16x32_f16 v[128:131], v[54:57], v[74:77], v[128:131]
	v_mfma_f32_16x16x32_f16 v[146:149], v[54:57], v[84:87], v[146:149]
	v_mfma_f32_16x16x32_f16 v[150:153], v[54:57], v[186:189], v[150:153]
	v_mfma_f32_16x16x32_f16 v[154:157], v[54:57], v[190:193], v[154:157]
	v_mfma_f32_16x16x32_f16 v[158:161], v[54:57], v[194:197], v[158:161]
	v_mfma_f32_16x16x32_f16 v[54:57], v[54:57], v[198:201], v[2:5]
	s_waitcnt vmcnt(12)
	v_mfma_f32_16x16x32_f16 v[14:17], v[58:61], v[46:49], v[14:17]
	v_mfma_f32_16x16x32_f16 v[18:21], v[58:61], v[70:73], v[18:21]
	v_mfma_f32_16x16x32_f16 v[30:33], v[58:61], v[74:77], v[30:33]
	v_mfma_f32_16x16x32_f16 v[34:37], v[58:61], v[84:87], v[34:37]
	v_mfma_f32_16x16x32_f16 v[42:45], v[58:61], v[186:189], v[42:45]
	v_mfma_f32_16x16x32_f16 v[46:49], v[58:61], v[190:193], v[62:65]
	v_mfma_f32_16x16x32_f16 v[62:65], v[58:61], v[194:197], v[66:69]
	v_mfma_f32_16x16x32_f16 v[58:61], v[58:61], v[198:201], v[6:9]
	global_load_dwordx4 v[22:25], v[116:117], off offset:3072
	s_nop 1
	global_load_dwordx4 v[6:9], v[218:219], off
	global_load_dwordx4 v[2:5], v[218:219], off offset:1024
	v_bitop3_b32 v66, v140, v145, 20 bitop3:0x36
	v_lshl_or_b32 v137, v66, 4, v220
	ds_read_b128 v[66:69], v137
	ds_read_b128 v[70:73], v137 offset:8192
	ds_read_b128 v[74:77], v137 offset:16384
	ds_read_b128 v[84:87], v137 offset:24576
	ds_read_b128 v[186:189], v137 offset:32768
	ds_read_b128 v[190:193], v137 offset:40960
	ds_read_b128 v[194:197], v137 offset:49152
	ds_read_b128 v[198:201], v137 offset:57344
	s_waitcnt vmcnt(14) lgkmcnt(7)
	v_mfma_f32_16x16x32_f16 v[96:99], v[92:95], v[66:69], v[96:99]
	s_waitcnt lgkmcnt(6)
	v_mfma_f32_16x16x32_f16 v[100:103], v[92:95], v[70:73], v[100:103]
	s_waitcnt lgkmcnt(5)
	v_mfma_f32_16x16x32_f16 v[104:107], v[92:95], v[74:77], v[104:107]
	s_waitcnt lgkmcnt(4)
	v_mfma_f32_16x16x32_f16 v[108:111], v[92:95], v[84:87], v[108:111]
	s_waitcnt lgkmcnt(3)
	v_mfma_f32_16x16x32_f16 v[112:115], v[92:95], v[186:189], v[112:115]
	s_waitcnt lgkmcnt(2)
	v_mfma_f32_16x16x32_f16 v[210:213], v[92:95], v[190:193], v[120:123]
	s_waitcnt lgkmcnt(1)
	v_mfma_f32_16x16x32_f16 v[124:127], v[92:95], v[194:197], v[124:127]
	s_waitcnt lgkmcnt(0)
	v_mfma_f32_16x16x32_f16 v[50:53], v[92:95], v[198:201], v[50:53]
	s_waitcnt vmcnt(13)
	v_mfma_f32_16x16x32_f16 v[92:95], v[170:173], v[66:69], v[202:205]
	v_mfma_f32_16x16x32_f16 v[202:205], v[170:173], v[70:73], v[206:209]
	v_mfma_f32_16x16x32_f16 v[128:131], v[170:173], v[74:77], v[128:131]
	v_mfma_f32_16x16x32_f16 v[146:149], v[170:173], v[84:87], v[146:149]
	v_mfma_f32_16x16x32_f16 v[150:153], v[170:173], v[186:189], v[150:153]
	v_mfma_f32_16x16x32_f16 v[154:157], v[170:173], v[190:193], v[154:157]
	v_mfma_f32_16x16x32_f16 v[158:161], v[170:173], v[194:197], v[158:161]
	v_mfma_f32_16x16x32_f16 v[54:57], v[170:173], v[198:201], v[54:57]
	s_waitcnt vmcnt(12)
	v_mfma_f32_16x16x32_f16 v[66:69], v[174:177], v[66:69], v[14:17]
	v_mfma_f32_16x16x32_f16 v[70:73], v[174:177], v[70:73], v[18:21]
	v_mfma_f32_16x16x32_f16 v[74:77], v[174:177], v[74:77], v[30:33]
	v_mfma_f32_16x16x32_f16 v[34:37], v[174:177], v[84:87], v[34:37]
	v_mfma_f32_16x16x32_f16 v[42:45], v[174:177], v[186:189], v[42:45]
	v_mfma_f32_16x16x32_f16 v[46:49], v[174:177], v[190:193], v[46:49]
	v_mfma_f32_16x16x32_f16 v[62:65], v[174:177], v[194:197], v[62:65]
	v_mfma_f32_16x16x32_f16 v[58:61], v[174:177], v[198:201], v[58:61]
	s_mov_b32 s8, 0x33000
	v_add_co_u32_e32 v122, vcc, s8, v118
	global_load_dwordx4 v[30:33], v[218:219], off offset:2048
	global_load_dwordx4 v[14:17], v[218:219], off offset:3072
	v_addc_co_u32_e32 v123, vcc, 0, v119, vcc
	global_load_dwordx4 v[18:21], v[122:123], off offset:-4096
	v_bitop3_b32 v84, v140, v145, 24 bitop3:0x36
	v_lshl_or_b32 v138, v84, 4, v220
	ds_read_b128 v[84:87], v138
	ds_read_b128 v[170:173], v138 offset:8192
	ds_read_b128 v[174:177], v138 offset:16384
	ds_read_b128 v[186:189], v138 offset:24576
	ds_read_b128 v[190:193], v138 offset:32768
	ds_read_b128 v[194:197], v138 offset:40960
	ds_read_b128 v[198:201], v138 offset:49152
	ds_read_b128 v[206:209], v138 offset:57344
	s_mov_b32 s8, 0x32000
	v_add_co_u32_e32 v116, vcc, s8, v118
	s_nop 1
	v_addc_co_u32_e32 v117, vcc, 0, v119, vcc
	s_waitcnt vmcnt(14) lgkmcnt(7)
	v_mfma_f32_16x16x32_f16 v[96:99], v[88:91], v[84:87], v[96:99]
	s_waitcnt lgkmcnt(6)
	v_mfma_f32_16x16x32_f16 v[100:103], v[88:91], v[170:173], v[100:103]
	s_waitcnt lgkmcnt(5)
	v_mfma_f32_16x16x32_f16 v[104:107], v[88:91], v[174:177], v[104:107]
	s_waitcnt lgkmcnt(4)
	v_mfma_f32_16x16x32_f16 v[108:111], v[88:91], v[186:189], v[108:111]
	s_waitcnt lgkmcnt(3)
	v_mfma_f32_16x16x32_f16 v[112:115], v[88:91], v[190:193], v[112:115]
	s_waitcnt lgkmcnt(2)
	v_mfma_f32_16x16x32_f16 v[210:213], v[88:91], v[194:197], v[210:213]
	s_waitcnt lgkmcnt(1)
	v_mfma_f32_16x16x32_f16 v[124:127], v[88:91], v[198:201], v[124:127]
	s_waitcnt lgkmcnt(0)
	v_mfma_f32_16x16x32_f16 v[50:53], v[88:91], v[206:209], v[50:53]
	s_waitcnt vmcnt(13)
	v_mfma_f32_16x16x32_f16 v[90:93], v[166:169], v[84:87], v[92:95]
	v_mfma_f32_16x16x32_f16 v[202:205], v[166:169], v[170:173], v[202:205]
	v_mfma_f32_16x16x32_f16 v[128:131], v[166:169], v[174:177], v[128:131]
	v_mfma_f32_16x16x32_f16 v[146:149], v[166:169], v[186:189], v[146:149]
	v_mfma_f32_16x16x32_f16 v[150:153], v[166:169], v[190:193], v[150:153]
	v_mfma_f32_16x16x32_f16 v[154:157], v[166:169], v[194:197], v[154:157]
	v_mfma_f32_16x16x32_f16 v[158:161], v[166:169], v[198:201], v[158:161]
	v_mfma_f32_16x16x32_f16 v[54:57], v[166:169], v[206:209], v[54:57]
	s_waitcnt vmcnt(12)
	v_mfma_f32_16x16x32_f16 v[166:169], v[178:181], v[84:87], v[66:69]
	v_mfma_f32_16x16x32_f16 v[170:173], v[178:181], v[170:173], v[70:73]
	v_mfma_f32_16x16x32_f16 v[174:177], v[178:181], v[174:177], v[74:77]
	v_mfma_f32_16x16x32_f16 v[186:189], v[178:181], v[186:189], v[34:37]
	v_mfma_f32_16x16x32_f16 v[190:193], v[178:181], v[190:193], v[42:45]
	v_mfma_f32_16x16x32_f16 v[194:197], v[178:181], v[194:197], v[46:49]
	v_mfma_f32_16x16x32_f16 v[198:201], v[178:181], v[198:201], v[62:65]
	v_mfma_f32_16x16x32_f16 v[178:181], v[178:181], v[206:209], v[58:61]
	s_nop 0
	global_load_dwordx4 v[46:49], v[116:117], off offset:1024
	global_load_dwordx4 v[42:45], v[116:117], off offset:2048
	global_load_dwordx4 v[34:37], v[116:117], off offset:3072
	v_bitop3_b32 v58, v140, v145, 28 bitop3:0x36
	v_lshl_or_b32 v140, v58, 4, v220
	ds_read_b128 v[58:61], v140
	ds_read_b128 v[62:65], v140 offset:8192
	ds_read_b128 v[206:209], v140 offset:16384
	ds_read_b128 v[214:217], v140 offset:24576
	ds_read_b128 v[218:221], v140 offset:32768
	ds_read_b128 v[222:225], v140 offset:40960
	ds_read_b128 v[226:229], v140 offset:49152
	ds_read_b128 v[230:233], v140 offset:57344
	s_waitcnt vmcnt(14) lgkmcnt(7)
	v_mfma_f32_16x16x32_f16 v[234:237], v[78:81], v[58:61], v[96:99]
	s_waitcnt lgkmcnt(6)
	v_mfma_f32_16x16x32_f16 v[238:241], v[78:81], v[62:65], v[100:103]
	s_waitcnt lgkmcnt(5)
	v_mfma_f32_16x16x32_f16 v[242:245], v[78:81], v[206:209], v[104:107]
	s_waitcnt lgkmcnt(4)
	v_mfma_f32_16x16x32_f16 v[246:249], v[78:81], v[214:217], v[108:111]
	s_waitcnt lgkmcnt(3)
	v_mfma_f32_16x16x32_f16 v[106:109], v[78:81], v[218:221], v[112:115]
	s_waitcnt lgkmcnt(2)
	v_mfma_f32_16x16x32_f16 v[102:105], v[78:81], v[222:225], v[210:213]
	s_waitcnt lgkmcnt(1)
	v_mfma_f32_16x16x32_f16 v[94:97], v[78:81], v[226:229], v[124:127]
	s_waitcnt lgkmcnt(0)
	v_mfma_f32_16x16x32_f16 v[86:89], v[78:81], v[230:233], v[50:53]
	s_waitcnt vmcnt(13)
	v_mfma_f32_16x16x32_f16 v[124:127], v[162:165], v[58:61], v[90:93]
	v_mfma_f32_16x16x32_f16 v[202:205], v[162:165], v[62:65], v[202:205]
	v_mfma_f32_16x16x32_f16 v[210:213], v[162:165], v[206:209], v[128:131]
	v_mfma_f32_16x16x32_f16 v[146:149], v[162:165], v[214:217], v[146:149]
	v_mfma_f32_16x16x32_f16 v[78:81], v[162:165], v[218:221], v[150:153]
	v_mfma_f32_16x16x32_f16 v[74:77], v[162:165], v[222:225], v[154:157]
	v_mfma_f32_16x16x32_f16 v[70:73], v[162:165], v[226:229], v[158:161]
	v_mfma_f32_16x16x32_f16 v[66:69], v[162:165], v[230:233], v[54:57]
	s_waitcnt vmcnt(12)
	v_mfma_f32_16x16x32_f16 v[150:153], v[182:185], v[58:61], v[166:169]
	v_mfma_f32_16x16x32_f16 v[154:157], v[182:185], v[62:65], v[170:173]
	v_mfma_f32_16x16x32_f16 v[114:117], v[182:185], v[206:209], v[174:177]
	v_mfma_f32_16x16x32_f16 v[110:113], v[182:185], v[214:217], v[186:189]
	v_mfma_f32_16x16x32_f16 v[62:65], v[182:185], v[218:221], v[190:193]
	v_mfma_f32_16x16x32_f16 v[58:61], v[182:185], v[222:225], v[194:197]
	v_mfma_f32_16x16x32_f16 v[54:57], v[182:185], v[226:229], v[198:201]
	v_mfma_f32_16x16x32_f16 v[50:53], v[182:185], v[230:233], v[178:181]
	v_lshl_add_u64 v[120:121], v[82:83], 2, s[4:5]
	global_load_dwordx4 v[98:101], v[120:121], off
	global_load_dwordx4 v[90:93], v[120:121], off offset:64
	global_load_dwordx4 v[82:85], v[120:121], off offset:128
	s_movk_i32 s5, 0x310
	v_mad_u32_u24 v130, v145, s5, v250
	v_mov_b32_e32 v158, v239
	v_mov_b32_e32 v159, v240
	v_mov_b32_e32 v160, v243
	v_mov_b32_e32 v161, v244
	v_mov_b32_e32 v162, v247
	v_mov_b32_e32 v163, v248
	v_mov_b32_e32 v164, v203
	v_mov_b32_e32 v165, v204
	v_mov_b32_e32 v169, v148
	v_mov_b32_e32 v166, v211
	v_mov_b32_e32 v167, v212
	v_mov_b32_e32 v168, v147
	s_barrier
	v_add_u32_e32 v132, 0x3000, v130
	v_add_u32_e32 v131, 0x6000, v130
	s_mov_b32 s4, 0xfffffd0
	v_mul_lo_u32 v176, v143, s4
	s_waitcnt vmcnt(2)
	v_pk_add_f32 v[170:171], v[234:235], v[98:99]
	v_pk_add_f32 v[172:173], v[236:237], v[100:101]
	v_add_f32_e32 v145, v238, v98
	v_pk_mov_b32 v[128:129], v[98:99], v[100:101] op_sel:[1,0]
	v_add_f32_e32 v99, v241, v101
	s_waitcnt vmcnt(1)
	v_pk_add_f32 v[124:125], v[124:125], v[90:91]
	v_pk_add_f32 v[174:175], v[126:127], v[92:93]
	v_add_f32_e32 v180, v202, v90
	v_pk_mov_b32 v[126:127], v[90:91], v[92:93] op_sel:[1,0]
	v_add_f32_e32 v91, v205, v93
	v_add_f32_e32 v100, v242, v98
	v_add_f32_e32 v177, v245, v101
	v_add_f32_e32 v92, v210, v90
	v_add_f32_e32 v181, v213, v93
	v_add_f32_e32 v183, v149, v93
	v_cvt_pk_f16_f32 v149, v172, v173
	v_cvt_f16_f32_e32 v145, v145
	v_cvt_f16_f32_e32 v99, v99
	v_cvt_f16_f32_e32 v173, v180
	v_cvt_f16_f32_e32 v91, v91
	v_cvt_pk_f16_f32 v148, v170, v171
	v_cvt_f16_f32_e32 v100, v100
	v_cvt_f16_f32_e32 v170, v177
	v_cvt_pk_f16_f32 v124, v124, v125
	v_cvt_pk_f16_f32 v125, v174, v175
	v_cvt_f16_f32_e32 v92, v92
	v_cvt_f16_f32_e32 v174, v181
	v_add_f32_e32 v182, v146, v90
	s_waitcnt vmcnt(0)
	v_pk_add_f32 v[146:147], v[150:151], v[82:83]
	v_pk_add_f32 v[150:151], v[158:159], v[128:129]
	v_pk_add_f32 v[158:159], v[160:161], v[128:129]
	v_pk_add_f32 v[160:161], v[162:163], v[128:129]
	v_pk_add_f32 v[162:163], v[164:165], v[126:127]
	v_pk_add_f32 v[164:165], v[166:167], v[126:127]
	v_cvt_pk_f16_f32 v146, v146, v147
	v_cvt_pk_f16_f32 v147, v150, v151
	v_cvt_pk_f16_f32 v150, v158, v159
	v_cvt_pk_f16_f32 v159, v162, v163
	v_cvt_pk_f16_f32 v151, v160, v161
	v_cvt_pk_f16_f32 v161, v164, v165
	ds_write2_b64 v130, v[148:149], v[124:125] offset1:4
	v_pack_b32_f16 v124, v145, v147
	v_alignbit_b32 v125, v99, v147, 16
	v_pack_b32_f16 v158, v173, v159
	v_alignbit_b32 v159, v91, v159, 16
	v_pack_b32_f16 v148, v100, v150
	v_alignbit_b32 v149, v170, v150, 16
	v_pack_b32_f16 v160, v92, v161
	v_alignbit_b32 v161, v174, v161, 16
	ds_write2_b64 v132, v[124:125], v[158:159] offset0:32 offset1:36
	ds_write2_b64 v131, v[148:149], v[160:161] offset0:64 offset1:68
	v_pk_add_f32 v[124:125], v[152:153], v[84:85]
	v_add_f32_e32 v92, v154, v82
	v_cvt_pk_f16_f32 v147, v124, v125
	v_pk_mov_b32 v[124:125], v[82:83], v[84:85] op_sel:[1,0]
	v_add_f32_e32 v83, v157, v85
	v_cvt_f16_f32_e32 v92, v92
	v_cvt_f16_f32_e32 v83, v83
	ds_write_b64 v130, v[146:147] offset:64
	v_mov_b32_e32 v146, v155
	v_mov_b32_e32 v147, v156
	v_pk_add_f32 v[146:147], v[146:147], v[124:125]
	v_add_f32_e32 v178, v246, v98
	v_cvt_pk_f16_f32 v84, v146, v147
	v_pack_b32_f16 v146, v92, v84
	v_alignbit_b32 v147, v83, v84, 16
	v_add_f32_e32 v83, v114, v82
	v_add_f32_e32 v84, v117, v85
	v_cvt_f16_f32_e32 v83, v83
	v_cvt_f16_f32_e32 v84, v84
	v_mov_b32_e32 v114, v115
	v_mov_b32_e32 v115, v116
	v_pk_add_f32 v[114:115], v[114:115], v[124:125]
	v_add_f32_e32 v179, v249, v101
	v_cvt_pk_f16_f32 v92, v114, v115
	v_pack_b32_f16 v114, v83, v92
	v_alignbit_b32 v115, v84, v92, 16
	v_add_f32_e32 v83, v110, v82
	v_add_f32_e32 v84, v113, v85
	v_cvt_f16_f32_e32 v83, v83
	v_cvt_f16_f32_e32 v84, v84
	v_mov_b32_e32 v110, v111
	v_mov_b32_e32 v111, v112
	v_cvt_f16_f32_e32 v171, v178
	v_cvt_f16_f32_e32 v172, v179
	v_cvt_f16_f32_e32 v175, v182
	v_pk_add_f32 v[166:167], v[168:169], v[126:127]
	v_cvt_f16_f32_e32 v168, v183
	v_pk_add_f32 v[110:111], v[110:111], v[124:125]
	v_cvt_pk_f16_f32 v163, v166, v167
	v_cvt_pk_f16_f32 v92, v110, v111
	v_pack_b32_f16 v110, v83, v92
	v_alignbit_b32 v111, v84, v92, 16
	v_or_b32_e32 v83, s16, v143
	ds_write_b64 v130, v[110:111] offset:37696
	v_add_lshl_u32 v111, v176, v0, 4
	v_mul_lo_u32 v112, v83, s6
	v_mul_u32_u24_e32 v83, 0x310, v143
	v_mul_u32_u24_e32 v84, 0x556, v141
	v_pack_b32_f16 v150, v171, v151
	v_alignbit_b32 v151, v172, v151, 16
	v_pack_b32_f16 v162, v175, v163
	v_alignbit_b32 v163, v168, v163, 16
	v_add_u32_e32 v91, 0x9000, v130
	v_add3_u32 v83, v111, v83, s14
	v_lshrrev_b32_e32 v154, 16, v84
	ds_write2_b64 v91, v[150:151], v[162:163] offset0:96 offset1:100
	ds_write_b64 v130, v[146:147] offset:12608
	ds_write_b64 v130, v[114:115] offset:25152
	s_waitcnt lgkmcnt(0)
	s_barrier
	ds_read_b128 v[114:117], v83
	v_mul_lo_u32 v84, v154, s4
	v_add_lshl_u32 v113, v84, v141, 4
	v_mul_u32_u24_e32 v84, 0x310, v154
	v_add3_u32 v84, v113, v84, s14
	ds_read_b128 v[146:149], v84
	v_add_u32_e32 v92, v111, v112
	s_waitcnt lgkmcnt(1)
	buffer_store_dwordx4 v[114:117], v92, s[0:3], 0 offen sc1
	v_or_b32_e32 v92, s16, v154
	s_nop 0
	v_mul_lo_u32 v114, v92, s6
	v_add_u32_e32 v92, v113, v114
	s_waitcnt lgkmcnt(0)
	buffer_store_dwordx4 v[146:149], v92, s[0:3], 0 offen sc1
	v_or_b32_e32 v92, 0x400, v0
	v_mul_u32_u24_e32 v99, 0x556, v92
	v_lshrrev_b32_e32 v155, 16, v99
	v_mul_lo_u32 v99, v155, s4
	v_add_lshl_u32 v115, v99, v92, 4
	v_mul_u32_u24_e32 v92, 0x310, v155
	v_mul_u32_u24_e32 v99, 0x556, v142
	v_add3_u32 v92, v115, v92, s14
	v_lshrrev_b32_e32 v156, 16, v99
	ds_read_b128 v[146:149], v92
	v_mul_lo_u32 v99, v156, s4
	v_add_lshl_u32 v117, v99, v142, 4
	v_mul_u32_u24_e32 v99, 0x310, v156
	v_or_b32_e32 v100, s16, v155
	v_add3_u32 v99, v117, v99, s14
	v_mul_lo_u32 v116, v100, s6
	ds_read_b128 v[150:153], v99
	v_add_u32_e32 v100, v115, v116
	s_waitcnt lgkmcnt(1)
	buffer_store_dwordx4 v[146:149], v100, s[0:3], 0 offen sc1
	v_or_b32_e32 v100, s16, v156
	v_mul_lo_u32 v142, v100, s6
	v_add_u32_e32 v100, v117, v142
	v_or_b32_e32 v0, 0x800, v0
	s_waitcnt lgkmcnt(0)
	buffer_store_dwordx4 v[150:153], v100, s[0:3], 0 offen sc1
	v_mul_u32_u24_e32 v100, 0xaab, v0
	v_lshrrev_b32_e32 v157, 17, v100
	v_mul_lo_u32 v100, v157, s4
	v_or_b32_e32 v110, s16, v157
	v_add_lshl_u32 v143, v100, v0, 4
	v_mul_lo_u32 v141, v110, s6
	v_mul_u32_u24_e32 v100, 0x310, v157
	v_mul_u32_u24_e32 v110, 0xaab, v144
	v_add3_u32 v100, v100, v143, s14
	v_lshrrev_b32_e32 v158, 17, v110
	ds_read_b128 v[146:149], v100
	v_mul_lo_u32 v110, v158, s4
	v_add_lshl_u32 v144, v110, v144, 4
	v_mul_u32_u24_e32 v110, 0x310, v158
	v_add3_u32 v110, v110, v144, s14
	ds_read_b128 v[150:153], v110
	v_add_u32_e32 v0, v143, v141
	s_waitcnt lgkmcnt(1)
	buffer_store_dwordx4 v[146:149], v0, s[0:3], 0 offen sc1
	v_or_b32_e32 v0, s16, v158
	v_mul_lo_u32 v145, v0, s6
	v_add_u32_e32 v0, v144, v145
	s_waitcnt lgkmcnt(0)
	buffer_store_dwordx4 v[150:153], v0, s[0:3], 0 offen sc1
	v_add_f32_e32 v0, v106, v98
	v_cvt_f16_f32_e32 v0, v0
	v_mov_b32_e32 v106, v107
	v_mov_b32_e32 v107, v108
	v_pk_add_f32 v[106:107], v[106:107], v[128:129]
	v_add_f32_e32 v108, v109, v101
	v_cvt_pk_f16_f32 v107, v106, v107
	v_pack_b32_f16 v106, v0, v107
	v_add_f32_e32 v0, v102, v98
	v_cvt_f16_f32_e32 v0, v0
	v_mov_b32_e32 v102, v103
	v_mov_b32_e32 v103, v104
	v_pk_add_f32 v[102:103], v[102:103], v[128:129]
	v_add_f32_e32 v104, v105, v101
	v_cvt_pk_f16_f32 v103, v102, v103
	v_pack_b32_f16 v102, v0, v103
	v_add_f32_e32 v0, v94, v98
	v_cvt_f16_f32_e32 v0, v0
	v_mov_b32_e32 v94, v95
	v_mov_b32_e32 v95, v96
	v_pk_add_f32 v[94:95], v[94:95], v[128:129]
	v_add_f32_e32 v96, v97, v101
	v_cvt_pk_f16_f32 v95, v94, v95
	v_pack_b32_f16 v94, v0, v95
	v_add_f32_e32 v0, v86, v98
	v_cvt_f16_f32_e32 v0, v0
	v_mov_b32_e32 v86, v87
	v_mov_b32_e32 v87, v88
	v_pk_add_f32 v[86:87], v[86:87], v[128:129]
	v_add_f32_e32 v88, v89, v101
	v_cvt_pk_f16_f32 v87, v86, v87
	v_pack_b32_f16 v86, v0, v87
	v_add_f32_e32 v0, v78, v90
	v_cvt_f16_f32_e32 v0, v0
	v_mov_b32_e32 v78, v79
	v_mov_b32_e32 v79, v80
	v_pk_add_f32 v[78:79], v[78:79], v[126:127]
	v_add_f32_e32 v80, v81, v93
	v_cvt_pk_f16_f32 v79, v78, v79
	v_pack_b32_f16 v78, v0, v79
	v_add_f32_e32 v0, v74, v90
	v_cvt_f16_f32_e32 v0, v0
	v_mov_b32_e32 v74, v75
	v_mov_b32_e32 v75, v76
	v_pk_add_f32 v[74:75], v[74:75], v[126:127]
	v_add_f32_e32 v76, v77, v93
	v_cvt_pk_f16_f32 v75, v74, v75
	v_pack_b32_f16 v74, v0, v75
	v_add_f32_e32 v0, v70, v90
	v_cvt_f16_f32_e32 v0, v0
	v_mov_b32_e32 v70, v71
	v_mov_b32_e32 v71, v72
	v_pk_add_f32 v[70:71], v[70:71], v[126:127]
	v_add_f32_e32 v72, v73, v93
	v_cvt_pk_f16_f32 v71, v70, v71
	v_pack_b32_f16 v70, v0, v71
	v_add_f32_e32 v0, v66, v90
	v_cvt_f16_f32_e32 v0, v0
	v_mov_b32_e32 v66, v67
	v_mov_b32_e32 v67, v68
	v_pk_add_f32 v[66:67], v[66:67], v[126:127]
	v_add_f32_e32 v68, v69, v93
	v_cvt_pk_f16_f32 v67, v66, v67
	v_pack_b32_f16 v66, v0, v67
	v_add_f32_e32 v0, v62, v82
	v_cvt_f16_f32_e32 v0, v0
	v_mov_b32_e32 v62, v63
	v_mov_b32_e32 v63, v64
	v_pk_add_f32 v[62:63], v[62:63], v[124:125]
	v_add_f32_e32 v64, v65, v85
	v_cvt_pk_f16_f32 v63, v62, v63
	v_pack_b32_f16 v62, v0, v63
	v_add_f32_e32 v0, v58, v82
	v_cvt_f16_f32_e32 v0, v0
	v_mov_b32_e32 v58, v59
	v_mov_b32_e32 v59, v60
	v_pk_add_f32 v[58:59], v[58:59], v[124:125]
	v_add_f32_e32 v60, v61, v85
	v_cvt_pk_f16_f32 v59, v58, v59
	v_pack_b32_f16 v58, v0, v59
	v_add_f32_e32 v0, v54, v82
	v_cvt_f16_f32_e32 v0, v0
	v_mov_b32_e32 v54, v55
	v_mov_b32_e32 v55, v56
	v_pk_add_f32 v[54:55], v[54:55], v[124:125]
	v_add_f32_e32 v56, v57, v85
	v_cvt_pk_f16_f32 v55, v54, v55
	v_pack_b32_f16 v54, v0, v55
	v_add_f32_e32 v0, v50, v82
	v_mov_b32_e32 v50, v51
	v_mov_b32_e32 v51, v52
	v_add_f32_e32 v52, v53, v85
	v_cvt_f16_f32_e32 v108, v108
	v_cvt_f16_f32_e32 v104, v104
	v_cvt_f16_f32_e32 v96, v96
	v_cvt_f16_f32_e32 v88, v88
	v_cvt_f16_f32_e32 v80, v80
	v_cvt_f16_f32_e32 v76, v76
	v_cvt_f16_f32_e32 v72, v72
	v_cvt_f16_f32_e32 v68, v68
	v_cvt_f16_f32_e32 v64, v64
	v_cvt_f16_f32_e32 v60, v60
	v_cvt_f16_f32_e32 v56, v56
	v_cvt_f16_f32_e32 v0, v0
	v_cvt_f16_f32_e32 v52, v52
	v_pk_add_f32 v[50:51], v[50:51], v[124:125]
	v_alignbit_b32 v107, v108, v107, 16
	v_cvt_pk_f16_f32 v51, v50, v51
	v_alignbit_b32 v103, v104, v103, 16
	v_alignbit_b32 v95, v96, v95, 16
	v_alignbit_b32 v87, v88, v87, 16
	v_alignbit_b32 v79, v80, v79, 16
	v_alignbit_b32 v75, v76, v75, 16
	v_alignbit_b32 v71, v72, v71, 16
	v_alignbit_b32 v67, v68, v67, 16
	v_alignbit_b32 v63, v64, v63, 16
	v_alignbit_b32 v59, v60, v59, 16
	v_alignbit_b32 v55, v56, v55, 16
	v_pack_b32_f16 v50, v0, v51
	v_alignbit_b32 v51, v52, v51, 16
	s_barrier
	ds_write2_b64 v130, v[106:107], v[78:79] offset1:4
	ds_write2_b64 v132, v[102:103], v[74:75] offset0:32 offset1:36
	ds_write2_b64 v131, v[94:95], v[70:71] offset0:64 offset1:68
	ds_write2_b64 v91, v[86:87], v[66:67] offset0:96 offset1:100
	ds_write_b64 v130, v[62:63] offset:64
	ds_write_b64 v130, v[58:59] offset:12608
	ds_write_b64 v130, v[54:55] offset:25152
	ds_write_b64 v130, v[50:51] offset:37696
	s_waitcnt lgkmcnt(0)
	s_barrier
	s_cmp_lt_u32 s94, 4
	s_cbranch_scc1 .Lmystag1_6
	s_sleep 7
.Lmystag1_6:
	global_load_dwordx4 v[50:53], v[122:123], off
	global_load_dwordx4 v[54:57], v[122:123], off offset:1024
	global_load_dwordx4 v[58:61], v[122:123], off offset:2048
	ds_read_b128 v[62:65], v83
	ds_read_b128 v[70:73], v84
	v_mul_lo_u32 v68, v139, s6
	v_add_u32_e32 v0, v68, v111
	ds_read_b128 v[74:77], v99
	s_waitcnt lgkmcnt(2)
	buffer_store_dwordx4 v[62:65], v0, s[0:3], 0 offen sc1
	v_or_b32_e32 v0, s7, v154
	v_mul_lo_u32 v69, v0, s6
	ds_read_b128 v[62:65], v92
	v_add_u32_e32 v0, v113, v69
	s_waitcnt lgkmcnt(2)
	buffer_store_dwordx4 v[70:73], v0, s[0:3], 0 offen sc1
	v_or_b32_e32 v0, s7, v155
	s_nop 0
	v_mul_lo_u32 v72, v0, s6
	v_add_u32_e32 v0, v115, v72
	s_waitcnt lgkmcnt(0)
	buffer_store_dwordx4 v[62:65], v0, s[0:3], 0 offen sc1
	v_or_b32_e32 v0, s7, v156
	v_mul_lo_u32 v70, v0, s6
	ds_read_b128 v[62:65], v100
	v_add_u32_e32 v0, v117, v70
	buffer_store_dwordx4 v[74:77], v0, s[0:3], 0 offen sc1
	v_or_b32_e32 v0, s7, v157
	v_mul_lo_u32 v71, v0, s6
	v_add_u32_e32 v0, v143, v71
	ds_read_b128 v[74:77], v110
	s_waitcnt lgkmcnt(1)
	buffer_store_dwordx4 v[62:65], v0, s[0:3], 0 offen sc1
	ds_read_b128 v[62:65], v134
	ds_read_b128 v[78:81], v134 offset:8192
	ds_read_b128 v[86:89], v134 offset:16384
	ds_read_b128 v[94:97], v134 offset:24576
	ds_read_b128 v[102:105], v134 offset:32768
	ds_read_b128 v[106:109], v134 offset:40960
	ds_read_b128 v[124:127], v134 offset:49152
	ds_read_b128 v[146:149], v134 offset:57344
	v_or_b32_e32 v0, s7, v158
	v_mul_lo_u32 v73, v0, s6
	v_add_u32_e32 v0, v144, v73
	s_waitcnt lgkmcnt(8)
	buffer_store_dwordx4 v[74:77], v0, s[0:3], 0 offen sc1
	s_waitcnt lgkmcnt(7)
	s_nop 0
	v_mfma_f32_16x16x32_f16 v[74:77], v[38:41], v[62:65], 0
	s_waitcnt lgkmcnt(6)
	v_mfma_f32_16x16x32_f16 v[150:153], v[38:41], v[78:81], 0
	s_waitcnt lgkmcnt(5)
	v_mfma_f32_16x16x32_f16 v[154:157], v[38:41], v[86:89], 0
	s_waitcnt lgkmcnt(4)
	v_mfma_f32_16x16x32_f16 v[158:161], v[38:41], v[94:97], 0
	s_waitcnt lgkmcnt(3)
	v_mfma_f32_16x16x32_f16 v[162:165], v[38:41], v[102:105], 0
	s_waitcnt lgkmcnt(2)
	v_mfma_f32_16x16x32_f16 v[166:169], v[38:41], v[106:109], 0
	s_waitcnt lgkmcnt(1)
	v_mfma_f32_16x16x32_f16 v[170:173], v[38:41], v[124:127], 0
	s_waitcnt lgkmcnt(0)
	v_mfma_f32_16x16x32_f16 v[38:41], v[38:41], v[146:149], 0
	v_mfma_f32_16x16x32_f16 v[174:177], v[26:29], v[62:65], 0
	v_mfma_f32_16x16x32_f16 v[178:181], v[26:29], v[78:81], 0
	v_mfma_f32_16x16x32_f16 v[182:185], v[26:29], v[86:89], 0
	v_mfma_f32_16x16x32_f16 v[186:189], v[26:29], v[94:97], 0
	v_mfma_f32_16x16x32_f16 v[190:193], v[26:29], v[102:105], 0
	v_mfma_f32_16x16x32_f16 v[194:197], v[26:29], v[106:109], 0
	v_mfma_f32_16x16x32_f16 v[198:201], v[26:29], v[124:127], 0
	v_mfma_f32_16x16x32_f16 v[26:29], v[26:29], v[146:149], 0
	v_mfma_f32_16x16x32_f16 v[62:65], v[10:13], v[62:65], 0
	v_mfma_f32_16x16x32_f16 v[78:81], v[10:13], v[78:81], 0
	v_mfma_f32_16x16x32_f16 v[86:89], v[10:13], v[86:89], 0
	v_mfma_f32_16x16x32_f16 v[94:97], v[10:13], v[94:97], 0
	v_mfma_f32_16x16x32_f16 v[102:105], v[10:13], v[102:105], 0
	v_mfma_f32_16x16x32_f16 v[106:109], v[10:13], v[106:109], 0
	v_mfma_f32_16x16x32_f16 v[124:127], v[10:13], v[124:127], 0
	v_mfma_f32_16x16x32_f16 v[10:13], v[10:13], v[146:149], 0
	s_mov_b32 s4, 0x34000
	v_add_co_u32_e32 v66, vcc, s4, v118
	s_mov_b32 s4, 0x35000
	s_nop 0
	v_addc_co_u32_e32 v67, vcc, 0, v119, vcc
	v_add_co_u32_e32 v118, vcc, s4, v118
	s_nop 1
	v_addc_co_u32_e32 v119, vcc, 0, v119, vcc
	global_load_dwordx4 v[146:149], v[118:119], off offset:-4096
	global_load_dwordx4 v[202:205], v[122:123], off offset:3072
	global_load_dwordx4 v[206:209], v[66:67], off offset:1024
	ds_read_b128 v[210:213], v1
	ds_read_b128 v[214:217], v1 offset:8192
	ds_read_b128 v[218:221], v1 offset:16384
	ds_read_b128 v[222:225], v1 offset:24576
	ds_read_b128 v[226:229], v1 offset:32768
	ds_read_b128 v[230:233], v1 offset:40960
	ds_read_b128 v[234:237], v1 offset:49152
	ds_read_b128 v[238:241], v1 offset:57344
	s_waitcnt lgkmcnt(7)
	v_mfma_f32_16x16x32_f16 v[74:77], v[22:25], v[210:213], v[74:77]
	s_waitcnt lgkmcnt(6)
	v_mfma_f32_16x16x32_f16 v[150:153], v[22:25], v[214:217], v[150:153]
	s_waitcnt lgkmcnt(5)
	v_mfma_f32_16x16x32_f16 v[154:157], v[22:25], v[218:221], v[154:157]
	s_waitcnt lgkmcnt(4)
	v_mfma_f32_16x16x32_f16 v[158:161], v[22:25], v[222:225], v[158:161]
	s_waitcnt lgkmcnt(3)
	v_mfma_f32_16x16x32_f16 v[162:165], v[22:25], v[226:229], v[162:165]
	s_waitcnt lgkmcnt(2)
	v_mfma_f32_16x16x32_f16 v[166:169], v[22:25], v[230:233], v[166:169]
	s_waitcnt lgkmcnt(1)
	v_mfma_f32_16x16x32_f16 v[170:173], v[22:25], v[234:237], v[170:173]
	s_waitcnt lgkmcnt(0)
	v_mfma_f32_16x16x32_f16 v[22:25], v[22:25], v[238:241], v[38:41]
	v_mfma_f32_16x16x32_f16 v[38:41], v[6:9], v[210:213], v[174:177]
	v_mfma_f32_16x16x32_f16 v[174:177], v[6:9], v[214:217], v[178:181]
	v_mfma_f32_16x16x32_f16 v[178:181], v[6:9], v[218:221], v[182:185]
	v_mfma_f32_16x16x32_f16 v[182:185], v[6:9], v[222:225], v[186:189]
	v_mfma_f32_16x16x32_f16 v[186:189], v[6:9], v[226:229], v[190:193]
	v_mfma_f32_16x16x32_f16 v[190:193], v[6:9], v[230:233], v[194:197]
	v_mfma_f32_16x16x32_f16 v[194:197], v[6:9], v[234:237], v[198:201]
	v_mfma_f32_16x16x32_f16 v[6:9], v[6:9], v[238:241], v[26:29]
	v_mfma_f32_16x16x32_f16 v[26:29], v[2:5], v[210:213], v[62:65]
	v_mfma_f32_16x16x32_f16 v[62:65], v[2:5], v[214:217], v[78:81]
	v_mfma_f32_16x16x32_f16 v[78:81], v[2:5], v[218:221], v[86:89]
	v_mfma_f32_16x16x32_f16 v[86:89], v[2:5], v[222:225], v[94:97]
	v_mfma_f32_16x16x32_f16 v[94:97], v[2:5], v[226:229], v[102:105]
	v_mfma_f32_16x16x32_f16 v[102:105], v[2:5], v[230:233], v[106:109]
	v_mfma_f32_16x16x32_f16 v[106:109], v[2:5], v[234:237], v[124:127]
	v_mfma_f32_16x16x32_f16 v[0:3], v[2:5], v[238:241], v[10:13]
	s_nop 2
	global_load_dwordx4 v[10:13], v[66:67], off offset:2048
	global_load_dwordx4 v[122:125], v[66:67], off offset:3072
	global_load_dwordx4 v[126:129], v[118:119], off
	ds_read_b128 v[198:201], v133
	ds_read_b128 v[210:213], v133 offset:8192
	ds_read_b128 v[214:217], v133 offset:16384
	ds_read_b128 v[218:221], v133 offset:24576
	ds_read_b128 v[222:225], v133 offset:32768
	ds_read_b128 v[226:229], v133 offset:40960
	ds_read_b128 v[230:233], v133 offset:49152
	ds_read_b128 v[234:237], v133 offset:57344
	s_waitcnt lgkmcnt(7)
	v_mfma_f32_16x16x32_f16 v[74:77], v[30:33], v[198:201], v[74:77]
	s_waitcnt lgkmcnt(6)
	v_mfma_f32_16x16x32_f16 v[150:153], v[30:33], v[210:213], v[150:153]
	s_waitcnt lgkmcnt(5)
	v_mfma_f32_16x16x32_f16 v[154:157], v[30:33], v[214:217], v[154:157]
	s_waitcnt lgkmcnt(4)
	v_mfma_f32_16x16x32_f16 v[158:161], v[30:33], v[218:221], v[158:161]
	s_waitcnt lgkmcnt(3)
	v_mfma_f32_16x16x32_f16 v[162:165], v[30:33], v[222:225], v[162:165]
	s_waitcnt lgkmcnt(2)
	v_mfma_f32_16x16x32_f16 v[166:169], v[30:33], v[226:229], v[166:169]
	s_waitcnt lgkmcnt(1)
	v_mfma_f32_16x16x32_f16 v[170:173], v[30:33], v[230:233], v[170:173]
	s_waitcnt lgkmcnt(0)
	v_mfma_f32_16x16x32_f16 v[22:25], v[30:33], v[234:237], v[22:25]
	v_mfma_f32_16x16x32_f16 v[30:33], v[14:17], v[198:201], v[38:41]
	v_mfma_f32_16x16x32_f16 v[38:41], v[14:17], v[210:213], v[174:177]
	v_mfma_f32_16x16x32_f16 v[174:177], v[14:17], v[214:217], v[178:181]
	v_mfma_f32_16x16x32_f16 v[178:181], v[14:17], v[218:221], v[182:185]
	v_mfma_f32_16x16x32_f16 v[182:185], v[14:17], v[222:225], v[186:189]
	v_mfma_f32_16x16x32_f16 v[186:189], v[14:17], v[226:229], v[190:193]
	v_mfma_f32_16x16x32_f16 v[190:193], v[14:17], v[230:233], v[194:197]
	v_mfma_f32_16x16x32_f16 v[4:7], v[14:17], v[234:237], v[6:9]
	v_mfma_f32_16x16x32_f16 v[14:17], v[18:21], v[198:201], v[26:29]
	v_mfma_f32_16x16x32_f16 v[26:29], v[18:21], v[210:213], v[62:65]
	v_mfma_f32_16x16x32_f16 v[62:65], v[18:21], v[214:217], v[78:81]
	v_mfma_f32_16x16x32_f16 v[78:81], v[18:21], v[218:221], v[86:89]
	v_mfma_f32_16x16x32_f16 v[86:89], v[18:21], v[222:225], v[94:97]
	v_mfma_f32_16x16x32_f16 v[94:97], v[18:21], v[226:229], v[102:105]
	v_mfma_f32_16x16x32_f16 v[102:105], v[18:21], v[230:233], v[106:109]
	v_mfma_f32_16x16x32_f16 v[0:3], v[18:21], v[234:237], v[0:3]
	global_load_dwordx4 v[18:21], v[118:119], off offset:1024
	s_nop 0
	global_load_dwordx4 v[106:109], v[118:119], off offset:2048
	global_load_dwordx4 v[194:197], v[118:119], off offset:3072
	ds_read_b128 v[198:201], v135
	ds_read_b128 v[210:213], v135 offset:8192
	ds_read_b128 v[214:217], v135 offset:16384
	ds_read_b128 v[218:221], v135 offset:24576
	ds_read_b128 v[222:225], v135 offset:32768
	ds_read_b128 v[226:229], v135 offset:40960
	ds_read_b128 v[230:233], v135 offset:49152
	ds_read_b128 v[234:237], v135 offset:57344
	s_waitcnt lgkmcnt(7)
	v_mfma_f32_16x16x32_f16 v[74:77], v[46:49], v[198:201], v[74:77]
	s_waitcnt lgkmcnt(6)
	v_mfma_f32_16x16x32_f16 v[150:153], v[46:49], v[210:213], v[150:153]
	s_waitcnt lgkmcnt(5)
	v_mfma_f32_16x16x32_f16 v[154:157], v[46:49], v[214:217], v[154:157]
	s_waitcnt lgkmcnt(4)
	v_mfma_f32_16x16x32_f16 v[158:161], v[46:49], v[218:221], v[158:161]
	s_waitcnt lgkmcnt(3)
	v_mfma_f32_16x16x32_f16 v[162:165], v[46:49], v[222:225], v[162:165]
	s_waitcnt lgkmcnt(2)
	v_mfma_f32_16x16x32_f16 v[166:169], v[46:49], v[226:229], v[166:169]
	s_waitcnt lgkmcnt(1)
	v_mfma_f32_16x16x32_f16 v[170:173], v[46:49], v[230:233], v[170:173]
	s_waitcnt lgkmcnt(0)
	v_mfma_f32_16x16x32_f16 v[22:25], v[46:49], v[234:237], v[22:25]
	v_mfma_f32_16x16x32_f16 v[30:33], v[42:45], v[198:201], v[30:33]
	v_mfma_f32_16x16x32_f16 v[38:41], v[42:45], v[210:213], v[38:41]
	v_mfma_f32_16x16x32_f16 v[46:49], v[42:45], v[214:217], v[174:177]
	v_mfma_f32_16x16x32_f16 v[174:177], v[42:45], v[218:221], v[178:181]
	v_mfma_f32_16x16x32_f16 v[178:181], v[42:45], v[222:225], v[182:185]
	v_mfma_f32_16x16x32_f16 v[182:185], v[42:45], v[226:229], v[186:189]
	v_mfma_f32_16x16x32_f16 v[186:189], v[42:45], v[230:233], v[190:193]
	v_mfma_f32_16x16x32_f16 v[4:7], v[42:45], v[234:237], v[4:7]
	v_mfma_f32_16x16x32_f16 v[14:17], v[34:37], v[198:201], v[14:17]
	v_mfma_f32_16x16x32_f16 v[26:29], v[34:37], v[210:213], v[26:29]
	v_mfma_f32_16x16x32_f16 v[42:45], v[34:37], v[214:217], v[62:65]
	v_mfma_f32_16x16x32_f16 v[62:65], v[34:37], v[218:221], v[78:81]
	v_mfma_f32_16x16x32_f16 v[78:81], v[34:37], v[222:225], v[86:89]
	v_mfma_f32_16x16x32_f16 v[86:89], v[34:37], v[226:229], v[94:97]
	v_mfma_f32_16x16x32_f16 v[94:97], v[34:37], v[230:233], v[102:105]
	v_mfma_f32_16x16x32_f16 v[0:3], v[34:37], v[234:237], v[0:3]
	ds_read_b128 v[34:37], v136
	s_nop 0
	ds_read_b128 v[102:105], v136 offset:8192
	ds_read_b128 v[190:193], v136 offset:16384
	ds_read_b128 v[198:201], v136 offset:24576
	ds_read_b128 v[210:213], v136 offset:32768
	ds_read_b128 v[214:217], v136 offset:40960
	ds_read_b128 v[218:221], v136 offset:49152
	ds_read_b128 v[222:225], v136 offset:57344
	s_waitcnt vmcnt(17) lgkmcnt(7)
	v_mfma_f32_16x16x32_f16 v[74:77], v[50:53], v[34:37], v[74:77]
	s_waitcnt lgkmcnt(6)
	v_mfma_f32_16x16x32_f16 v[150:153], v[50:53], v[102:105], v[150:153]
	s_waitcnt lgkmcnt(5)
	v_mfma_f32_16x16x32_f16 v[154:157], v[50:53], v[190:193], v[154:157]
	s_waitcnt lgkmcnt(4)
	v_mfma_f32_16x16x32_f16 v[158:161], v[50:53], v[198:201], v[158:161]
	s_waitcnt lgkmcnt(3)
	v_mfma_f32_16x16x32_f16 v[162:165], v[50:53], v[210:213], v[162:165]
	s_waitcnt lgkmcnt(2)
	v_mfma_f32_16x16x32_f16 v[166:169], v[50:53], v[214:217], v[166:169]
	s_waitcnt lgkmcnt(1)
	v_mfma_f32_16x16x32_f16 v[170:173], v[50:53], v[218:221], v[170:173]
	s_waitcnt lgkmcnt(0)
	v_mfma_f32_16x16x32_f16 v[22:25], v[50:53], v[222:225], v[22:25]
	s_waitcnt vmcnt(16)
	v_mfma_f32_16x16x32_f16 v[30:33], v[54:57], v[34:37], v[30:33]
	v_mfma_f32_16x16x32_f16 v[38:41], v[54:57], v[102:105], v[38:41]
	v_mfma_f32_16x16x32_f16 v[46:49], v[54:57], v[190:193], v[46:49]
	v_mfma_f32_16x16x32_f16 v[50:53], v[54:57], v[198:201], v[174:177]
	v_mfma_f32_16x16x32_f16 v[174:177], v[54:57], v[210:213], v[178:181]
	v_mfma_f32_16x16x32_f16 v[178:181], v[54:57], v[214:217], v[182:185]
	v_mfma_f32_16x16x32_f16 v[182:185], v[54:57], v[218:221], v[186:189]
	v_mfma_f32_16x16x32_f16 v[4:7], v[54:57], v[222:225], v[4:7]
	s_waitcnt vmcnt(15)
	v_mfma_f32_16x16x32_f16 v[14:17], v[58:61], v[34:37], v[14:17]
	v_mfma_f32_16x16x32_f16 v[26:29], v[58:61], v[102:105], v[26:29]
	v_mfma_f32_16x16x32_f16 v[34:37], v[58:61], v[190:193], v[42:45]
	v_mfma_f32_16x16x32_f16 v[42:45], v[58:61], v[198:201], v[62:65]
	v_mfma_f32_16x16x32_f16 v[54:57], v[58:61], v[210:213], v[78:81]
	v_mfma_f32_16x16x32_f16 v[62:65], v[58:61], v[214:217], v[86:89]
	v_mfma_f32_16x16x32_f16 v[78:81], v[58:61], v[218:221], v[94:97]
	v_mfma_f32_16x16x32_f16 v[0:3], v[58:61], v[222:225], v[0:3]
	ds_read_b128 v[58:61], v137
	ds_read_b128 v[86:89], v137 offset:8192
	ds_read_b128 v[94:97], v137 offset:16384
	ds_read_b128 v[102:105], v137 offset:24576
	ds_read_b128 v[186:189], v137 offset:32768
	ds_read_b128 v[190:193], v137 offset:40960
	ds_read_b128 v[198:201], v137 offset:49152
	ds_read_b128 v[134:137], v137 offset:57344
	s_waitcnt vmcnt(7) lgkmcnt(7)
	v_mfma_f32_16x16x32_f16 v[74:77], v[202:205], v[58:61], v[74:77]
	s_waitcnt lgkmcnt(6)
	v_mfma_f32_16x16x32_f16 v[150:153], v[202:205], v[86:89], v[150:153]
	s_waitcnt lgkmcnt(5)
	v_mfma_f32_16x16x32_f16 v[154:157], v[202:205], v[94:97], v[154:157]
	s_waitcnt lgkmcnt(4)
	v_mfma_f32_16x16x32_f16 v[158:161], v[202:205], v[102:105], v[158:161]
	s_waitcnt lgkmcnt(3)
	v_mfma_f32_16x16x32_f16 v[162:165], v[202:205], v[186:189], v[162:165]
	s_waitcnt lgkmcnt(2)
	v_mfma_f32_16x16x32_f16 v[166:169], v[202:205], v[190:193], v[166:169]
	s_waitcnt lgkmcnt(1)
	v_mfma_f32_16x16x32_f16 v[170:173], v[202:205], v[198:201], v[170:173]
	s_waitcnt lgkmcnt(0)
	v_mfma_f32_16x16x32_f16 v[22:25], v[202:205], v[134:137], v[22:25]
	v_mfma_f32_16x16x32_f16 v[30:33], v[146:149], v[58:61], v[30:33]
	v_mfma_f32_16x16x32_f16 v[38:41], v[146:149], v[86:89], v[38:41]
	v_mfma_f32_16x16x32_f16 v[46:49], v[146:149], v[94:97], v[46:49]
	v_mfma_f32_16x16x32_f16 v[50:53], v[146:149], v[102:105], v[50:53]
	v_mfma_f32_16x16x32_f16 v[174:177], v[146:149], v[186:189], v[174:177]
	v_mfma_f32_16x16x32_f16 v[178:181], v[146:149], v[190:193], v[178:181]
	v_mfma_f32_16x16x32_f16 v[182:185], v[146:149], v[198:201], v[182:185]
	v_mfma_f32_16x16x32_f16 v[4:7], v[146:149], v[134:137], v[4:7]
	s_waitcnt vmcnt(6)
	v_mfma_f32_16x16x32_f16 v[14:17], v[206:209], v[58:61], v[14:17]
	v_mfma_f32_16x16x32_f16 v[26:29], v[206:209], v[86:89], v[26:29]
	v_mfma_f32_16x16x32_f16 v[34:37], v[206:209], v[94:97], v[34:37]
	v_mfma_f32_16x16x32_f16 v[42:45], v[206:209], v[102:105], v[42:45]
	v_mfma_f32_16x16x32_f16 v[54:57], v[206:209], v[186:189], v[54:57]
	v_mfma_f32_16x16x32_f16 v[58:61], v[206:209], v[190:193], v[62:65]
	v_mfma_f32_16x16x32_f16 v[62:65], v[206:209], v[198:201], v[78:81]
	v_mfma_f32_16x16x32_f16 v[0:3], v[206:209], v[134:137], v[0:3]
	s_nop 1
	ds_read_b128 v[78:81], v138
	ds_read_b128 v[86:89], v138 offset:8192
	ds_read_b128 v[94:97], v138 offset:16384
	ds_read_b128 v[102:105], v138 offset:24576
	ds_read_b128 v[134:137], v138 offset:32768
	ds_read_b128 v[146:149], v138 offset:40960
	ds_read_b128 v[186:189], v138 offset:49152
	ds_read_b128 v[190:193], v138 offset:57344
	s_waitcnt vmcnt(5) lgkmcnt(7)
	v_mfma_f32_16x16x32_f16 v[74:77], v[10:13], v[78:81], v[74:77]
	s_waitcnt lgkmcnt(6)
	v_mfma_f32_16x16x32_f16 v[150:153], v[10:13], v[86:89], v[150:153]
	s_waitcnt lgkmcnt(5)
	v_mfma_f32_16x16x32_f16 v[154:157], v[10:13], v[94:97], v[154:157]
	s_waitcnt lgkmcnt(4)
	v_mfma_f32_16x16x32_f16 v[158:161], v[10:13], v[102:105], v[158:161]
	s_waitcnt lgkmcnt(3)
	v_mfma_f32_16x16x32_f16 v[162:165], v[10:13], v[134:137], v[162:165]
	s_waitcnt lgkmcnt(2)
	v_mfma_f32_16x16x32_f16 v[166:169], v[10:13], v[146:149], v[166:169]
	s_waitcnt lgkmcnt(1)
	v_mfma_f32_16x16x32_f16 v[170:173], v[10:13], v[186:189], v[170:173]
	s_waitcnt lgkmcnt(0)
	v_mfma_f32_16x16x32_f16 v[8:11], v[10:13], v[190:193], v[22:25]
	s_waitcnt vmcnt(4)
	v_mfma_f32_16x16x32_f16 v[22:25], v[122:125], v[78:81], v[30:33]
	v_mfma_f32_16x16x32_f16 v[30:33], v[122:125], v[86:89], v[38:41]
	v_mfma_f32_16x16x32_f16 v[198:201], v[122:125], v[94:97], v[46:49]
	v_mfma_f32_16x16x32_f16 v[48:51], v[122:125], v[102:105], v[50:53]
	v_mfma_f32_16x16x32_f16 v[174:177], v[122:125], v[134:137], v[174:177]
	v_mfma_f32_16x16x32_f16 v[178:181], v[122:125], v[146:149], v[178:181]
	v_mfma_f32_16x16x32_f16 v[182:185], v[122:125], v[186:189], v[182:185]
	v_mfma_f32_16x16x32_f16 v[4:7], v[122:125], v[190:193], v[4:7]
	s_waitcnt vmcnt(3)
	v_mfma_f32_16x16x32_f16 v[12:15], v[126:129], v[78:81], v[14:17]
	v_mfma_f32_16x16x32_f16 v[78:81], v[126:129], v[86:89], v[26:29]
	v_mfma_f32_16x16x32_f16 v[86:89], v[126:129], v[94:97], v[34:37]
	v_mfma_f32_16x16x32_f16 v[40:43], v[126:129], v[102:105], v[42:45]
	v_mfma_f32_16x16x32_f16 v[94:97], v[126:129], v[134:137], v[54:57]
	v_mfma_f32_16x16x32_f16 v[102:105], v[126:129], v[146:149], v[58:61]
	v_mfma_f32_16x16x32_f16 v[64:67], v[126:129], v[186:189], v[62:65]
	v_mfma_f32_16x16x32_f16 v[0:3], v[126:129], v[190:193], v[0:3]
	s_nop 1
	ds_read_b128 v[60:63], v140
	ds_read_b128 v[122:125], v140 offset:8192
	ds_read_b128 v[126:129], v140 offset:16384
	ds_read_b128 v[134:137], v140 offset:24576
	ds_read_b128 v[146:149], v140 offset:32768
	ds_read_b128 v[186:189], v140 offset:40960
	ds_read_b128 v[190:193], v140 offset:49152
	ds_read_b128 v[202:205], v140 offset:57344
	s_waitcnt vmcnt(2) lgkmcnt(7)
	v_mfma_f32_16x16x32_f16 v[74:77], v[18:21], v[60:63], v[74:77]
	s_waitcnt lgkmcnt(6)
	v_mfma_f32_16x16x32_f16 v[150:153], v[18:21], v[122:125], v[150:153]
	s_waitcnt lgkmcnt(5)
	v_mfma_f32_16x16x32_f16 v[154:157], v[18:21], v[126:129], v[154:157]
	s_waitcnt lgkmcnt(4)
	v_mfma_f32_16x16x32_f16 v[158:161], v[18:21], v[134:137], v[158:161]
	s_waitcnt lgkmcnt(3)
	v_mfma_f32_16x16x32_f16 v[56:59], v[18:21], v[146:149], v[162:165]
	s_waitcnt lgkmcnt(2)
	v_mfma_f32_16x16x32_f16 v[52:55], v[18:21], v[186:189], v[166:169]
	s_waitcnt lgkmcnt(1)
	v_mfma_f32_16x16x32_f16 v[44:47], v[18:21], v[190:193], v[170:173]
	s_waitcnt lgkmcnt(0)
	v_mfma_f32_16x16x32_f16 v[36:39], v[18:21], v[202:205], v[8:11]
	s_waitcnt vmcnt(1)
	v_mfma_f32_16x16x32_f16 v[162:165], v[106:109], v[60:63], v[22:25]
	v_mfma_f32_16x16x32_f16 v[166:169], v[106:109], v[122:125], v[30:33]
	v_mfma_f32_16x16x32_f16 v[170:173], v[106:109], v[126:129], v[198:201]
	v_mfma_f32_16x16x32_f16 v[198:201], v[106:109], v[134:137], v[48:51]
	v_mfma_f32_16x16x32_f16 v[32:35], v[106:109], v[146:149], v[174:177]
	v_mfma_f32_16x16x32_f16 v[24:27], v[106:109], v[186:189], v[178:181]
	v_mfma_f32_16x16x32_f16 v[20:23], v[106:109], v[190:193], v[182:185]
	v_mfma_f32_16x16x32_f16 v[16:19], v[106:109], v[202:205], v[4:7]
	s_waitcnt vmcnt(0)
	v_mfma_f32_16x16x32_f16 v[106:109], v[194:197], v[60:63], v[12:15]
	v_mfma_f32_16x16x32_f16 v[78:81], v[194:197], v[122:125], v[78:81]
	v_mfma_f32_16x16x32_f16 v[86:89], v[194:197], v[126:129], v[86:89]
	v_mfma_f32_16x16x32_f16 v[60:63], v[194:197], v[134:137], v[40:43]
	v_mfma_f32_16x16x32_f16 v[12:15], v[194:197], v[146:149], v[94:97]
	v_mfma_f32_16x16x32_f16 v[8:11], v[194:197], v[186:189], v[102:105]
	v_mfma_f32_16x16x32_f16 v[4:7], v[194:197], v[190:193], v[64:67]
	v_mfma_f32_16x16x32_f16 v[0:3], v[194:197], v[202:205], v[0:3]
	global_load_dwordx4 v[48:51], v[120:121], off offset:1536
	global_load_dwordx4 v[40:43], v[120:121], off offset:1600
	global_load_dwordx4 v[28:31], v[120:121], off offset:1664
	v_mov_b32_e32 v94, v155
	v_mov_b32_e32 v95, v156
	v_mov_b32_e32 v96, v159
	v_mov_b32_e32 v97, v160
	v_mov_b32_e32 v64, v151
	v_mov_b32_e32 v65, v152
	v_mov_b32_e32 v102, v167
	v_mov_b32_e32 v103, v168
	v_mov_b32_e32 v104, v171
	v_mov_b32_e32 v105, v172
	v_mov_b32_e32 v118, v199
	v_mov_b32_e32 v119, v200
	s_barrier
	s_waitcnt vmcnt(2)
	v_pk_add_f32 v[74:75], v[74:75], v[48:49]
	v_add_f32_e32 v82, v150, v48
	v_pk_mov_b32 v[120:121], v[48:49], v[50:51] op_sel:[1,0]
	v_add_f32_e32 v49, v153, v51
	s_waitcnt vmcnt(1)
	v_pk_add_f32 v[122:123], v[162:163], v[40:41]
	v_add_f32_e32 v98, v166, v40
	v_pk_mov_b32 v[66:67], v[40:41], v[42:43] op_sel:[1,0]
	v_add_f32_e32 v41, v169, v43
	v_pk_add_f32 v[76:77], v[76:77], v[50:51]
	v_add_f32_e32 v50, v154, v48
	v_add_f32_e32 v85, v157, v51
	v_add_f32_e32 v90, v158, v48
	v_add_f32_e32 v93, v161, v51
	v_pk_add_f32 v[124:125], v[164:165], v[42:43]
	v_add_f32_e32 v42, v170, v40
	v_add_f32_e32 v101, v173, v43
	v_add_f32_e32 v126, v198, v40
	v_add_f32_e32 v127, v201, v43
	v_cvt_f16_f32_e32 v82, v82
	v_cvt_f16_f32_e32 v49, v49
	v_cvt_f16_f32_e32 v98, v98
	v_cvt_f16_f32_e32 v41, v41
	v_cvt_pk_f16_f32 v74, v74, v75
	v_cvt_pk_f16_f32 v75, v76, v77
	v_cvt_f16_f32_e32 v50, v50
	v_pk_add_f32 v[76:77], v[94:95], v[120:121]
	v_cvt_f16_f32_e32 v85, v85
	v_cvt_f16_f32_e32 v90, v90
	v_pk_add_f32 v[94:95], v[96:97], v[120:121]
	v_cvt_f16_f32_e32 v93, v93
	v_cvt_pk_f16_f32 v96, v122, v123
	v_cvt_f16_f32_e32 v42, v42
	v_cvt_f16_f32_e32 v101, v101
	v_cvt_f16_f32_e32 v122, v126
	v_cvt_f16_f32_e32 v123, v127
	v_pk_add_f32 v[64:65], v[64:65], v[120:121]
	v_pk_add_f32 v[102:103], v[102:103], v[66:67]
	v_pk_add_f32 v[104:105], v[104:105], v[66:67]
	v_pk_add_f32 v[118:119], v[118:119], v[66:67]
	v_cvt_pk_f16_f32 v65, v64, v65
	v_cvt_pk_f16_f32 v76, v76, v77
	v_cvt_pk_f16_f32 v77, v94, v95
	v_cvt_pk_f16_f32 v95, v102, v103
	s_waitcnt vmcnt(0)
	v_pk_add_f32 v[106:107], v[106:107], v[28:29]
	v_pk_add_f32 v[108:109], v[108:109], v[30:31]
	v_cvt_pk_f16_f32 v97, v124, v125
	v_cvt_pk_f16_f32 v102, v104, v105
	v_cvt_pk_f16_f32 v103, v118, v119
	v_pack_b32_f16 v64, v82, v65
	v_alignbit_b32 v65, v49, v65, 16
	v_pack_b32_f16 v94, v98, v95
	v_alignbit_b32 v95, v41, v95, 16
	v_add_f32_e32 v78, v78, v28
	v_cvt_pk_f16_f32 v106, v106, v107
	v_cvt_pk_f16_f32 v107, v108, v109
	ds_write2_b64 v130, v[74:75], v[96:97] offset1:4
	ds_write_b64 v130, v[106:107] offset:64
	v_pack_b32_f16 v74, v50, v76
	v_alignbit_b32 v75, v85, v76, 16
	v_pack_b32_f16 v76, v90, v77
	v_alignbit_b32 v77, v93, v77, 16
	v_pack_b32_f16 v96, v42, v102
	v_alignbit_b32 v97, v101, v102, 16
	v_pack_b32_f16 v102, v122, v103
	v_alignbit_b32 v103, v123, v103, 16
	ds_write2_b64 v132, v[64:65], v[94:95] offset0:32 offset1:36
	ds_write2_b64 v131, v[74:75], v[96:97] offset0:64 offset1:68
	ds_write2_b64 v91, v[76:77], v[102:103] offset0:96 offset1:100
	v_pk_mov_b32 v[64:65], v[28:29], v[30:31] op_sel:[1,0]
	v_add_f32_e32 v29, v81, v31
	v_cvt_f16_f32_e32 v78, v78
	v_cvt_f16_f32_e32 v29, v29
	v_mov_b32_e32 v74, v79
	v_mov_b32_e32 v75, v80
	v_pk_add_f32 v[74:75], v[74:75], v[64:65]
	v_add_f32_e32 v56, v56, v48
	v_cvt_pk_f16_f32 v30, v74, v75
	v_pack_b32_f16 v74, v78, v30
	v_alignbit_b32 v75, v29, v30, 16
	v_add_f32_e32 v29, v86, v28
	v_add_f32_e32 v30, v89, v31
	v_cvt_f16_f32_e32 v29, v29
	v_cvt_f16_f32_e32 v30, v30
	ds_write_b64 v130, v[74:75] offset:12608
	v_mov_b32_e32 v74, v87
	v_mov_b32_e32 v75, v88
	v_pk_add_f32 v[74:75], v[74:75], v[64:65]
	v_add_f32_e32 v52, v52, v48
	v_cvt_pk_f16_f32 v41, v74, v75
	v_pack_b32_f16 v74, v29, v41
	v_alignbit_b32 v75, v30, v41, 16
	v_add_f32_e32 v29, v60, v28
	v_add_f32_e32 v30, v63, v31
	v_cvt_f16_f32_e32 v29, v29
	v_cvt_f16_f32_e32 v30, v30
	v_mov_b32_e32 v60, v61
	v_mov_b32_e32 v61, v62
	v_pk_add_f32 v[60:61], v[60:61], v[64:65]
	ds_write_b64 v130, v[74:75] offset:25152
	v_cvt_pk_f16_f32 v41, v60, v61
	v_pack_b32_f16 v60, v29, v41
	v_alignbit_b32 v61, v30, v41, 16
	ds_write_b64 v130, v[60:61] offset:37696
	s_waitcnt lgkmcnt(0)
	s_barrier
	ds_read_b128 v[60:63], v83
	ds_read_b128 v[74:77], v84
	v_add_u32_e32 v29, 0x300, v111
	v_add_u32_e32 v30, v29, v112
	v_add_f32_e32 v44, v44, v48
	s_waitcnt lgkmcnt(1)
	buffer_store_dwordx4 v[60:63], v30, s[0:3], 0 offen sc1
	v_add_u32_e32 v30, 0x300, v113
	ds_read_b128 v[60:63], v92
	v_add_u32_e32 v41, v30, v114
	s_waitcnt lgkmcnt(1)
	buffer_store_dwordx4 v[74:77], v41, s[0:3], 0 offen sc1
	ds_read_b128 v[74:77], v99
	v_add_u32_e32 v41, 0x300, v115
	v_add_u32_e32 v42, v41, v116
	s_waitcnt lgkmcnt(1)
	buffer_store_dwordx4 v[60:63], v42, s[0:3], 0 offen sc1
	v_add_u32_e32 v42, 0x300, v117
	ds_read_b128 v[60:63], v100
	v_add_u32_e32 v49, v42, v142
	s_waitcnt lgkmcnt(1)
	buffer_store_dwordx4 v[74:77], v49, s[0:3], 0 offen sc1
	ds_read_b128 v[74:77], v110
	v_add_u32_e32 v49, 0x300, v143
	v_add_u32_e32 v50, v49, v141
	s_waitcnt lgkmcnt(1)
	buffer_store_dwordx4 v[60:63], v50, s[0:3], 0 offen sc1
	v_add_u32_e32 v50, 0x300, v144
	v_add_f32_e32 v36, v36, v48
	v_add_u32_e32 v60, v50, v145
	s_waitcnt lgkmcnt(0)
	buffer_store_dwordx4 v[74:77], v60, s[0:3], 0 offen sc1
	v_cvt_f16_f32_e32 v60, v56
	v_mov_b32_e32 v56, v57
	v_mov_b32_e32 v57, v58
	v_add_f32_e32 v58, v59, v51
	v_cvt_f16_f32_e32 v58, v58
	v_pk_add_f32 v[56:57], v[56:57], v[120:121]
	v_add_f32_e32 v32, v32, v40
	v_cvt_pk_f16_f32 v57, v56, v57
	v_pack_b32_f16 v56, v60, v57
	v_alignbit_b32 v57, v58, v57, 16
	v_cvt_f16_f32_e32 v58, v52
	v_mov_b32_e32 v52, v53
	v_mov_b32_e32 v53, v54
	v_add_f32_e32 v54, v55, v51
	v_cvt_f16_f32_e32 v54, v54
	v_pk_add_f32 v[52:53], v[52:53], v[120:121]
	v_add_f32_e32 v24, v24, v40
	v_cvt_pk_f16_f32 v53, v52, v53
	v_pack_b32_f16 v52, v58, v53
	v_alignbit_b32 v53, v54, v53, 16
	v_cvt_f16_f32_e32 v54, v44
	v_mov_b32_e32 v44, v45
	v_mov_b32_e32 v45, v46
	v_add_f32_e32 v46, v47, v51
	v_cvt_f16_f32_e32 v46, v46
	v_pk_add_f32 v[44:45], v[44:45], v[120:121]
	s_nop 0
	v_cvt_pk_f16_f32 v45, v44, v45
	v_pack_b32_f16 v44, v54, v45
	v_alignbit_b32 v45, v46, v45, 16
	v_cvt_f16_f32_e32 v46, v36
	v_mov_b32_e32 v36, v37
	v_mov_b32_e32 v37, v38
	v_add_f32_e32 v38, v39, v51
	v_cvt_f16_f32_e32 v38, v38
	v_pk_add_f32 v[36:37], v[36:37], v[120:121]
	s_barrier
	v_cvt_pk_f16_f32 v37, v36, v37
	v_pack_b32_f16 v36, v46, v37
	v_alignbit_b32 v37, v38, v37, 16
	v_cvt_f16_f32_e32 v38, v32
	v_mov_b32_e32 v32, v33
	v_mov_b32_e32 v33, v34
	v_add_f32_e32 v34, v35, v43
	v_cvt_f16_f32_e32 v34, v34
	v_pk_add_f32 v[32:33], v[32:33], v[66:67]
	s_nop 0
	v_cvt_pk_f16_f32 v33, v32, v33
	v_pack_b32_f16 v32, v38, v33
	v_alignbit_b32 v33, v34, v33, 16
	ds_write2_b64 v130, v[56:57], v[32:33] offset1:4
	v_cvt_f16_f32_e32 v32, v24
	v_mov_b32_e32 v24, v25
	v_mov_b32_e32 v25, v26
	v_add_f32_e32 v26, v27, v43
	v_cvt_f16_f32_e32 v26, v26
	v_pk_add_f32 v[24:25], v[24:25], v[66:67]
	v_add_f32_e32 v20, v20, v40
	v_cvt_pk_f16_f32 v25, v24, v25
	v_pack_b32_f16 v24, v32, v25
	v_alignbit_b32 v25, v26, v25, 16
	ds_write2_b64 v132, v[52:53], v[24:25] offset0:32 offset1:36
	v_cvt_f16_f32_e32 v24, v20
	v_mov_b32_e32 v20, v21
	v_mov_b32_e32 v21, v22
	v_add_f32_e32 v22, v23, v43
	v_cvt_f16_f32_e32 v22, v22
	v_pk_add_f32 v[20:21], v[20:21], v[66:67]
	v_add_f32_e32 v16, v16, v40
	v_cvt_pk_f16_f32 v21, v20, v21
	v_pack_b32_f16 v20, v24, v21
	v_alignbit_b32 v21, v22, v21, 16
	ds_write2_b64 v131, v[44:45], v[20:21] offset0:64 offset1:68
	v_cvt_f16_f32_e32 v20, v16
	v_mov_b32_e32 v16, v17
	v_mov_b32_e32 v17, v18
	v_add_f32_e32 v18, v19, v43
	v_cvt_f16_f32_e32 v18, v18
	v_pk_add_f32 v[16:17], v[16:17], v[66:67]
	v_add_f32_e32 v12, v12, v28
	v_cvt_pk_f16_f32 v17, v16, v17
	v_pack_b32_f16 v16, v20, v17
	v_alignbit_b32 v17, v18, v17, 16
	ds_write2_b64 v91, v[36:37], v[16:17] offset0:96 offset1:100
	v_cvt_f16_f32_e32 v16, v12
	v_mov_b32_e32 v12, v13
	v_mov_b32_e32 v13, v14
	v_add_f32_e32 v14, v15, v31
	v_cvt_f16_f32_e32 v14, v14
	v_pk_add_f32 v[12:13], v[12:13], v[64:65]
	v_add_f32_e32 v8, v8, v28
	v_cvt_pk_f16_f32 v13, v12, v13
	v_pack_b32_f16 v12, v16, v13
	v_alignbit_b32 v13, v14, v13, 16
	ds_write_b64 v130, v[12:13] offset:64
	v_cvt_f16_f32_e32 v12, v8
	v_mov_b32_e32 v8, v9
	v_mov_b32_e32 v9, v10
	v_add_f32_e32 v10, v11, v31
	v_cvt_f16_f32_e32 v10, v10
	v_pk_add_f32 v[8:9], v[8:9], v[64:65]
	v_add_f32_e32 v4, v4, v28
	v_cvt_pk_f16_f32 v9, v8, v9
	v_pack_b32_f16 v8, v12, v9
	v_alignbit_b32 v9, v10, v9, 16
	ds_write_b64 v130, v[8:9] offset:12608
	v_cvt_f16_f32_e32 v8, v4
	v_mov_b32_e32 v4, v5
	v_mov_b32_e32 v5, v6
	v_add_f32_e32 v6, v7, v31
	v_cvt_f16_f32_e32 v6, v6
	v_pk_add_f32 v[4:5], v[4:5], v[64:65]
	v_add_f32_e32 v0, v0, v28
	v_cvt_pk_f16_f32 v5, v4, v5
	v_pack_b32_f16 v4, v8, v5
	v_alignbit_b32 v5, v6, v5, 16
	ds_write_b64 v130, v[4:5] offset:25152
	v_cvt_f16_f32_e32 v4, v0
	v_mov_b32_e32 v0, v1
	v_mov_b32_e32 v1, v2
	v_add_f32_e32 v2, v3, v31
	v_cvt_f16_f32_e32 v2, v2
	v_pk_add_f32 v[0:1], v[0:1], v[64:65]
	v_add_u32_e32 v8, v29, v68
	v_cvt_pk_f16_f32 v1, v0, v1
	v_pack_b32_f16 v0, v4, v1
	v_alignbit_b32 v1, v2, v1, 16
	ds_write_b64 v130, v[0:1] offset:37696
	s_waitcnt lgkmcnt(0)
	s_barrier
	ds_read_b128 v[0:3], v83
	ds_read_b128 v[4:7], v84
	v_add_u32_e32 v12, v42, v70
	s_waitcnt lgkmcnt(1)
	buffer_store_dwordx4 v[0:3], v8, s[0:3], 0 offen sc1
	ds_read_b128 v[0:3], v92
	v_add_u32_e32 v8, v30, v69
	s_waitcnt lgkmcnt(1)
	buffer_store_dwordx4 v[4:7], v8, s[0:3], 0 offen sc1
	v_add_u32_e32 v8, v41, v72
	ds_read_b128 v[4:7], v99
	s_waitcnt lgkmcnt(1)
	buffer_store_dwordx4 v[0:3], v8, s[0:3], 0 offen sc1
	ds_read_b128 v[0:3], v100
	ds_read_b128 v[8:11], v110
	s_waitcnt lgkmcnt(2)
	buffer_store_dwordx4 v[4:7], v12, s[0:3], 0 offen sc1
	s_nop 1
	v_add_u32_e32 v4, v49, v71
	s_waitcnt lgkmcnt(1)
	buffer_store_dwordx4 v[0:3], v4, s[0:3], 0 offen sc1
	s_nop 1
	v_add_u32_e32 v0, v50, v73
	s_waitcnt lgkmcnt(0)
	buffer_store_dwordx4 v[8:11], v0, s[0:3], 0 offen sc1
	s_endpgm

_Z7k_stageILi0ELi8EEv8AttnArgsPKDF16_PKfPDF16_iii:
	v_readfirstlane_b32 s94, v0
	s_nop 0
	s_lshr_b32 s94, s94, 6
	s_load_dwordx4 s[8:11], s[0:1], 0x88
	s_lshl_b32 s4, s2, 4
	s_and_b32 s4, s4, 0x70
	s_lshr_b32 s5, s2, 3
	s_add_i32 s4, s4, s5
	s_lshr_b32 s7, s4, 5
	s_lshl_b32 s6, s4, 1
	s_waitcnt lgkmcnt(0)
	s_lshl_b32 s11, s2, 1
	s_cmp_gt_i32 s10, 0
	v_readfirstlane_b32 s24, v0
	s_cbranch_scc1 .LBB3_2
	s_lshl_b32 s31, s7, 12
	s_ashr_i32 s2, s3, 31
	s_mov_b64 s[4:5], 0
	s_branch .LBB3_3

.LBB3_82:
	s_mul_i32 s0, s9, s3
	s_lshl_b32 s1, s30, 6
	s_add_i32 s0, s0, s8
	s_or_b32 s1, s1, s31
	s_or_b32 s7, s1, s11
	s_mul_i32 s4, s0, 0x60000
	s_mul_hi_i32 s1, s0, 0x60000
	s_waitcnt lgkmcnt(0)
	s_add_u32 s6, s12, s4
	s_mulk_i32 s0, 0x300
	s_addc_u32 s8, s13, s1
	s_ashr_i32 s1, s0, 31
	s_lshl_b64 s[0:1], s[0:1], 2
	s_add_u32 s4, s14, s0
	s_addc_u32 s5, s15, s1
	s_mul_i32 s0, s2, 0x1800000
	s_mul_hi_u32 s1, s3, 0x1800000
	s_add_i32 s1, s1, s0
	s_mul_i32 s0, s3, 0x1800000
	s_add_u32 s0, s20, s0
	v_readfirstlane_b32 s2, v0
	s_addc_u32 s1, s21, s1
	s_lshr_b32 s9, s2, 6
	s_and_b32 s1, s1, 0xffff
	s_mul_i32 s2, s9, 0x6000
	v_and_b32_e32 v2, 63, v0
	s_mul_hi_u32 s3, s9, 0x6000
	s_add_u32 s2, s6, s2
	s_addc_u32 s3, s8, s3
	v_lshlrev_b32_e32 v82, 4, v2
	v_mov_b32_e32 v83, 0
	v_lshl_add_u64 v[118:119], s[2:3], 0, v[82:83]
	s_movk_i32 s6, 0x1000
	v_add_co_u32_e32 v50, vcc, s6, v118
	s_movk_i32 s6, 0x2000
	s_nop 0
	v_addc_co_u32_e32 v51, vcc, 0, v119, vcc
	v_add_co_u32_e32 v52, vcc, s6, v118
	global_load_dwordx4 v[2:5], v82, s[2:3] offset:1024
	global_load_dwordx4 v[6:9], v82, s[2:3] offset:2048
	v_addc_co_u32_e32 v53, vcc, 0, v119, vcc
	global_load_dwordx4 v[10:13], v82, s[2:3] offset:3072
	global_load_dwordx4 v[14:17], v[52:53], off offset:-4096
	global_load_dwordx4 v[18:21], v[50:51], off offset:1024
	global_load_dwordx4 v[22:25], v[50:51], off offset:2048
	global_load_dwordx4 v[26:29], v82, s[2:3]
	global_load_dwordx4 v[30:33], v[50:51], off offset:3072
	global_load_dwordx4 v[34:37], v[52:53], off
	global_load_dwordx4 v[38:41], v[52:53], off offset:1024
	global_load_dwordx4 v[42:45], v[52:53], off offset:2048
	global_load_dwordx4 v[46:49], v[52:53], off offset:3072
	s_movk_i32 s2, 0x3000
	v_add_co_u32_e32 v116, vcc, s2, v118
	s_movk_i32 s2, 0x4000
	s_nop 0
	v_addc_co_u32_e32 v117, vcc, 0, v119, vcc
	v_add_co_u32_e32 v156, vcc, s2, v118
	s_nop 1
	v_addc_co_u32_e32 v157, vcc, 0, v119, vcc
	s_barrier
	s_cmp_lt_u32 s94, 4
	s_cbranch_scc1 .Lmystag3_1
	s_sleep 7
.Lmystag3_1:
	global_load_dwordx4 v[50:53], v[156:157], off offset:-4096
	global_load_dwordx4 v[54:57], v[116:117], off offset:1024
	global_load_dwordx4 v[58:61], v[116:117], off offset:2048
	v_mul_u32_u24_e32 v62, 0x556, v0
	v_lshlrev_b32_e32 v132, 9, v1
	v_lshrrev_b32_e32 v142, 16, v62
	v_xor_b32_e32 v62, v158, v1
	v_lshl_or_b32 v135, v62, 4, v132
	ds_read_b128 v[62:65], v135
	ds_read_b128 v[66:69], v135 offset:8192
	ds_read_b128 v[70:73], v135 offset:16384
	ds_read_b128 v[74:77], v135 offset:24576
	ds_read_b128 v[78:81], v135 offset:32768
	ds_read_b128 v[84:87], v135 offset:40960
	ds_read_b128 v[88:91], v135 offset:49152
	ds_read_b128 v[92:95], v135 offset:57344
	s_mul_i32 s6, s9, 48
	v_lshl_or_b32 v82, v158, 2, s6
	s_mul_i32 s6, s9, 0x60
	s_add_i32 s6, s6, 0x10000
	v_lshlrev_b32_e32 v96, 3, v142
	s_movk_i32 s9, 0x47
	v_lshl_or_b32 v248, v158, 3, s6
	s_or_b32 s6, s7, 8
	v_bitop3_b32 v143, v96, s9, v142 bitop3:0xc8
	s_mov_b32 s2, 0x1800000
	s_mov_b32 s3, 0x20000
	s_mov_b32 s8, 0x10000
	v_or_b32_e32 v140, s6, v143
	s_waitcnt vmcnt(8) lgkmcnt(7)
	v_mfma_f32_16x16x32_f16 v[96:99], v[26:29], v[62:65], 0
	s_waitcnt lgkmcnt(6)
	v_mfma_f32_16x16x32_f16 v[100:103], v[26:29], v[66:69], 0
	s_waitcnt lgkmcnt(5)
	v_mfma_f32_16x16x32_f16 v[104:107], v[26:29], v[70:73], 0
	s_waitcnt lgkmcnt(4)
	v_mfma_f32_16x16x32_f16 v[108:111], v[26:29], v[74:77], 0
	s_waitcnt lgkmcnt(3)
	v_mfma_f32_16x16x32_f16 v[112:115], v[26:29], v[78:81], 0
	s_waitcnt lgkmcnt(2)
	v_mfma_f32_16x16x32_f16 v[120:123], v[26:29], v[84:87], 0
	s_waitcnt lgkmcnt(1)
	v_mfma_f32_16x16x32_f16 v[124:127], v[26:29], v[88:91], 0
	s_waitcnt lgkmcnt(0)
	v_mfma_f32_16x16x32_f16 v[26:29], v[26:29], v[92:95], 0
	v_mfma_f32_16x16x32_f16 v[128:131], v[2:5], v[62:65], 0
	v_mfma_f32_16x16x32_f16 v[136:139], v[2:5], v[66:69], 0
	v_mfma_f32_16x16x32_f16 v[144:147], v[2:5], v[70:73], 0
	v_mfma_f32_16x16x32_f16 v[148:151], v[2:5], v[74:77], 0
	v_mfma_f32_16x16x32_f16 v[152:155], v[2:5], v[78:81], 0
	v_mfma_f32_16x16x32_f16 v[160:163], v[2:5], v[84:87], 0
	v_mfma_f32_16x16x32_f16 v[164:167], v[2:5], v[88:91], 0
	v_mfma_f32_16x16x32_f16 v[2:5], v[2:5], v[92:95], 0
	v_mfma_f32_16x16x32_f16 v[62:65], v[6:9], v[62:65], 0
	v_mfma_f32_16x16x32_f16 v[66:69], v[6:9], v[66:69], 0
	v_mfma_f32_16x16x32_f16 v[70:73], v[6:9], v[70:73], 0
	v_mfma_f32_16x16x32_f16 v[74:77], v[6:9], v[74:77], 0
	v_mfma_f32_16x16x32_f16 v[78:81], v[6:9], v[78:81], 0
	v_mfma_f32_16x16x32_f16 v[84:87], v[6:9], v[84:87], 0
	v_mfma_f32_16x16x32_f16 v[88:91], v[6:9], v[88:91], 0
	v_mfma_f32_16x16x32_f16 v[6:9], v[6:9], v[92:95], 0
	global_load_dwordx4 v[92:95], v[116:117], off offset:3072
	global_load_dwordx4 v[168:171], v[156:157], off
	global_load_dwordx4 v[172:175], v[156:157], off offset:1024
	v_bitop3_b32 v116, v158, v1, 4 bitop3:0x36
	v_lshl_or_b32 v133, v116, 4, v132
	ds_read_b128 v[176:179], v133
	ds_read_b128 v[180:183], v133 offset:8192
	ds_read_b128 v[184:187], v133 offset:16384
	ds_read_b128 v[188:191], v133 offset:24576
	ds_read_b128 v[192:195], v133 offset:32768
	ds_read_b128 v[196:199], v133 offset:40960
	ds_read_b128 v[200:203], v133 offset:49152
	ds_read_b128 v[204:207], v133 offset:57344
	s_waitcnt lgkmcnt(7)
	v_mfma_f32_16x16x32_f16 v[96:99], v[10:13], v[176:179], v[96:99]
	s_waitcnt lgkmcnt(6)
	v_mfma_f32_16x16x32_f16 v[100:103], v[10:13], v[180:183], v[100:103]
	s_waitcnt lgkmcnt(5)
	v_mfma_f32_16x16x32_f16 v[104:107], v[10:13], v[184:187], v[104:107]
	s_waitcnt lgkmcnt(4)
	v_mfma_f32_16x16x32_f16 v[108:111], v[10:13], v[188:191], v[108:111]
	s_waitcnt lgkmcnt(3)
	v_mfma_f32_16x16x32_f16 v[112:115], v[10:13], v[192:195], v[112:115]
	s_waitcnt lgkmcnt(2)
	v_mfma_f32_16x16x32_f16 v[120:123], v[10:13], v[196:199], v[120:123]
	s_waitcnt lgkmcnt(1)
	v_mfma_f32_16x16x32_f16 v[124:127], v[10:13], v[200:203], v[124:127]
	s_waitcnt lgkmcnt(0)
	v_mfma_f32_16x16x32_f16 v[10:13], v[10:13], v[204:207], v[26:29]
	v_mfma_f32_16x16x32_f16 v[26:29], v[14:17], v[176:179], v[128:131]
	v_mfma_f32_16x16x32_f16 v[128:131], v[14:17], v[180:183], v[136:139]
	v_mfma_f32_16x16x32_f16 v[136:139], v[14:17], v[184:187], v[144:147]
	v_mfma_f32_16x16x32_f16 v[144:147], v[14:17], v[188:191], v[148:151]
	v_mfma_f32_16x16x32_f16 v[148:151], v[14:17], v[192:195], v[152:155]
	v_mfma_f32_16x16x32_f16 v[152:155], v[14:17], v[196:199], v[160:163]
	v_mfma_f32_16x16x32_f16 v[160:163], v[14:17], v[200:203], v[164:167]
	v_mfma_f32_16x16x32_f16 v[2:5], v[14:17], v[204:207], v[2:5]
	v_mfma_f32_16x16x32_f16 v[14:17], v[18:21], v[176:179], v[62:65]
	v_mfma_f32_16x16x32_f16 v[62:65], v[18:21], v[180:183], v[66:69]
	v_mfma_f32_16x16x32_f16 v[66:69], v[18:21], v[184:187], v[70:73]
	v_mfma_f32_16x16x32_f16 v[70:73], v[18:21], v[188:191], v[74:77]
	v_mfma_f32_16x16x32_f16 v[74:77], v[18:21], v[192:195], v[78:81]
	v_mfma_f32_16x16x32_f16 v[78:81], v[18:21], v[196:199], v[84:87]
	v_mfma_f32_16x16x32_f16 v[84:87], v[18:21], v[200:203], v[88:91]
	v_mfma_f32_16x16x32_f16 v[6:9], v[18:21], v[204:207], v[6:9]
	s_movk_i32 s9, 0x5000
	v_add_co_u32_e32 v116, vcc, s9, v118
	global_load_dwordx4 v[88:91], v[156:157], off offset:2048
	global_load_dwordx4 v[164:167], v[156:157], off offset:3072
	v_addc_co_u32_e32 v117, vcc, 0, v119, vcc
	global_load_dwordx4 v[176:179], v[116:117], off
	v_bitop3_b32 v18, v158, v1, 8 bitop3:0x36
	v_lshl_or_b32 v134, v18, 4, v132
	ds_read_b128 v[18:21], v134
	ds_read_b128 v[180:183], v134 offset:8192
	ds_read_b128 v[184:187], v134 offset:16384
	ds_read_b128 v[188:191], v134 offset:24576
	ds_read_b128 v[192:195], v134 offset:32768
	ds_read_b128 v[196:199], v134 offset:40960
	ds_read_b128 v[200:203], v134 offset:49152
	ds_read_b128 v[204:207], v134 offset:57344
	s_waitcnt lgkmcnt(7)
	v_mfma_f32_16x16x32_f16 v[96:99], v[22:25], v[18:21], v[96:99]
	s_waitcnt lgkmcnt(6)
	v_mfma_f32_16x16x32_f16 v[100:103], v[22:25], v[180:183], v[100:103]
	s_waitcnt lgkmcnt(5)
	v_mfma_f32_16x16x32_f16 v[104:107], v[22:25], v[184:187], v[104:107]
	s_waitcnt lgkmcnt(4)
	v_mfma_f32_16x16x32_f16 v[108:111], v[22:25], v[188:191], v[108:111]
	s_waitcnt lgkmcnt(3)
	v_mfma_f32_16x16x32_f16 v[112:115], v[22:25], v[192:195], v[112:115]
	s_waitcnt lgkmcnt(2)
	v_mfma_f32_16x16x32_f16 v[120:123], v[22:25], v[196:199], v[120:123]
	s_waitcnt lgkmcnt(1)
	v_mfma_f32_16x16x32_f16 v[124:127], v[22:25], v[200:203], v[124:127]
	s_waitcnt lgkmcnt(0)
	v_mfma_f32_16x16x32_f16 v[10:13], v[22:25], v[204:207], v[10:13]
	s_waitcnt vmcnt(13)
	v_mfma_f32_16x16x32_f16 v[22:25], v[30:33], v[18:21], v[26:29]
	v_mfma_f32_16x16x32_f16 v[26:29], v[30:33], v[180:183], v[128:131]
	v_mfma_f32_16x16x32_f16 v[128:131], v[30:33], v[184:187], v[136:139]
	v_mfma_f32_16x16x32_f16 v[144:147], v[30:33], v[188:191], v[144:147]
	v_mfma_f32_16x16x32_f16 v[148:151], v[30:33], v[192:195], v[148:151]
	v_mfma_f32_16x16x32_f16 v[152:155], v[30:33], v[196:199], v[152:155]
	v_mfma_f32_16x16x32_f16 v[160:163], v[30:33], v[200:203], v[160:163]
	v_mfma_f32_16x16x32_f16 v[2:5], v[30:33], v[204:207], v[2:5]
	s_waitcnt vmcnt(12)
	v_mfma_f32_16x16x32_f16 v[14:17], v[34:37], v[18:21], v[14:17]
	v_mfma_f32_16x16x32_f16 v[18:21], v[34:37], v[180:183], v[62:65]
	v_mfma_f32_16x16x32_f16 v[30:33], v[34:37], v[184:187], v[66:69]
	v_mfma_f32_16x16x32_f16 v[62:65], v[34:37], v[188:191], v[70:73]
	v_mfma_f32_16x16x32_f16 v[66:69], v[34:37], v[192:195], v[74:77]
	v_mfma_f32_16x16x32_f16 v[70:73], v[34:37], v[196:199], v[78:81]
	v_mfma_f32_16x16x32_f16 v[74:77], v[34:37], v[200:203], v[84:87]
	v_mfma_f32_16x16x32_f16 v[6:9], v[34:37], v[204:207], v[6:9]
	s_nop 0
	global_load_dwordx4 v[78:81], v[116:117], off offset:1024
	global_load_dwordx4 v[180:183], v[116:117], off offset:2048
	global_load_dwordx4 v[184:187], v[116:117], off offset:3072
	v_bitop3_b32 v34, v158, v1, 12 bitop3:0x36
	v_lshl_or_b32 v136, v34, 4, v132
	ds_read_b128 v[34:37], v136
	ds_read_b128 v[84:87], v136 offset:8192
	ds_read_b128 v[188:191], v136 offset:16384
	ds_read_b128 v[192:195], v136 offset:24576
	ds_read_b128 v[196:199], v136 offset:32768
	ds_read_b128 v[200:203], v136 offset:40960
	ds_read_b128 v[204:207], v136 offset:49152
	ds_read_b128 v[208:211], v136 offset:57344
	s_waitcnt vmcnt(14) lgkmcnt(7)
	v_mfma_f32_16x16x32_f16 v[96:99], v[38:41], v[34:37], v[96:99]
	s_waitcnt lgkmcnt(6)
	v_mfma_f32_16x16x32_f16 v[100:103], v[38:41], v[84:87], v[100:103]
	s_waitcnt lgkmcnt(5)
	v_mfma_f32_16x16x32_f16 v[104:107], v[38:41], v[188:191], v[104:107]
	s_waitcnt lgkmcnt(4)
	v_mfma_f32_16x16x32_f16 v[108:111], v[38:41], v[192:195], v[108:111]
	s_waitcnt lgkmcnt(3)
	v_mfma_f32_16x16x32_f16 v[112:115], v[38:41], v[196:199], v[112:115]
	s_waitcnt lgkmcnt(2)
	v_mfma_f32_16x16x32_f16 v[120:123], v[38:41], v[200:203], v[120:123]
	s_waitcnt lgkmcnt(1)
	v_mfma_f32_16x16x32_f16 v[124:127], v[38:41], v[204:207], v[124:127]
	s_waitcnt lgkmcnt(0)
	v_mfma_f32_16x16x32_f16 v[212:215], v[38:41], v[208:211], v[10:13]
	s_waitcnt vmcnt(13)
	v_mfma_f32_16x16x32_f16 v[22:25], v[42:45], v[34:37], v[22:25]
	v_mfma_f32_16x16x32_f16 v[216:219], v[42:45], v[84:87], v[26:29]
	v_mfma_f32_16x16x32_f16 v[128:131], v[42:45], v[188:191], v[128:131]
	v_mfma_f32_16x16x32_f16 v[144:147], v[42:45], v[192:195], v[144:147]
	v_mfma_f32_16x16x32_f16 v[148:151], v[42:45], v[196:199], v[148:151]
	v_mfma_f32_16x16x32_f16 v[152:155], v[42:45], v[200:203], v[152:155]
	v_mfma_f32_16x16x32_f16 v[160:163], v[42:45], v[204:207], v[160:163]
	v_mfma_f32_16x16x32_f16 v[2:5], v[42:45], v[208:211], v[2:5]
	s_waitcnt vmcnt(12)
	v_mfma_f32_16x16x32_f16 v[14:17], v[46:49], v[34:37], v[14:17]
	v_mfma_f32_16x16x32_f16 v[18:21], v[46:49], v[84:87], v[18:21]
	v_mfma_f32_16x16x32_f16 v[30:33], v[46:49], v[188:191], v[30:33]
	v_mfma_f32_16x16x32_f16 v[34:37], v[46:49], v[192:195], v[62:65]
	v_mfma_f32_16x16x32_f16 v[42:45], v[46:49], v[196:199], v[66:69]
	v_mfma_f32_16x16x32_f16 v[62:65], v[46:49], v[200:203], v[70:73]
	v_mfma_f32_16x16x32_f16 v[66:69], v[46:49], v[204:207], v[74:77]
	v_mfma_f32_16x16x32_f16 v[6:9], v[46:49], v[208:211], v[6:9]
	s_mov_b32 s9, 0x30000
	v_add_co_u32_e32 v116, vcc, s9, v118
	s_mov_b32 s9, 0x31000
	s_nop 0
	v_addc_co_u32_e32 v117, vcc, 0, v119, vcc
	v_add_co_u32_e32 v156, vcc, s9, v118
	v_bitop3_b32 v46, v158, v1, 16 bitop3:0x36
	s_nop 0
	v_addc_co_u32_e32 v157, vcc, 0, v119, vcc
	global_load_dwordx4 v[38:41], v[156:157], off offset:-4096
	global_load_dwordx4 v[26:29], v[116:117], off offset:1024
	global_load_dwordx4 v[10:13], v[116:117], off offset:2048
	v_lshl_or_b32 v137, v46, 4, v132
	ds_read_b128 v[46:49], v137
	ds_read_b128 v[70:73], v137 offset:8192
	ds_read_b128 v[74:77], v137 offset:16384
	ds_read_b128 v[84:87], v137 offset:24576
	ds_read_b128 v[188:191], v137 offset:32768
	ds_read_b128 v[192:195], v137 offset:40960
	ds_read_b128 v[196:199], v137 offset:49152
	ds_read_b128 v[200:203], v137 offset:57344
	s_waitcnt vmcnt(14) lgkmcnt(7)
	v_mfma_f32_16x16x32_f16 v[96:99], v[50:53], v[46:49], v[96:99]
	s_waitcnt lgkmcnt(6)
	v_mfma_f32_16x16x32_f16 v[100:103], v[50:53], v[70:73], v[100:103]
	s_waitcnt lgkmcnt(5)
	v_mfma_f32_16x16x32_f16 v[104:107], v[50:53], v[74:77], v[104:107]
	s_waitcnt lgkmcnt(4)
	v_mfma_f32_16x16x32_f16 v[108:111], v[50:53], v[84:87], v[108:111]
	s_waitcnt lgkmcnt(3)
	v_mfma_f32_16x16x32_f16 v[112:115], v[50:53], v[188:191], v[112:115]
	s_waitcnt lgkmcnt(2)
	v_mfma_f32_16x16x32_f16 v[120:123], v[50:53], v[192:195], v[120:123]
	s_waitcnt lgkmcnt(1)
	v_mfma_f32_16x16x32_f16 v[124:127], v[50:53], v[196:199], v[124:127]
	s_waitcnt lgkmcnt(0)
	v_mfma_f32_16x16x32_f16 v[50:53], v[50:53], v[200:203], v[212:215]
	s_waitcnt vmcnt(13)
	v_mfma_f32_16x16x32_f16 v[204:207], v[54:57], v[46:49], v[22:25]
	v_mfma_f32_16x16x32_f16 v[208:211], v[54:57], v[70:73], v[216:219]
	v_mfma_f32_16x16x32_f16 v[128:131], v[54:57], v[74:77], v[128:131]
	v_mfma_f32_16x16x32_f16 v[144:147], v[54:57], v[84:87], v[144:147]
	v_mfma_f32_16x16x32_f16 v[148:151], v[54:57], v[188:191], v[148:151]
	v_mfma_f32_16x16x32_f16 v[152:155], v[54:57], v[192:195], v[152:155]
	v_mfma_f32_16x16x32_f16 v[160:163], v[54:57], v[196:199], v[160:163]
	v_mfma_f32_16x16x32_f16 v[54:57], v[54:57], v[200:203], v[2:5]
	s_waitcnt vmcnt(12)
	v_mfma_f32_16x16x32_f16 v[14:17], v[58:61], v[46:49], v[14:17]
	v_mfma_f32_16x16x32_f16 v[18:21], v[58:61], v[70:73], v[18:21]
	v_mfma_f32_16x16x32_f16 v[30:33], v[58:61], v[74:77], v[30:33]
	v_mfma_f32_16x16x32_f16 v[34:37], v[58:61], v[84:87], v[34:37]
	v_mfma_f32_16x16x32_f16 v[42:45], v[58:61], v[188:191], v[42:45]
	v_mfma_f32_16x16x32_f16 v[46:49], v[58:61], v[192:195], v[62:65]
	v_mfma_f32_16x16x32_f16 v[62:65], v[58:61], v[196:199], v[66:69]
	v_mfma_f32_16x16x32_f16 v[58:61], v[58:61], v[200:203], v[6:9]
	global_load_dwordx4 v[22:25], v[116:117], off offset:3072
	s_nop 1
	global_load_dwordx4 v[6:9], v[156:157], off
	global_load_dwordx4 v[2:5], v[156:157], off offset:1024
	v_bitop3_b32 v66, v158, v1, 20 bitop3:0x36
	v_lshl_or_b32 v138, v66, 4, v132
	ds_read_b128 v[66:69], v138
	ds_read_b128 v[70:73], v138 offset:8192
	ds_read_b128 v[74:77], v138 offset:16384
	ds_read_b128 v[84:87], v138 offset:24576
	ds_read_b128 v[188:191], v138 offset:32768
	ds_read_b128 v[192:195], v138 offset:40960
	ds_read_b128 v[196:199], v138 offset:49152
	ds_read_b128 v[200:203], v138 offset:57344
	s_waitcnt vmcnt(14) lgkmcnt(7)
	v_mfma_f32_16x16x32_f16 v[96:99], v[92:95], v[66:69], v[96:99]
	s_waitcnt lgkmcnt(6)
	v_mfma_f32_16x16x32_f16 v[100:103], v[92:95], v[70:73], v[100:103]
	s_waitcnt lgkmcnt(5)
	v_mfma_f32_16x16x32_f16 v[104:107], v[92:95], v[74:77], v[104:107]
	s_waitcnt lgkmcnt(4)
	v_mfma_f32_16x16x32_f16 v[108:111], v[92:95], v[84:87], v[108:111]
	s_waitcnt lgkmcnt(3)
	v_mfma_f32_16x16x32_f16 v[112:115], v[92:95], v[188:191], v[112:115]
	s_waitcnt lgkmcnt(2)
	v_mfma_f32_16x16x32_f16 v[212:215], v[92:95], v[192:195], v[120:123]
	s_waitcnt lgkmcnt(1)
	v_mfma_f32_16x16x32_f16 v[124:127], v[92:95], v[196:199], v[124:127]
	s_waitcnt lgkmcnt(0)
	v_mfma_f32_16x16x32_f16 v[50:53], v[92:95], v[200:203], v[50:53]
	s_waitcnt vmcnt(13)
	v_mfma_f32_16x16x32_f16 v[92:95], v[168:171], v[66:69], v[204:207]
	v_mfma_f32_16x16x32_f16 v[204:207], v[168:171], v[70:73], v[208:211]
	v_mfma_f32_16x16x32_f16 v[128:131], v[168:171], v[74:77], v[128:131]
	v_mfma_f32_16x16x32_f16 v[144:147], v[168:171], v[84:87], v[144:147]
	v_mfma_f32_16x16x32_f16 v[148:151], v[168:171], v[188:191], v[148:151]
	v_mfma_f32_16x16x32_f16 v[152:155], v[168:171], v[192:195], v[152:155]
	v_mfma_f32_16x16x32_f16 v[160:163], v[168:171], v[196:199], v[160:163]
	v_mfma_f32_16x16x32_f16 v[54:57], v[168:171], v[200:203], v[54:57]
	s_waitcnt vmcnt(12)
	v_mfma_f32_16x16x32_f16 v[66:69], v[172:175], v[66:69], v[14:17]
	v_mfma_f32_16x16x32_f16 v[70:73], v[172:175], v[70:73], v[18:21]
	v_mfma_f32_16x16x32_f16 v[74:77], v[172:175], v[74:77], v[30:33]
	v_mfma_f32_16x16x32_f16 v[34:37], v[172:175], v[84:87], v[34:37]
	v_mfma_f32_16x16x32_f16 v[42:45], v[172:175], v[188:191], v[42:45]
	v_mfma_f32_16x16x32_f16 v[46:49], v[172:175], v[192:195], v[46:49]
	v_mfma_f32_16x16x32_f16 v[62:65], v[172:175], v[196:199], v[62:65]
	v_mfma_f32_16x16x32_f16 v[58:61], v[172:175], v[200:203], v[58:61]
	s_mov_b32 s9, 0x33000
	v_add_co_u32_e32 v122, vcc, s9, v118
	global_load_dwordx4 v[30:33], v[156:157], off offset:2048
	global_load_dwordx4 v[14:17], v[156:157], off offset:3072
	v_addc_co_u32_e32 v123, vcc, 0, v119, vcc
	global_load_dwordx4 v[18:21], v[122:123], off offset:-4096
	v_bitop3_b32 v84, v158, v1, 24 bitop3:0x36
	v_lshl_or_b32 v139, v84, 4, v132
	ds_read_b128 v[84:87], v139
	ds_read_b128 v[168:171], v139 offset:8192
	ds_read_b128 v[172:175], v139 offset:16384
	ds_read_b128 v[188:191], v139 offset:24576
	ds_read_b128 v[192:195], v139 offset:32768
	ds_read_b128 v[196:199], v139 offset:40960
	ds_read_b128 v[200:203], v139 offset:49152
	ds_read_b128 v[208:211], v139 offset:57344
	s_mov_b32 s9, 0x32000
	v_add_co_u32_e32 v116, vcc, s9, v118
	s_nop 1
	v_addc_co_u32_e32 v117, vcc, 0, v119, vcc
	s_waitcnt vmcnt(14) lgkmcnt(7)
	v_mfma_f32_16x16x32_f16 v[96:99], v[88:91], v[84:87], v[96:99]
	s_waitcnt lgkmcnt(6)
	v_mfma_f32_16x16x32_f16 v[100:103], v[88:91], v[168:171], v[100:103]
	s_waitcnt lgkmcnt(5)
	v_mfma_f32_16x16x32_f16 v[104:107], v[88:91], v[172:175], v[104:107]
	s_waitcnt lgkmcnt(4)
	v_mfma_f32_16x16x32_f16 v[108:111], v[88:91], v[188:191], v[108:111]
	s_waitcnt lgkmcnt(3)
	v_mfma_f32_16x16x32_f16 v[112:115], v[88:91], v[192:195], v[112:115]
	s_waitcnt lgkmcnt(2)
	v_mfma_f32_16x16x32_f16 v[212:215], v[88:91], v[196:199], v[212:215]
	s_waitcnt lgkmcnt(1)
	v_mfma_f32_16x16x32_f16 v[124:127], v[88:91], v[200:203], v[124:127]
	s_waitcnt lgkmcnt(0)
	v_mfma_f32_16x16x32_f16 v[50:53], v[88:91], v[208:211], v[50:53]
	s_waitcnt vmcnt(13)
	v_mfma_f32_16x16x32_f16 v[90:93], v[164:167], v[84:87], v[92:95]
	v_mfma_f32_16x16x32_f16 v[204:207], v[164:167], v[168:171], v[204:207]
	v_mfma_f32_16x16x32_f16 v[128:131], v[164:167], v[172:175], v[128:131]
	v_mfma_f32_16x16x32_f16 v[144:147], v[164:167], v[188:191], v[144:147]
	v_mfma_f32_16x16x32_f16 v[148:151], v[164:167], v[192:195], v[148:151]
	v_mfma_f32_16x16x32_f16 v[152:155], v[164:167], v[196:199], v[152:155]
	v_mfma_f32_16x16x32_f16 v[160:163], v[164:167], v[200:203], v[160:163]
	v_mfma_f32_16x16x32_f16 v[54:57], v[164:167], v[208:211], v[54:57]
	s_waitcnt vmcnt(12)
	v_mfma_f32_16x16x32_f16 v[164:167], v[176:179], v[84:87], v[66:69]
	v_mfma_f32_16x16x32_f16 v[168:171], v[176:179], v[168:171], v[70:73]
	v_mfma_f32_16x16x32_f16 v[172:175], v[176:179], v[172:175], v[74:77]
	v_mfma_f32_16x16x32_f16 v[188:191], v[176:179], v[188:191], v[34:37]
	v_mfma_f32_16x16x32_f16 v[192:195], v[176:179], v[192:195], v[42:45]
	v_mfma_f32_16x16x32_f16 v[196:199], v[176:179], v[196:199], v[46:49]
	v_mfma_f32_16x16x32_f16 v[200:203], v[176:179], v[200:203], v[62:65]
	v_mfma_f32_16x16x32_f16 v[176:179], v[176:179], v[208:211], v[58:61]
	s_nop 0
	global_load_dwordx4 v[46:49], v[116:117], off offset:1024
	global_load_dwordx4 v[42:45], v[116:117], off offset:2048
	global_load_dwordx4 v[34:37], v[116:117], off offset:3072
	v_bitop3_b32 v58, v158, v1, 28 bitop3:0x36
	v_lshl_or_b32 v141, v58, 4, v132
	ds_read_b128 v[58:61], v141
	ds_read_b128 v[62:65], v141 offset:8192
	ds_read_b128 v[156:159], v141 offset:16384
	ds_read_b128 v[208:211], v141 offset:24576
	ds_read_b128 v[216:219], v141 offset:32768
	ds_read_b128 v[220:223], v141 offset:40960
	ds_read_b128 v[224:227], v141 offset:49152
	ds_read_b128 v[228:231], v141 offset:57344
	s_waitcnt vmcnt(14) lgkmcnt(7)
	v_mfma_f32_16x16x32_f16 v[232:235], v[78:81], v[58:61], v[96:99]
	s_waitcnt lgkmcnt(6)
	v_mfma_f32_16x16x32_f16 v[236:239], v[78:81], v[62:65], v[100:103]
	s_waitcnt lgkmcnt(5)
	v_mfma_f32_16x16x32_f16 v[240:243], v[78:81], v[156:159], v[104:107]
	s_waitcnt lgkmcnt(4)
	v_mfma_f32_16x16x32_f16 v[244:247], v[78:81], v[208:211], v[108:111]
	s_waitcnt lgkmcnt(3)
	v_mfma_f32_16x16x32_f16 v[106:109], v[78:81], v[216:219], v[112:115]
	s_waitcnt lgkmcnt(2)
	v_mfma_f32_16x16x32_f16 v[102:105], v[78:81], v[220:223], v[212:215]
	s_waitcnt lgkmcnt(1)
	v_mfma_f32_16x16x32_f16 v[94:97], v[78:81], v[224:227], v[124:127]
	s_waitcnt lgkmcnt(0)
	v_mfma_f32_16x16x32_f16 v[86:89], v[78:81], v[228:231], v[50:53]
	s_waitcnt vmcnt(13)
	v_mfma_f32_16x16x32_f16 v[124:127], v[180:183], v[58:61], v[90:93]
	v_mfma_f32_16x16x32_f16 v[204:207], v[180:183], v[62:65], v[204:207]
	v_mfma_f32_16x16x32_f16 v[212:215], v[180:183], v[156:159], v[128:131]
	v_mfma_f32_16x16x32_f16 v[144:147], v[180:183], v[208:211], v[144:147]
	v_mfma_f32_16x16x32_f16 v[78:81], v[180:183], v[216:219], v[148:151]
	v_mfma_f32_16x16x32_f16 v[74:77], v[180:183], v[220:223], v[152:155]
	v_mfma_f32_16x16x32_f16 v[70:73], v[180:183], v[224:227], v[160:163]
	v_mfma_f32_16x16x32_f16 v[66:69], v[180:183], v[228:231], v[54:57]
	s_waitcnt vmcnt(12)
	v_mfma_f32_16x16x32_f16 v[148:151], v[184:187], v[58:61], v[164:167]
	v_mfma_f32_16x16x32_f16 v[152:155], v[184:187], v[62:65], v[168:171]
	v_mfma_f32_16x16x32_f16 v[114:117], v[184:187], v[156:159], v[172:175]
	v_mfma_f32_16x16x32_f16 v[110:113], v[184:187], v[208:211], v[188:191]
	v_mfma_f32_16x16x32_f16 v[62:65], v[184:187], v[216:219], v[192:195]
	v_mfma_f32_16x16x32_f16 v[58:61], v[184:187], v[220:223], v[196:199]
	v_mfma_f32_16x16x32_f16 v[54:57], v[184:187], v[224:227], v[200:203]
	v_mfma_f32_16x16x32_f16 v[50:53], v[184:187], v[228:231], v[176:179]
	v_lshl_add_u64 v[120:121], v[82:83], 2, s[4:5]
	global_load_dwordx4 v[98:101], v[120:121], off
	global_load_dwordx4 v[90:93], v[120:121], off offset:64
	global_load_dwordx4 v[82:85], v[120:121], off offset:128
	s_movk_i32 s4, 0x310
	v_mad_u32_u24 v130, v1, s4, v248
	v_mov_b32_e32 v156, v237
	v_mov_b32_e32 v157, v238
	v_mov_b32_e32 v158, v241
	v_mov_b32_e32 v159, v242
	v_mov_b32_e32 v160, v245
	v_mov_b32_e32 v161, v246
	v_mov_b32_e32 v162, v205
	v_mov_b32_e32 v163, v206
	v_mov_b32_e32 v167, v146
	v_mov_b32_e32 v164, v213
	v_mov_b32_e32 v165, v214
	v_mov_b32_e32 v166, v145
	s_barrier
	v_add_u32_e32 v132, 0x3000, v130
	v_add_u32_e32 v131, 0x6000, v130
	s_mov_b32 s5, 0xfffffd0
	v_mul_lo_u32 v174, v142, s5
	s_movk_i32 s4, 0x600
	s_movk_i32 s9, 0xc7
	s_waitcnt vmcnt(2)
	v_pk_add_f32 v[168:169], v[232:233], v[98:99]
	v_pk_add_f32 v[170:171], v[234:235], v[100:101]
	v_add_f32_e32 v1, v236, v98
	v_pk_mov_b32 v[128:129], v[98:99], v[100:101] op_sel:[1,0]
	v_add_f32_e32 v99, v239, v101
	s_waitcnt vmcnt(1)
	v_pk_add_f32 v[124:125], v[124:125], v[90:91]
	v_pk_add_f32 v[172:173], v[126:127], v[92:93]
	v_add_f32_e32 v178, v204, v90
	v_pk_mov_b32 v[126:127], v[90:91], v[92:93] op_sel:[1,0]
	v_add_f32_e32 v91, v207, v93
	v_add_f32_e32 v100, v240, v98
	v_add_f32_e32 v175, v243, v101
	v_add_f32_e32 v92, v212, v90
	v_add_f32_e32 v179, v215, v93
	v_add_f32_e32 v181, v147, v93
	v_cvt_pk_f16_f32 v147, v170, v171
	v_cvt_f16_f32_e32 v1, v1
	v_cvt_f16_f32_e32 v99, v99
	v_cvt_f16_f32_e32 v171, v178
	v_cvt_f16_f32_e32 v91, v91
	v_cvt_pk_f16_f32 v146, v168, v169
	v_cvt_f16_f32_e32 v100, v100
	v_cvt_f16_f32_e32 v168, v175
	v_cvt_pk_f16_f32 v124, v124, v125
	v_cvt_pk_f16_f32 v125, v172, v173
	v_cvt_f16_f32_e32 v92, v92
	v_cvt_f16_f32_e32 v172, v179
	v_add_f32_e32 v180, v144, v90
	s_waitcnt vmcnt(0)
	v_pk_add_f32 v[144:145], v[148:149], v[82:83]
	v_pk_add_f32 v[148:149], v[156:157], v[128:129]
	v_pk_add_f32 v[156:157], v[158:159], v[128:129]
	v_pk_add_f32 v[158:159], v[160:161], v[128:129]
	v_pk_add_f32 v[160:161], v[162:163], v[126:127]
	v_pk_add_f32 v[162:163], v[164:165], v[126:127]
	v_cvt_pk_f16_f32 v144, v144, v145
	v_cvt_pk_f16_f32 v145, v148, v149
	v_cvt_pk_f16_f32 v148, v156, v157
	v_cvt_pk_f16_f32 v157, v160, v161
	v_cvt_pk_f16_f32 v149, v158, v159
	v_cvt_pk_f16_f32 v159, v162, v163
	ds_write2_b64 v130, v[146:147], v[124:125] offset1:4
	v_pack_b32_f16 v124, v1, v145
	v_alignbit_b32 v125, v99, v145, 16
	v_pack_b32_f16 v156, v171, v157
	v_alignbit_b32 v157, v91, v157, 16
	v_pack_b32_f16 v146, v100, v148
	v_alignbit_b32 v147, v168, v148, 16
	v_pack_b32_f16 v158, v92, v159
	v_alignbit_b32 v159, v172, v159, 16
	ds_write2_b64 v132, v[124:125], v[156:157] offset0:32 offset1:36
	ds_write2_b64 v131, v[146:147], v[158:159] offset0:64 offset1:68
	v_pk_add_f32 v[124:125], v[150:151], v[84:85]
	v_add_f32_e32 v1, v152, v82
	v_cvt_pk_f16_f32 v145, v124, v125
	v_pk_mov_b32 v[124:125], v[82:83], v[84:85] op_sel:[1,0]
	v_add_f32_e32 v83, v155, v85
	v_cvt_f16_f32_e32 v1, v1
	v_cvt_f16_f32_e32 v83, v83
	ds_write_b64 v130, v[144:145] offset:64
	v_mov_b32_e32 v144, v153
	v_mov_b32_e32 v145, v154
	v_pk_add_f32 v[144:145], v[144:145], v[124:125]
	v_add_f32_e32 v176, v244, v98
	v_cvt_pk_f16_f32 v84, v144, v145
	v_pack_b32_f16 v144, v1, v84
	v_alignbit_b32 v145, v83, v84, 16
	v_add_f32_e32 v1, v114, v82
	v_add_f32_e32 v83, v117, v85
	v_cvt_f16_f32_e32 v1, v1
	v_cvt_f16_f32_e32 v83, v83
	v_mov_b32_e32 v114, v115
	v_mov_b32_e32 v115, v116
	v_pk_add_f32 v[114:115], v[114:115], v[124:125]
	v_add_f32_e32 v177, v247, v101
	v_cvt_pk_f16_f32 v84, v114, v115
	v_pack_b32_f16 v114, v1, v84
	v_alignbit_b32 v115, v83, v84, 16
	v_add_f32_e32 v1, v110, v82
	v_add_f32_e32 v83, v113, v85
	v_cvt_f16_f32_e32 v1, v1
	v_cvt_f16_f32_e32 v83, v83
	v_mov_b32_e32 v110, v111
	v_mov_b32_e32 v111, v112
	v_cvt_f16_f32_e32 v169, v176
	v_cvt_f16_f32_e32 v170, v177
	v_cvt_f16_f32_e32 v173, v180
	v_pk_add_f32 v[164:165], v[166:167], v[126:127]
	v_cvt_f16_f32_e32 v166, v181
	v_pk_add_f32 v[110:111], v[110:111], v[124:125]
	v_cvt_pk_f16_f32 v161, v164, v165
	v_cvt_pk_f16_f32 v84, v110, v111
	v_pack_b32_f16 v110, v1, v84
	v_alignbit_b32 v111, v83, v84, 16
	ds_write_b64 v130, v[110:111] offset:37696
	v_add_lshl_u32 v111, v174, v0, 4
	v_mul_u32_u24_e32 v83, 0x310, v142
	v_pack_b32_f16 v148, v169, v149
	v_alignbit_b32 v149, v170, v149, 16
	v_pack_b32_f16 v160, v173, v161
	v_alignbit_b32 v161, v166, v161, 16
	v_add_u32_e32 v91, 0x9000, v130
	v_add3_u32 v83, v111, v83, s8
	v_or_b32_e32 v84, 0x200, v0
	ds_write2_b64 v91, v[148:149], v[160:161] offset0:96 offset1:100
	ds_write_b64 v130, v[144:145] offset:12608
	ds_write_b64 v130, v[114:115] offset:25152
	s_waitcnt lgkmcnt(0)
	s_barrier
	ds_read_b128 v[114:117], v83
	v_mul_u32_u24_e32 v92, 0x556, v84
	v_lshrrev_b32_e32 v92, 16, v92
	v_or_b32_e32 v1, s7, v143
	v_mul_lo_u32 v99, v92, s5
	v_mul_lo_u32 v112, v1, s4
	v_add_lshl_u32 v113, v99, v84, 4
	v_mul_u32_u24_e32 v84, 0x310, v92
	v_add_u32_e32 v1, v112, v111
	v_add3_u32 v84, v113, v84, s8
	ds_read_b128 v[142:145], v84
	s_waitcnt lgkmcnt(1)
	buffer_store_dwordx4 v[114:117], v1, s[0:3], 0 offen sc1
	v_lshlrev_b32_e32 v1, 3, v92
	v_bitop3_b32 v154, v1, s9, v92 bitop3:0xc8
	v_or_b32_e32 v1, s7, v154
	v_mul_lo_u32 v114, v1, s4
	v_add_u32_e32 v1, v114, v113
	s_waitcnt lgkmcnt(0)
	buffer_store_dwordx4 v[142:145], v1, s[0:3], 0 offen sc1
	v_or_b32_e32 v1, 0x400, v0
	v_mul_u32_u24_e32 v92, 0x556, v1
	v_lshrrev_b32_e32 v92, 16, v92
	v_mul_lo_u32 v99, v92, s5
	v_lshlrev_b32_e32 v100, 3, v92
	s_movk_i32 s9, 0x1c7
	v_bitop3_b32 v155, v100, s9, v92 bitop3:0xc8
	v_add_lshl_u32 v115, v99, v1, 4
	v_mul_u32_u24_e32 v92, 0x310, v92
	v_or_b32_e32 v100, s7, v155
	v_add3_u32 v92, v115, v92, s8
	v_or_b32_e32 v99, 0x600, v0
	v_mul_lo_u32 v116, v100, s4
	ds_read_b128 v[142:145], v92
	v_mul_u32_u24_e32 v100, 0x556, v99
	v_lshrrev_b32_e32 v100, 16, v100
	v_mul_lo_u32 v110, v100, s5
	v_add_lshl_u32 v117, v110, v99, 4
	v_mul_u32_u24_e32 v99, 0x310, v100
	v_add_u32_e32 v1, v116, v115
	v_add3_u32 v99, v117, v99, s8
	ds_read_b128 v[146:149], v99
	s_waitcnt lgkmcnt(1)
	buffer_store_dwordx4 v[142:145], v1, s[0:3], 0 offen sc1
	v_lshlrev_b32_e32 v1, 3, v100
	v_bitop3_b32 v156, v1, s9, v100 bitop3:0xc8
	v_add_u32_e32 v1, s7, v156
	v_mul_lo_u32 v142, v1, s4
	v_add_u32_e32 v1, v142, v117
	s_waitcnt lgkmcnt(0)
	buffer_store_dwordx4 v[146:149], v1, s[0:3], 0 offen sc1
	v_or_b32_e32 v1, 0x800, v0
	v_mul_u32_u24_e32 v100, 0xaab, v1
	v_lshrrev_b32_e32 v100, 17, v100
	v_mul_lo_u32 v110, v100, s5
	v_lshlrev_b32_e32 v143, 3, v100
	v_bitop3_b32 v157, v143, s9, v100 bitop3:0xc8
	v_add_lshl_u32 v144, v110, v1, 4
	v_mul_u32_u24_e32 v100, 0x310, v100
	v_or_b32_e32 v0, 0xa00, v0
	v_add3_u32 v100, v100, v144, s8
	v_mul_u32_u24_e32 v110, 0xaab, v0
	ds_read_b128 v[146:149], v100
	v_lshrrev_b32_e32 v158, 17, v110
	v_mul_lo_u32 v110, v158, s5
	v_or_b32_e32 v143, s7, v157
	v_add_lshl_u32 v145, v110, v0, 4
	v_mul_u32_u24_e32 v0, 0x310, v158
	v_mul_lo_u32 v143, v143, s4
	v_add3_u32 v110, v0, v145, s8
	v_add_u32_e32 v1, v143, v144
	ds_read_b128 v[150:153], v110
	v_lshlrev_b32_e32 v0, 3, v158
	s_movk_i32 s5, 0x3c7
	s_waitcnt lgkmcnt(1)
	buffer_store_dwordx4 v[146:149], v1, s[0:3], 0 offen sc1
	v_mov_b32_e32 v1, v108
	v_add_f32_e32 v102, v102, v98
	v_bitop3_b32 v147, v0, s5, v158 bitop3:0xc8
	v_add_u32_e32 v0, s7, v147
	v_mul_lo_u32 v146, v0, s4
	v_add_u32_e32 v0, v146, v145
	s_waitcnt lgkmcnt(0)
	buffer_store_dwordx4 v[150:153], v0, s[0:3], 0 offen sc1
	v_add_f32_e32 v0, v106, v98
	v_cvt_f16_f32_e32 v106, v0
	v_mov_b32_e32 v0, v107
	v_pk_add_f32 v[0:1], v[0:1], v[128:129]
	v_add_f32_e32 v94, v94, v98
	v_cvt_pk_f16_f32 v1, v0, v1
	v_pack_b32_f16 v0, v106, v1
	v_cvt_f16_f32_e32 v106, v102
	v_mov_b32_e32 v102, v103
	v_mov_b32_e32 v103, v104
	v_add_f32_e32 v104, v105, v101
	v_cvt_f16_f32_e32 v104, v104
	v_pk_add_f32 v[102:103], v[102:103], v[128:129]
	v_add_f32_e32 v86, v86, v98
	v_cvt_pk_f16_f32 v103, v102, v103
	v_pack_b32_f16 v102, v106, v103
	v_alignbit_b32 v103, v104, v103, 16
	v_cvt_f16_f32_e32 v104, v94
	v_mov_b32_e32 v94, v95
	v_mov_b32_e32 v95, v96
	v_add_f32_e32 v96, v97, v101
	v_cvt_f16_f32_e32 v96, v96
	v_pk_add_f32 v[94:95], v[94:95], v[128:129]
	v_add_f32_e32 v78, v78, v90
	v_cvt_pk_f16_f32 v95, v94, v95
	v_pack_b32_f16 v94, v104, v95
	v_alignbit_b32 v95, v96, v95, 16
	v_cvt_f16_f32_e32 v96, v86
	v_mov_b32_e32 v86, v87
	v_mov_b32_e32 v87, v88
	v_add_f32_e32 v88, v89, v101
	v_cvt_f16_f32_e32 v88, v88
	v_pk_add_f32 v[86:87], v[86:87], v[128:129]
	v_add_f32_e32 v107, v109, v101
	v_cvt_pk_f16_f32 v87, v86, v87
	v_pack_b32_f16 v86, v96, v87
	v_alignbit_b32 v87, v88, v87, 16
	v_cvt_f16_f32_e32 v88, v78
	v_mov_b32_e32 v78, v79
	v_mov_b32_e32 v79, v80
	v_add_f32_e32 v80, v81, v93
	v_cvt_f16_f32_e32 v107, v107
	v_cvt_f16_f32_e32 v80, v80
	v_pk_add_f32 v[78:79], v[78:79], v[126:127]
	s_nop 0
	v_cvt_pk_f16_f32 v79, v78, v79
	v_alignbit_b32 v1, v107, v1, 16
	v_pack_b32_f16 v78, v88, v79
	v_alignbit_b32 v79, v80, v79, 16
	s_barrier
	ds_write2_b64 v130, v[0:1], v[78:79] offset1:4
	v_add_f32_e32 v0, v74, v90
	v_cvt_f16_f32_e32 v74, v0
	v_mov_b32_e32 v0, v75
	v_add_f32_e32 v75, v77, v93
	v_cvt_f16_f32_e32 v75, v75
	v_mov_b32_e32 v1, v76
	v_pk_add_f32 v[0:1], v[0:1], v[126:127]
	s_nop 0
	v_cvt_pk_f16_f32 v1, v0, v1
	v_pack_b32_f16 v0, v74, v1
	v_alignbit_b32 v1, v75, v1, 16
	ds_write2_b64 v132, v[102:103], v[0:1] offset0:32 offset1:36
	v_add_f32_e32 v0, v70, v90
	v_cvt_f16_f32_e32 v70, v0
	v_mov_b32_e32 v0, v71
	v_add_f32_e32 v71, v73, v93
	v_cvt_f16_f32_e32 v71, v71
	v_mov_b32_e32 v1, v72
	v_pk_add_f32 v[0:1], v[0:1], v[126:127]
	s_nop 0
	v_cvt_pk_f16_f32 v1, v0, v1
	v_pack_b32_f16 v0, v70, v1
	v_alignbit_b32 v1, v71, v1, 16
	ds_write2_b64 v131, v[94:95], v[0:1] offset0:64 offset1:68
	v_add_f32_e32 v0, v66, v90
	v_cvt_f16_f32_e32 v66, v0
	v_mov_b32_e32 v0, v67
	v_add_f32_e32 v67, v69, v93
	v_cvt_f16_f32_e32 v67, v67
	v_mov_b32_e32 v1, v68
	v_pk_add_f32 v[0:1], v[0:1], v[126:127]
	v_mul_lo_u32 v68, v140, s4
	v_cvt_pk_f16_f32 v1, v0, v1
	v_pack_b32_f16 v0, v66, v1
	v_alignbit_b32 v1, v67, v1, 16
	ds_write2_b64 v91, v[86:87], v[0:1] offset0:96 offset1:100
	v_add_f32_e32 v0, v62, v82
	v_cvt_f16_f32_e32 v62, v0
	v_mov_b32_e32 v0, v63
	v_add_f32_e32 v63, v65, v85
	v_cvt_f16_f32_e32 v63, v63
	v_mov_b32_e32 v1, v64
	v_pk_add_f32 v[0:1], v[0:1], v[124:125]
	s_nop 0
	v_cvt_pk_f16_f32 v1, v0, v1
	v_pack_b32_f16 v0, v62, v1
	v_alignbit_b32 v1, v63, v1, 16
	ds_write_b64 v130, v[0:1] offset:64
	v_add_f32_e32 v0, v58, v82
	v_cvt_f16_f32_e32 v58, v0
	v_mov_b32_e32 v0, v59
	v_add_f32_e32 v59, v61, v85
	v_cvt_f16_f32_e32 v59, v59
	v_mov_b32_e32 v1, v60
	v_pk_add_f32 v[0:1], v[0:1], v[124:125]
	s_nop 0
	v_cvt_pk_f16_f32 v1, v0, v1
	v_pack_b32_f16 v0, v58, v1
	v_alignbit_b32 v1, v59, v1, 16
	ds_write_b64 v130, v[0:1] offset:12608
	v_add_f32_e32 v0, v54, v82
	v_cvt_f16_f32_e32 v54, v0
	v_mov_b32_e32 v0, v55
	v_add_f32_e32 v55, v57, v85
	v_cvt_f16_f32_e32 v55, v55
	v_mov_b32_e32 v1, v56
	v_pk_add_f32 v[0:1], v[0:1], v[124:125]
	s_nop 0
	v_cvt_pk_f16_f32 v1, v0, v1
	v_pack_b32_f16 v0, v54, v1
	v_alignbit_b32 v1, v55, v1, 16
	ds_write_b64 v130, v[0:1] offset:25152
	v_add_f32_e32 v0, v50, v82
	v_cvt_f16_f32_e32 v50, v0
	v_mov_b32_e32 v0, v51
	v_add_f32_e32 v51, v53, v85
	v_cvt_f16_f32_e32 v51, v51
	v_mov_b32_e32 v1, v52
	v_pk_add_f32 v[0:1], v[0:1], v[124:125]
	s_nop 0
	v_cvt_pk_f16_f32 v1, v0, v1
	v_pack_b32_f16 v0, v50, v1
	v_alignbit_b32 v1, v51, v1, 16
	ds_write_b64 v130, v[0:1] offset:37696
	s_waitcnt lgkmcnt(0)
	s_barrier
	s_cmp_lt_u32 s94, 4
	s_cbranch_scc1 .Lmystag3_5
	s_sleep 7
.Lmystag3_5:
	global_load_dwordx4 v[50:53], v[122:123], off
	global_load_dwordx4 v[54:57], v[122:123], off offset:1024
	global_load_dwordx4 v[58:61], v[122:123], off offset:2048
	ds_read_b128 v[62:65], v83
	ds_read_b128 v[70:73], v84
	v_add_u32_e32 v0, v68, v111
	ds_read_b128 v[74:77], v99
	s_waitcnt lgkmcnt(2)
	buffer_store_dwordx4 v[62:65], v0, s[0:3], 0 offen sc1
	v_or_b32_e32 v0, s6, v154
	v_mul_lo_u32 v69, v0, s4
	ds_read_b128 v[62:65], v92
	v_add_u32_e32 v0, v69, v113
	s_waitcnt lgkmcnt(2)
	buffer_store_dwordx4 v[70:73], v0, s[0:3], 0 offen sc1
	v_or_b32_e32 v0, s6, v155
	s_nop 0
	v_mul_lo_u32 v72, v0, s4
	v_add_u32_e32 v0, v72, v115
	s_waitcnt lgkmcnt(0)
	buffer_store_dwordx4 v[62:65], v0, s[0:3], 0 offen sc1
	v_add_u32_e32 v0, s6, v156
	v_mul_lo_u32 v70, v0, s4
	ds_read_b128 v[62:65], v100
	v_add_u32_e32 v0, v70, v117
	buffer_store_dwordx4 v[74:77], v0, s[0:3], 0 offen sc1
	v_or_b32_e32 v0, s6, v157
	v_mul_lo_u32 v71, v0, s4
	v_add_u32_e32 v0, v71, v144
	ds_read_b128 v[74:77], v110
	s_waitcnt lgkmcnt(1)
	buffer_store_dwordx4 v[62:65], v0, s[0:3], 0 offen sc1
	ds_read_b128 v[62:65], v135
	ds_read_b128 v[78:81], v135 offset:8192
	ds_read_b128 v[86:89], v135 offset:16384
	ds_read_b128 v[94:97], v135 offset:24576
	ds_read_b128 v[102:105], v135 offset:32768
	ds_read_b128 v[106:109], v135 offset:40960
	ds_read_b128 v[124:127], v135 offset:49152
	ds_read_b128 v[148:151], v135 offset:57344
	v_add_u32_e32 v0, s6, v147
	v_mul_lo_u32 v73, v0, s4
	v_add_u32_e32 v0, v73, v145
	s_waitcnt lgkmcnt(8)
	buffer_store_dwordx4 v[74:77], v0, s[0:3], 0 offen sc1
	s_waitcnt lgkmcnt(7)
	s_nop 0
	v_mfma_f32_16x16x32_f16 v[74:77], v[38:41], v[62:65], 0
	s_waitcnt lgkmcnt(6)
	v_mfma_f32_16x16x32_f16 v[152:155], v[38:41], v[78:81], 0
	s_waitcnt lgkmcnt(5)
	v_mfma_f32_16x16x32_f16 v[156:159], v[38:41], v[86:89], 0
	s_waitcnt lgkmcnt(4)
	v_mfma_f32_16x16x32_f16 v[160:163], v[38:41], v[94:97], 0
	s_waitcnt lgkmcnt(3)
	v_mfma_f32_16x16x32_f16 v[164:167], v[38:41], v[102:105], 0
	s_waitcnt lgkmcnt(2)
	v_mfma_f32_16x16x32_f16 v[168:171], v[38:41], v[106:109], 0
	s_waitcnt lgkmcnt(1)
	v_mfma_f32_16x16x32_f16 v[172:175], v[38:41], v[124:127], 0
	s_waitcnt lgkmcnt(0)
	v_mfma_f32_16x16x32_f16 v[38:41], v[38:41], v[148:151], 0
	v_mfma_f32_16x16x32_f16 v[176:179], v[26:29], v[62:65], 0
	v_mfma_f32_16x16x32_f16 v[180:183], v[26:29], v[78:81], 0
	v_mfma_f32_16x16x32_f16 v[184:187], v[26:29], v[86:89], 0
	v_mfma_f32_16x16x32_f16 v[188:191], v[26:29], v[94:97], 0
	v_mfma_f32_16x16x32_f16 v[192:195], v[26:29], v[102:105], 0
	v_mfma_f32_16x16x32_f16 v[196:199], v[26:29], v[106:109], 0
	v_mfma_f32_16x16x32_f16 v[200:203], v[26:29], v[124:127], 0
	v_mfma_f32_16x16x32_f16 v[26:29], v[26:29], v[148:151], 0
	v_mfma_f32_16x16x32_f16 v[62:65], v[10:13], v[62:65], 0
	v_mfma_f32_16x16x32_f16 v[78:81], v[10:13], v[78:81], 0
	v_mfma_f32_16x16x32_f16 v[86:89], v[10:13], v[86:89], 0
	v_mfma_f32_16x16x32_f16 v[94:97], v[10:13], v[94:97], 0
	v_mfma_f32_16x16x32_f16 v[102:105], v[10:13], v[102:105], 0
	v_mfma_f32_16x16x32_f16 v[106:109], v[10:13], v[106:109], 0
	v_mfma_f32_16x16x32_f16 v[124:127], v[10:13], v[124:127], 0
	v_mfma_f32_16x16x32_f16 v[10:13], v[10:13], v[148:151], 0
	s_mov_b32 s4, 0x34000
	v_add_co_u32_e32 v66, vcc, s4, v118
	s_mov_b32 s4, 0x35000
	s_nop 0
	v_addc_co_u32_e32 v67, vcc, 0, v119, vcc
	v_add_co_u32_e32 v118, vcc, s4, v118
	s_nop 1
	v_addc_co_u32_e32 v119, vcc, 0, v119, vcc
	global_load_dwordx4 v[148:151], v[118:119], off offset:-4096
	global_load_dwordx4 v[204:207], v[122:123], off offset:3072
	global_load_dwordx4 v[208:211], v[66:67], off offset:1024
	ds_read_b128 v[212:215], v133
	ds_read_b128 v[216:219], v133 offset:8192
	ds_read_b128 v[220:223], v133 offset:16384
	ds_read_b128 v[224:227], v133 offset:24576
	ds_read_b128 v[228:231], v133 offset:32768
	ds_read_b128 v[232:235], v133 offset:40960
	ds_read_b128 v[236:239], v133 offset:49152
	ds_read_b128 v[240:243], v133 offset:57344
	s_waitcnt lgkmcnt(7)
	v_mfma_f32_16x16x32_f16 v[74:77], v[22:25], v[212:215], v[74:77]
	s_waitcnt lgkmcnt(6)
	v_mfma_f32_16x16x32_f16 v[152:155], v[22:25], v[216:219], v[152:155]
	s_waitcnt lgkmcnt(5)
	v_mfma_f32_16x16x32_f16 v[156:159], v[22:25], v[220:223], v[156:159]
	s_waitcnt lgkmcnt(4)
	v_mfma_f32_16x16x32_f16 v[160:163], v[22:25], v[224:227], v[160:163]
	s_waitcnt lgkmcnt(3)
	v_mfma_f32_16x16x32_f16 v[164:167], v[22:25], v[228:231], v[164:167]
	s_waitcnt lgkmcnt(2)
	v_mfma_f32_16x16x32_f16 v[168:171], v[22:25], v[232:235], v[168:171]
	s_waitcnt lgkmcnt(1)
	v_mfma_f32_16x16x32_f16 v[172:175], v[22:25], v[236:239], v[172:175]
	s_waitcnt lgkmcnt(0)
	v_mfma_f32_16x16x32_f16 v[22:25], v[22:25], v[240:243], v[38:41]
	v_mfma_f32_16x16x32_f16 v[38:41], v[6:9], v[212:215], v[176:179]
	v_mfma_f32_16x16x32_f16 v[176:179], v[6:9], v[216:219], v[180:183]
	v_mfma_f32_16x16x32_f16 v[180:183], v[6:9], v[220:223], v[184:187]
	v_mfma_f32_16x16x32_f16 v[184:187], v[6:9], v[224:227], v[188:191]
	v_mfma_f32_16x16x32_f16 v[188:191], v[6:9], v[228:231], v[192:195]
	v_mfma_f32_16x16x32_f16 v[192:195], v[6:9], v[232:235], v[196:199]
	v_mfma_f32_16x16x32_f16 v[196:199], v[6:9], v[236:239], v[200:203]
	v_mfma_f32_16x16x32_f16 v[6:9], v[6:9], v[240:243], v[26:29]
	v_mfma_f32_16x16x32_f16 v[26:29], v[2:5], v[212:215], v[62:65]
	v_mfma_f32_16x16x32_f16 v[62:65], v[2:5], v[216:219], v[78:81]
	v_mfma_f32_16x16x32_f16 v[78:81], v[2:5], v[220:223], v[86:89]
	v_mfma_f32_16x16x32_f16 v[86:89], v[2:5], v[224:227], v[94:97]
	v_mfma_f32_16x16x32_f16 v[94:97], v[2:5], v[228:231], v[102:105]
	v_mfma_f32_16x16x32_f16 v[102:105], v[2:5], v[232:235], v[106:109]
	v_mfma_f32_16x16x32_f16 v[106:109], v[2:5], v[236:239], v[124:127]
	v_mfma_f32_16x16x32_f16 v[0:3], v[2:5], v[240:243], v[10:13]
	s_nop 2
	global_load_dwordx4 v[10:13], v[66:67], off offset:2048
	global_load_dwordx4 v[122:125], v[66:67], off offset:3072
	global_load_dwordx4 v[126:129], v[118:119], off
	ds_read_b128 v[200:203], v134
	ds_read_b128 v[212:215], v134 offset:8192
	ds_read_b128 v[216:219], v134 offset:16384
	ds_read_b128 v[220:223], v134 offset:24576
	ds_read_b128 v[224:227], v134 offset:32768
	ds_read_b128 v[228:231], v134 offset:40960
	ds_read_b128 v[232:235], v134 offset:49152
	ds_read_b128 v[236:239], v134 offset:57344
	s_waitcnt lgkmcnt(7)
	v_mfma_f32_16x16x32_f16 v[74:77], v[30:33], v[200:203], v[74:77]
	s_waitcnt lgkmcnt(6)
	v_mfma_f32_16x16x32_f16 v[152:155], v[30:33], v[212:215], v[152:155]
	s_waitcnt lgkmcnt(5)
	v_mfma_f32_16x16x32_f16 v[156:159], v[30:33], v[216:219], v[156:159]
	s_waitcnt lgkmcnt(4)
	v_mfma_f32_16x16x32_f16 v[160:163], v[30:33], v[220:223], v[160:163]
	s_waitcnt lgkmcnt(3)
	v_mfma_f32_16x16x32_f16 v[164:167], v[30:33], v[224:227], v[164:167]
	s_waitcnt lgkmcnt(2)
	v_mfma_f32_16x16x32_f16 v[168:171], v[30:33], v[228:231], v[168:171]
	s_waitcnt lgkmcnt(1)
	v_mfma_f32_16x16x32_f16 v[172:175], v[30:33], v[232:235], v[172:175]
	s_waitcnt lgkmcnt(0)
	v_mfma_f32_16x16x32_f16 v[22:25], v[30:33], v[236:239], v[22:25]
	v_mfma_f32_16x16x32_f16 v[30:33], v[14:17], v[200:203], v[38:41]
	v_mfma_f32_16x16x32_f16 v[38:41], v[14:17], v[212:215], v[176:179]
	v_mfma_f32_16x16x32_f16 v[176:179], v[14:17], v[216:219], v[180:183]
	v_mfma_f32_16x16x32_f16 v[180:183], v[14:17], v[220:223], v[184:187]
	v_mfma_f32_16x16x32_f16 v[184:187], v[14:17], v[224:227], v[188:191]
	v_mfma_f32_16x16x32_f16 v[188:191], v[14:17], v[228:231], v[192:195]
	v_mfma_f32_16x16x32_f16 v[192:195], v[14:17], v[232:235], v[196:199]
	v_mfma_f32_16x16x32_f16 v[4:7], v[14:17], v[236:239], v[6:9]
	v_mfma_f32_16x16x32_f16 v[14:17], v[18:21], v[200:203], v[26:29]
	v_mfma_f32_16x16x32_f16 v[26:29], v[18:21], v[212:215], v[62:65]
	v_mfma_f32_16x16x32_f16 v[62:65], v[18:21], v[216:219], v[78:81]
	v_mfma_f32_16x16x32_f16 v[78:81], v[18:21], v[220:223], v[86:89]
	v_mfma_f32_16x16x32_f16 v[86:89], v[18:21], v[224:227], v[94:97]
	v_mfma_f32_16x16x32_f16 v[94:97], v[18:21], v[228:231], v[102:105]
	v_mfma_f32_16x16x32_f16 v[102:105], v[18:21], v[232:235], v[106:109]
	v_mfma_f32_16x16x32_f16 v[0:3], v[18:21], v[236:239], v[0:3]
	global_load_dwordx4 v[18:21], v[118:119], off offset:1024
	s_nop 0
	global_load_dwordx4 v[106:109], v[118:119], off offset:2048
	global_load_dwordx4 v[196:199], v[118:119], off offset:3072
	ds_read_b128 v[200:203], v136
	ds_read_b128 v[212:215], v136 offset:8192
	ds_read_b128 v[216:219], v136 offset:16384
	ds_read_b128 v[220:223], v136 offset:24576
	ds_read_b128 v[224:227], v136 offset:32768
	ds_read_b128 v[228:231], v136 offset:40960
	ds_read_b128 v[232:235], v136 offset:49152
	ds_read_b128 v[236:239], v136 offset:57344
	s_waitcnt lgkmcnt(7)
	v_mfma_f32_16x16x32_f16 v[74:77], v[46:49], v[200:203], v[74:77]
	s_waitcnt lgkmcnt(6)
	v_mfma_f32_16x16x32_f16 v[152:155], v[46:49], v[212:215], v[152:155]
	s_waitcnt lgkmcnt(5)
	v_mfma_f32_16x16x32_f16 v[156:159], v[46:49], v[216:219], v[156:159]
	s_waitcnt lgkmcnt(4)
	v_mfma_f32_16x16x32_f16 v[160:163], v[46:49], v[220:223], v[160:163]
	s_waitcnt lgkmcnt(3)
	v_mfma_f32_16x16x32_f16 v[164:167], v[46:49], v[224:227], v[164:167]
	s_waitcnt lgkmcnt(2)
	v_mfma_f32_16x16x32_f16 v[168:171], v[46:49], v[228:231], v[168:171]
	s_waitcnt lgkmcnt(1)
	v_mfma_f32_16x16x32_f16 v[172:175], v[46:49], v[232:235], v[172:175]
	s_waitcnt lgkmcnt(0)
	v_mfma_f32_16x16x32_f16 v[22:25], v[46:49], v[236:239], v[22:25]
	v_mfma_f32_16x16x32_f16 v[30:33], v[42:45], v[200:203], v[30:33]
	v_mfma_f32_16x16x32_f16 v[38:41], v[42:45], v[212:215], v[38:41]
	v_mfma_f32_16x16x32_f16 v[46:49], v[42:45], v[216:219], v[176:179]
	v_mfma_f32_16x16x32_f16 v[176:179], v[42:45], v[220:223], v[180:183]
	v_mfma_f32_16x16x32_f16 v[180:183], v[42:45], v[224:227], v[184:187]
	v_mfma_f32_16x16x32_f16 v[184:187], v[42:45], v[228:231], v[188:191]
	v_mfma_f32_16x16x32_f16 v[188:191], v[42:45], v[232:235], v[192:195]
	v_mfma_f32_16x16x32_f16 v[4:7], v[42:45], v[236:239], v[4:7]
	v_mfma_f32_16x16x32_f16 v[14:17], v[34:37], v[200:203], v[14:17]
	v_mfma_f32_16x16x32_f16 v[26:29], v[34:37], v[212:215], v[26:29]
	v_mfma_f32_16x16x32_f16 v[42:45], v[34:37], v[216:219], v[62:65]
	v_mfma_f32_16x16x32_f16 v[62:65], v[34:37], v[220:223], v[78:81]
	v_mfma_f32_16x16x32_f16 v[78:81], v[34:37], v[224:227], v[86:89]
	v_mfma_f32_16x16x32_f16 v[86:89], v[34:37], v[228:231], v[94:97]
	v_mfma_f32_16x16x32_f16 v[94:97], v[34:37], v[232:235], v[102:105]
	v_mfma_f32_16x16x32_f16 v[0:3], v[34:37], v[236:239], v[0:3]
	ds_read_b128 v[34:37], v137
	s_nop 0
	ds_read_b128 v[102:105], v137 offset:8192
	ds_read_b128 v[192:195], v137 offset:16384
	ds_read_b128 v[200:203], v137 offset:24576
	ds_read_b128 v[212:215], v137 offset:32768
	ds_read_b128 v[216:219], v137 offset:40960
	ds_read_b128 v[220:223], v137 offset:49152
	ds_read_b128 v[134:137], v137 offset:57344
	s_waitcnt vmcnt(17) lgkmcnt(7)
	v_mfma_f32_16x16x32_f16 v[74:77], v[50:53], v[34:37], v[74:77]
	s_waitcnt lgkmcnt(6)
	v_mfma_f32_16x16x32_f16 v[152:155], v[50:53], v[102:105], v[152:155]
	s_waitcnt lgkmcnt(5)
	v_mfma_f32_16x16x32_f16 v[156:159], v[50:53], v[192:195], v[156:159]
	s_waitcnt lgkmcnt(4)
	v_mfma_f32_16x16x32_f16 v[160:163], v[50:53], v[200:203], v[160:163]
	s_waitcnt lgkmcnt(3)
	v_mfma_f32_16x16x32_f16 v[164:167], v[50:53], v[212:215], v[164:167]
	s_waitcnt lgkmcnt(2)
	v_mfma_f32_16x16x32_f16 v[168:171], v[50:53], v[216:219], v[168:171]
	s_waitcnt lgkmcnt(1)
	v_mfma_f32_16x16x32_f16 v[172:175], v[50:53], v[220:223], v[172:175]
	s_waitcnt lgkmcnt(0)
	v_mfma_f32_16x16x32_f16 v[22:25], v[50:53], v[134:137], v[22:25]
	s_waitcnt vmcnt(16)
	v_mfma_f32_16x16x32_f16 v[30:33], v[54:57], v[34:37], v[30:33]
	v_mfma_f32_16x16x32_f16 v[38:41], v[54:57], v[102:105], v[38:41]
	v_mfma_f32_16x16x32_f16 v[46:49], v[54:57], v[192:195], v[46:49]
	v_mfma_f32_16x16x32_f16 v[50:53], v[54:57], v[200:203], v[176:179]
	v_mfma_f32_16x16x32_f16 v[176:179], v[54:57], v[212:215], v[180:183]
	v_mfma_f32_16x16x32_f16 v[180:183], v[54:57], v[216:219], v[184:187]
	v_mfma_f32_16x16x32_f16 v[184:187], v[54:57], v[220:223], v[188:191]
	v_mfma_f32_16x16x32_f16 v[4:7], v[54:57], v[134:137], v[4:7]
	s_waitcnt vmcnt(15)
	v_mfma_f32_16x16x32_f16 v[14:17], v[58:61], v[34:37], v[14:17]
	v_mfma_f32_16x16x32_f16 v[26:29], v[58:61], v[102:105], v[26:29]
	v_mfma_f32_16x16x32_f16 v[34:37], v[58:61], v[192:195], v[42:45]
	v_mfma_f32_16x16x32_f16 v[42:45], v[58:61], v[200:203], v[62:65]
	v_mfma_f32_16x16x32_f16 v[54:57], v[58:61], v[212:215], v[78:81]
	v_mfma_f32_16x16x32_f16 v[62:65], v[58:61], v[216:219], v[86:89]
	v_mfma_f32_16x16x32_f16 v[78:81], v[58:61], v[220:223], v[94:97]
	v_mfma_f32_16x16x32_f16 v[0:3], v[58:61], v[134:137], v[0:3]
	ds_read_b128 v[58:61], v138
	ds_read_b128 v[86:89], v138 offset:8192
	ds_read_b128 v[94:97], v138 offset:16384
	ds_read_b128 v[102:105], v138 offset:24576
	ds_read_b128 v[134:137], v138 offset:32768
	ds_read_b128 v[188:191], v138 offset:40960
	ds_read_b128 v[192:195], v138 offset:49152
	ds_read_b128 v[200:203], v138 offset:57344
	s_waitcnt vmcnt(7) lgkmcnt(7)
	v_mfma_f32_16x16x32_f16 v[74:77], v[204:207], v[58:61], v[74:77]
	s_waitcnt lgkmcnt(6)
	v_mfma_f32_16x16x32_f16 v[152:155], v[204:207], v[86:89], v[152:155]
	s_waitcnt lgkmcnt(5)
	v_mfma_f32_16x16x32_f16 v[156:159], v[204:207], v[94:97], v[156:159]
	s_waitcnt lgkmcnt(4)
	v_mfma_f32_16x16x32_f16 v[160:163], v[204:207], v[102:105], v[160:163]
	s_waitcnt lgkmcnt(3)
	v_mfma_f32_16x16x32_f16 v[164:167], v[204:207], v[134:137], v[164:167]
	s_waitcnt lgkmcnt(2)
	v_mfma_f32_16x16x32_f16 v[168:171], v[204:207], v[188:191], v[168:171]
	s_waitcnt lgkmcnt(1)
	v_mfma_f32_16x16x32_f16 v[172:175], v[204:207], v[192:195], v[172:175]
	s_waitcnt lgkmcnt(0)
	v_mfma_f32_16x16x32_f16 v[22:25], v[204:207], v[200:203], v[22:25]
	v_mfma_f32_16x16x32_f16 v[30:33], v[148:151], v[58:61], v[30:33]
	v_mfma_f32_16x16x32_f16 v[38:41], v[148:151], v[86:89], v[38:41]
	v_mfma_f32_16x16x32_f16 v[46:49], v[148:151], v[94:97], v[46:49]
	v_mfma_f32_16x16x32_f16 v[50:53], v[148:151], v[102:105], v[50:53]
	v_mfma_f32_16x16x32_f16 v[176:179], v[148:151], v[134:137], v[176:179]
	v_mfma_f32_16x16x32_f16 v[180:183], v[148:151], v[188:191], v[180:183]
	v_mfma_f32_16x16x32_f16 v[184:187], v[148:151], v[192:195], v[184:187]
	v_mfma_f32_16x16x32_f16 v[4:7], v[148:151], v[200:203], v[4:7]
	s_waitcnt vmcnt(6)
	v_mfma_f32_16x16x32_f16 v[14:17], v[208:211], v[58:61], v[14:17]
	v_mfma_f32_16x16x32_f16 v[26:29], v[208:211], v[86:89], v[26:29]
	v_mfma_f32_16x16x32_f16 v[34:37], v[208:211], v[94:97], v[34:37]
	v_mfma_f32_16x16x32_f16 v[42:45], v[208:211], v[102:105], v[42:45]
	v_mfma_f32_16x16x32_f16 v[54:57], v[208:211], v[134:137], v[54:57]
	v_mfma_f32_16x16x32_f16 v[58:61], v[208:211], v[188:191], v[62:65]
	v_mfma_f32_16x16x32_f16 v[62:65], v[208:211], v[192:195], v[78:81]
	v_mfma_f32_16x16x32_f16 v[0:3], v[208:211], v[200:203], v[0:3]
	s_nop 1
	ds_read_b128 v[78:81], v139
	ds_read_b128 v[86:89], v139 offset:8192
	ds_read_b128 v[94:97], v139 offset:16384
	ds_read_b128 v[102:105], v139 offset:24576
	ds_read_b128 v[134:137], v139 offset:32768
	ds_read_b128 v[148:151], v139 offset:40960
	ds_read_b128 v[188:191], v139 offset:49152
	ds_read_b128 v[192:195], v139 offset:57344
	s_waitcnt vmcnt(5) lgkmcnt(7)
	v_mfma_f32_16x16x32_f16 v[74:77], v[10:13], v[78:81], v[74:77]
	s_waitcnt lgkmcnt(6)
	v_mfma_f32_16x16x32_f16 v[152:155], v[10:13], v[86:89], v[152:155]
	s_waitcnt lgkmcnt(5)
	v_mfma_f32_16x16x32_f16 v[156:159], v[10:13], v[94:97], v[156:159]
	s_waitcnt lgkmcnt(4)
	v_mfma_f32_16x16x32_f16 v[160:163], v[10:13], v[102:105], v[160:163]
	s_waitcnt lgkmcnt(3)
	v_mfma_f32_16x16x32_f16 v[164:167], v[10:13], v[134:137], v[164:167]
	s_waitcnt lgkmcnt(2)
	v_mfma_f32_16x16x32_f16 v[168:171], v[10:13], v[148:151], v[168:171]
	s_waitcnt lgkmcnt(1)
	v_mfma_f32_16x16x32_f16 v[172:175], v[10:13], v[188:191], v[172:175]
	s_waitcnt lgkmcnt(0)
	v_mfma_f32_16x16x32_f16 v[8:11], v[10:13], v[192:195], v[22:25]
	s_waitcnt vmcnt(4)
	v_mfma_f32_16x16x32_f16 v[22:25], v[122:125], v[78:81], v[30:33]
	v_mfma_f32_16x16x32_f16 v[30:33], v[122:125], v[86:89], v[38:41]
	v_mfma_f32_16x16x32_f16 v[200:203], v[122:125], v[94:97], v[46:49]
	v_mfma_f32_16x16x32_f16 v[48:51], v[122:125], v[102:105], v[50:53]
	v_mfma_f32_16x16x32_f16 v[176:179], v[122:125], v[134:137], v[176:179]
	v_mfma_f32_16x16x32_f16 v[180:183], v[122:125], v[148:151], v[180:183]
	v_mfma_f32_16x16x32_f16 v[184:187], v[122:125], v[188:191], v[184:187]
	v_mfma_f32_16x16x32_f16 v[4:7], v[122:125], v[192:195], v[4:7]
	s_waitcnt vmcnt(3)
	v_mfma_f32_16x16x32_f16 v[12:15], v[126:129], v[78:81], v[14:17]
	v_mfma_f32_16x16x32_f16 v[78:81], v[126:129], v[86:89], v[26:29]
	v_mfma_f32_16x16x32_f16 v[86:89], v[126:129], v[94:97], v[34:37]
	v_mfma_f32_16x16x32_f16 v[40:43], v[126:129], v[102:105], v[42:45]
	v_mfma_f32_16x16x32_f16 v[94:97], v[126:129], v[134:137], v[54:57]
	v_mfma_f32_16x16x32_f16 v[102:105], v[126:129], v[148:151], v[58:61]
	v_mfma_f32_16x16x32_f16 v[64:67], v[126:129], v[188:191], v[62:65]
	v_mfma_f32_16x16x32_f16 v[0:3], v[126:129], v[192:195], v[0:3]
	s_nop 1
	ds_read_b128 v[60:63], v141
	ds_read_b128 v[122:125], v141 offset:8192
	ds_read_b128 v[126:129], v141 offset:16384
	ds_read_b128 v[134:137], v141 offset:24576
	ds_read_b128 v[148:151], v141 offset:32768
	ds_read_b128 v[188:191], v141 offset:40960
	ds_read_b128 v[192:195], v141 offset:49152
	ds_read_b128 v[138:141], v141 offset:57344
	s_waitcnt vmcnt(2) lgkmcnt(7)
	v_mfma_f32_16x16x32_f16 v[74:77], v[18:21], v[60:63], v[74:77]
	s_waitcnt lgkmcnt(6)
	v_mfma_f32_16x16x32_f16 v[152:155], v[18:21], v[122:125], v[152:155]
	s_waitcnt lgkmcnt(5)
	v_mfma_f32_16x16x32_f16 v[156:159], v[18:21], v[126:129], v[156:159]
	s_waitcnt lgkmcnt(4)
	v_mfma_f32_16x16x32_f16 v[160:163], v[18:21], v[134:137], v[160:163]
	s_waitcnt lgkmcnt(3)
	v_mfma_f32_16x16x32_f16 v[56:59], v[18:21], v[148:151], v[164:167]
	s_waitcnt lgkmcnt(2)
	v_mfma_f32_16x16x32_f16 v[52:55], v[18:21], v[188:191], v[168:171]
	s_waitcnt lgkmcnt(1)
	v_mfma_f32_16x16x32_f16 v[44:47], v[18:21], v[192:195], v[172:175]
	s_waitcnt lgkmcnt(0)
	v_mfma_f32_16x16x32_f16 v[36:39], v[18:21], v[138:141], v[8:11]
	s_waitcnt vmcnt(1)
	v_mfma_f32_16x16x32_f16 v[164:167], v[106:109], v[60:63], v[22:25]
	v_mfma_f32_16x16x32_f16 v[168:171], v[106:109], v[122:125], v[30:33]
	v_mfma_f32_16x16x32_f16 v[172:175], v[106:109], v[126:129], v[200:203]
	v_mfma_f32_16x16x32_f16 v[200:203], v[106:109], v[134:137], v[48:51]
	v_mfma_f32_16x16x32_f16 v[32:35], v[106:109], v[148:151], v[176:179]
	v_mfma_f32_16x16x32_f16 v[24:27], v[106:109], v[188:191], v[180:183]
	v_mfma_f32_16x16x32_f16 v[20:23], v[106:109], v[192:195], v[184:187]
	v_mfma_f32_16x16x32_f16 v[16:19], v[106:109], v[138:141], v[4:7]
	s_waitcnt vmcnt(0)
	v_mfma_f32_16x16x32_f16 v[106:109], v[196:199], v[60:63], v[12:15]
	v_mfma_f32_16x16x32_f16 v[78:81], v[196:199], v[122:125], v[78:81]
	v_mfma_f32_16x16x32_f16 v[86:89], v[196:199], v[126:129], v[86:89]
	v_mfma_f32_16x16x32_f16 v[60:63], v[196:199], v[134:137], v[40:43]
	v_mfma_f32_16x16x32_f16 v[12:15], v[196:199], v[148:151], v[94:97]
	v_mfma_f32_16x16x32_f16 v[8:11], v[196:199], v[188:191], v[102:105]
	v_mfma_f32_16x16x32_f16 v[4:7], v[196:199], v[192:195], v[64:67]
	v_mfma_f32_16x16x32_f16 v[0:3], v[196:199], v[138:141], v[0:3]
	global_load_dwordx4 v[48:51], v[120:121], off offset:1536
	global_load_dwordx4 v[40:43], v[120:121], off offset:1600
	global_load_dwordx4 v[28:31], v[120:121], off offset:1664
	v_mov_b32_e32 v94, v157
	v_mov_b32_e32 v95, v158
	v_mov_b32_e32 v96, v161
	v_mov_b32_e32 v97, v162
	v_mov_b32_e32 v64, v153
	v_mov_b32_e32 v65, v154
	v_mov_b32_e32 v102, v169
	v_mov_b32_e32 v103, v170
	v_mov_b32_e32 v104, v173
	v_mov_b32_e32 v105, v174
	v_mov_b32_e32 v118, v201
	v_mov_b32_e32 v119, v202
	s_barrier
	s_waitcnt vmcnt(2)
	v_pk_add_f32 v[74:75], v[74:75], v[48:49]
	v_add_f32_e32 v82, v152, v48
	v_pk_mov_b32 v[120:121], v[48:49], v[50:51] op_sel:[1,0]
	v_add_f32_e32 v49, v155, v51
	s_waitcnt vmcnt(1)
	v_pk_add_f32 v[122:123], v[164:165], v[40:41]
	v_add_f32_e32 v98, v168, v40
	v_pk_mov_b32 v[66:67], v[40:41], v[42:43] op_sel:[1,0]
	v_add_f32_e32 v41, v171, v43
	v_pk_add_f32 v[76:77], v[76:77], v[50:51]
	v_add_f32_e32 v50, v156, v48
	v_add_f32_e32 v85, v159, v51
	v_add_f32_e32 v90, v160, v48
	v_add_f32_e32 v93, v163, v51
	v_pk_add_f32 v[124:125], v[166:167], v[42:43]
	v_add_f32_e32 v42, v172, v40
	v_add_f32_e32 v101, v175, v43
	v_add_f32_e32 v126, v200, v40
	v_add_f32_e32 v127, v203, v43
	v_cvt_f16_f32_e32 v82, v82
	v_cvt_f16_f32_e32 v49, v49
	v_cvt_f16_f32_e32 v98, v98
	v_cvt_f16_f32_e32 v41, v41
	v_cvt_pk_f16_f32 v74, v74, v75
	v_cvt_pk_f16_f32 v75, v76, v77
	v_cvt_f16_f32_e32 v50, v50
	v_pk_add_f32 v[76:77], v[94:95], v[120:121]
	v_cvt_f16_f32_e32 v85, v85
	v_cvt_f16_f32_e32 v90, v90
	v_pk_add_f32 v[94:95], v[96:97], v[120:121]
	v_cvt_f16_f32_e32 v93, v93
	v_cvt_pk_f16_f32 v96, v122, v123
	v_cvt_f16_f32_e32 v42, v42
	v_cvt_f16_f32_e32 v101, v101
	v_cvt_f16_f32_e32 v122, v126
	v_cvt_f16_f32_e32 v123, v127
	v_pk_add_f32 v[64:65], v[64:65], v[120:121]
	v_pk_add_f32 v[102:103], v[102:103], v[66:67]
	v_pk_add_f32 v[104:105], v[104:105], v[66:67]
	v_pk_add_f32 v[118:119], v[118:119], v[66:67]
	v_cvt_pk_f16_f32 v65, v64, v65
	v_cvt_pk_f16_f32 v76, v76, v77
	v_cvt_pk_f16_f32 v77, v94, v95
	v_cvt_pk_f16_f32 v95, v102, v103
	s_waitcnt vmcnt(0)
	v_pk_add_f32 v[106:107], v[106:107], v[28:29]
	v_pk_add_f32 v[108:109], v[108:109], v[30:31]
	v_cvt_pk_f16_f32 v97, v124, v125
	v_cvt_pk_f16_f32 v102, v104, v105
	v_cvt_pk_f16_f32 v103, v118, v119
	v_pack_b32_f16 v64, v82, v65
	v_alignbit_b32 v65, v49, v65, 16
	v_pack_b32_f16 v94, v98, v95
	v_alignbit_b32 v95, v41, v95, 16
	v_add_f32_e32 v78, v78, v28
	v_cvt_pk_f16_f32 v106, v106, v107
	v_cvt_pk_f16_f32 v107, v108, v109
	ds_write2_b64 v130, v[74:75], v[96:97] offset1:4
	ds_write_b64 v130, v[106:107] offset:64
	v_pack_b32_f16 v74, v50, v76
	v_alignbit_b32 v75, v85, v76, 16
	v_pack_b32_f16 v76, v90, v77
	v_alignbit_b32 v77, v93, v77, 16
	v_pack_b32_f16 v96, v42, v102
	v_alignbit_b32 v97, v101, v102, 16
	v_pack_b32_f16 v102, v122, v103
	v_alignbit_b32 v103, v123, v103, 16
	ds_write2_b64 v132, v[64:65], v[94:95] offset0:32 offset1:36
	ds_write2_b64 v131, v[74:75], v[96:97] offset0:64 offset1:68
	ds_write2_b64 v91, v[76:77], v[102:103] offset0:96 offset1:100
	v_pk_mov_b32 v[64:65], v[28:29], v[30:31] op_sel:[1,0]
	v_add_f32_e32 v29, v81, v31
	v_cvt_f16_f32_e32 v78, v78
	v_cvt_f16_f32_e32 v29, v29
	v_mov_b32_e32 v74, v79
	v_mov_b32_e32 v75, v80
	v_pk_add_f32 v[74:75], v[74:75], v[64:65]
	v_add_f32_e32 v56, v56, v48
	v_cvt_pk_f16_f32 v30, v74, v75
	v_pack_b32_f16 v74, v78, v30
	v_alignbit_b32 v75, v29, v30, 16
	v_add_f32_e32 v29, v86, v28
	v_add_f32_e32 v30, v89, v31
	v_cvt_f16_f32_e32 v29, v29
	v_cvt_f16_f32_e32 v30, v30
	ds_write_b64 v130, v[74:75] offset:12608
	v_mov_b32_e32 v74, v87
	v_mov_b32_e32 v75, v88
	v_pk_add_f32 v[74:75], v[74:75], v[64:65]
	v_add_f32_e32 v52, v52, v48
	v_cvt_pk_f16_f32 v41, v74, v75
	v_pack_b32_f16 v74, v29, v41
	v_alignbit_b32 v75, v30, v41, 16
	v_add_f32_e32 v29, v60, v28
	v_add_f32_e32 v30, v63, v31
	v_cvt_f16_f32_e32 v29, v29
	v_cvt_f16_f32_e32 v30, v30
	v_mov_b32_e32 v60, v61
	v_mov_b32_e32 v61, v62
	v_pk_add_f32 v[60:61], v[60:61], v[64:65]
	ds_write_b64 v130, v[74:75] offset:25152
	v_cvt_pk_f16_f32 v41, v60, v61
	v_pack_b32_f16 v60, v29, v41
	v_alignbit_b32 v61, v30, v41, 16
	ds_write_b64 v130, v[60:61] offset:37696
	s_waitcnt lgkmcnt(0)
	s_barrier
	ds_read_b128 v[60:63], v83
	ds_read_b128 v[74:77], v84
	v_add_u32_e32 v29, 0x300, v111
	v_add_u32_e32 v30, v29, v112
	v_add_f32_e32 v44, v44, v48
	s_waitcnt lgkmcnt(1)
	buffer_store_dwordx4 v[60:63], v30, s[0:3], 0 offen sc1
	v_add_u32_e32 v30, 0x300, v113
	ds_read_b128 v[60:63], v92
	v_add_u32_e32 v41, v30, v114
	s_waitcnt lgkmcnt(1)
	buffer_store_dwordx4 v[74:77], v41, s[0:3], 0 offen sc1
	ds_read_b128 v[74:77], v99
	v_add_u32_e32 v41, 0x300, v115
	v_add_u32_e32 v42, v41, v116
	s_waitcnt lgkmcnt(1)
	buffer_store_dwordx4 v[60:63], v42, s[0:3], 0 offen sc1
	v_add_u32_e32 v42, 0x300, v117
	ds_read_b128 v[60:63], v100
	v_add_u32_e32 v49, v42, v142
	s_waitcnt lgkmcnt(1)
	buffer_store_dwordx4 v[74:77], v49, s[0:3], 0 offen sc1
	ds_read_b128 v[74:77], v110
	v_add_u32_e32 v49, 0x300, v144
	v_add_u32_e32 v50, v49, v143
	s_waitcnt lgkmcnt(1)
	buffer_store_dwordx4 v[60:63], v50, s[0:3], 0 offen sc1
	v_add_u32_e32 v50, 0x300, v145
	v_add_f32_e32 v36, v36, v48
	v_add_u32_e32 v60, v50, v146
	s_waitcnt lgkmcnt(0)
	buffer_store_dwordx4 v[74:77], v60, s[0:3], 0 offen sc1
	v_cvt_f16_f32_e32 v60, v56
	v_mov_b32_e32 v56, v57
	v_mov_b32_e32 v57, v58
	v_add_f32_e32 v58, v59, v51
	v_cvt_f16_f32_e32 v58, v58
	v_pk_add_f32 v[56:57], v[56:57], v[120:121]
	v_add_f32_e32 v32, v32, v40
	v_cvt_pk_f16_f32 v57, v56, v57
	v_pack_b32_f16 v56, v60, v57
	v_alignbit_b32 v57, v58, v57, 16
	v_cvt_f16_f32_e32 v58, v52
	v_mov_b32_e32 v52, v53
	v_mov_b32_e32 v53, v54
	v_add_f32_e32 v54, v55, v51
	v_cvt_f16_f32_e32 v54, v54
	v_pk_add_f32 v[52:53], v[52:53], v[120:121]
	v_add_f32_e32 v24, v24, v40
	v_cvt_pk_f16_f32 v53, v52, v53
	v_pack_b32_f16 v52, v58, v53
	v_alignbit_b32 v53, v54, v53, 16
	v_cvt_f16_f32_e32 v54, v44
	v_mov_b32_e32 v44, v45
	v_mov_b32_e32 v45, v46
	v_add_f32_e32 v46, v47, v51
	v_cvt_f16_f32_e32 v46, v46
	v_pk_add_f32 v[44:45], v[44:45], v[120:121]
	s_nop 0
	v_cvt_pk_f16_f32 v45, v44, v45
	v_pack_b32_f16 v44, v54, v45
	v_alignbit_b32 v45, v46, v45, 16
	v_cvt_f16_f32_e32 v46, v36
	v_mov_b32_e32 v36, v37
	v_mov_b32_e32 v37, v38
	v_add_f32_e32 v38, v39, v51
	v_cvt_f16_f32_e32 v38, v38
	v_pk_add_f32 v[36:37], v[36:37], v[120:121]
	s_barrier
	v_cvt_pk_f16_f32 v37, v36, v37
	v_pack_b32_f16 v36, v46, v37
	v_alignbit_b32 v37, v38, v37, 16
	v_cvt_f16_f32_e32 v38, v32
	v_mov_b32_e32 v32, v33
	v_mov_b32_e32 v33, v34
	v_add_f32_e32 v34, v35, v43
	v_cvt_f16_f32_e32 v34, v34
	v_pk_add_f32 v[32:33], v[32:33], v[66:67]
	s_nop 0
	v_cvt_pk_f16_f32 v33, v32, v33
	v_pack_b32_f16 v32, v38, v33
	v_alignbit_b32 v33, v34, v33, 16
	ds_write2_b64 v130, v[56:57], v[32:33] offset1:4
	v_cvt_f16_f32_e32 v32, v24
	v_mov_b32_e32 v24, v25
	v_mov_b32_e32 v25, v26
	v_add_f32_e32 v26, v27, v43
	v_cvt_f16_f32_e32 v26, v26
	v_pk_add_f32 v[24:25], v[24:25], v[66:67]
	v_add_f32_e32 v20, v20, v40
	v_cvt_pk_f16_f32 v25, v24, v25
	v_pack_b32_f16 v24, v32, v25
	v_alignbit_b32 v25, v26, v25, 16
	ds_write2_b64 v132, v[52:53], v[24:25] offset0:32 offset1:36
	v_cvt_f16_f32_e32 v24, v20
	v_mov_b32_e32 v20, v21
	v_mov_b32_e32 v21, v22
	v_add_f32_e32 v22, v23, v43
	v_cvt_f16_f32_e32 v22, v22
	v_pk_add_f32 v[20:21], v[20:21], v[66:67]
	v_add_f32_e32 v16, v16, v40
	v_cvt_pk_f16_f32 v21, v20, v21
	v_pack_b32_f16 v20, v24, v21
	v_alignbit_b32 v21, v22, v21, 16
	ds_write2_b64 v131, v[44:45], v[20:21] offset0:64 offset1:68
	v_cvt_f16_f32_e32 v20, v16
	v_mov_b32_e32 v16, v17
	v_mov_b32_e32 v17, v18
	v_add_f32_e32 v18, v19, v43
	v_cvt_f16_f32_e32 v18, v18
	v_pk_add_f32 v[16:17], v[16:17], v[66:67]
	v_add_f32_e32 v12, v12, v28
	v_cvt_pk_f16_f32 v17, v16, v17
	v_pack_b32_f16 v16, v20, v17
	v_alignbit_b32 v17, v18, v17, 16
	ds_write2_b64 v91, v[36:37], v[16:17] offset0:96 offset1:100
	v_cvt_f16_f32_e32 v16, v12
	v_mov_b32_e32 v12, v13
	v_mov_b32_e32 v13, v14
	v_add_f32_e32 v14, v15, v31
	v_cvt_f16_f32_e32 v14, v14
	v_pk_add_f32 v[12:13], v[12:13], v[64:65]
	v_add_f32_e32 v8, v8, v28
	v_cvt_pk_f16_f32 v13, v12, v13
	v_pack_b32_f16 v12, v16, v13
	v_alignbit_b32 v13, v14, v13, 16
	ds_write_b64 v130, v[12:13] offset:64
	v_cvt_f16_f32_e32 v12, v8
	v_mov_b32_e32 v8, v9
	v_mov_b32_e32 v9, v10
	v_add_f32_e32 v10, v11, v31
	v_cvt_f16_f32_e32 v10, v10
	v_pk_add_f32 v[8:9], v[8:9], v[64:65]
	v_add_f32_e32 v4, v4, v28
	v_cvt_pk_f16_f32 v9, v8, v9
	v_pack_b32_f16 v8, v12, v9
	v_alignbit_b32 v9, v10, v9, 16
	ds_write_b64 v130, v[8:9] offset:12608
	v_cvt_f16_f32_e32 v8, v4
	v_mov_b32_e32 v4, v5
	v_mov_b32_e32 v5, v6
	v_add_f32_e32 v6, v7, v31
	v_cvt_f16_f32_e32 v6, v6
	v_pk_add_f32 v[4:5], v[4:5], v[64:65]
	v_add_f32_e32 v0, v0, v28
	v_cvt_pk_f16_f32 v5, v4, v5
	v_pack_b32_f16 v4, v8, v5
	v_alignbit_b32 v5, v6, v5, 16
	ds_write_b64 v130, v[4:5] offset:25152
	v_cvt_f16_f32_e32 v4, v0
	v_mov_b32_e32 v0, v1
	v_mov_b32_e32 v1, v2
	v_add_f32_e32 v2, v3, v31
	v_cvt_f16_f32_e32 v2, v2
	v_pk_add_f32 v[0:1], v[0:1], v[64:65]
	v_add_u32_e32 v8, v29, v68
	v_cvt_pk_f16_f32 v1, v0, v1
	v_pack_b32_f16 v0, v4, v1
	v_alignbit_b32 v1, v2, v1, 16
	ds_write_b64 v130, v[0:1] offset:37696
	s_waitcnt lgkmcnt(0)
	s_barrier
	ds_read_b128 v[0:3], v83
	ds_read_b128 v[4:7], v84
	v_add_u32_e32 v12, v42, v70
	s_waitcnt lgkmcnt(1)
	buffer_store_dwordx4 v[0:3], v8, s[0:3], 0 offen sc1
	ds_read_b128 v[0:3], v92
	v_add_u32_e32 v8, v30, v69
	s_waitcnt lgkmcnt(1)
	buffer_store_dwordx4 v[4:7], v8, s[0:3], 0 offen sc1
	v_add_u32_e32 v8, v41, v72
	ds_read_b128 v[4:7], v99
	s_waitcnt lgkmcnt(1)
	buffer_store_dwordx4 v[0:3], v8, s[0:3], 0 offen sc1
	ds_read_b128 v[0:3], v100
	ds_read_b128 v[8:11], v110
	s_waitcnt lgkmcnt(2)
	buffer_store_dwordx4 v[4:7], v12, s[0:3], 0 offen sc1
	s_nop 1
	v_add_u32_e32 v4, v49, v71
	s_waitcnt lgkmcnt(1)
	buffer_store_dwordx4 v[0:3], v4, s[0:3], 0 offen sc1
	s_nop 1
	v_add_u32_e32 v0, v50, v73
	s_waitcnt lgkmcnt(0)
	buffer_store_dwordx4 v[8:11], v0, s[0:3], 0 offen sc1
	s_endpgm
	.p2alignl 8, 3212836864

_Z7k_stageILi1ELi4EEv8AttnArgsPKDF16_PKfPDF16_iii:
	v_readfirstlane_b32 s94, v0
	s_nop 0
	s_lshr_b32 s94, s94, 6
	s_load_dwordx4 s[28:31], s[0:1], 0x70
	s_load_dwordx2 s[24:25], s[0:1], 0x80
	s_load_dword s33, s[0:1], 0x90
	s_lshl_b32 s4, s2, 5
	s_and_b32 s45, s4, 0xe0
	s_lshr_b32 s4, s2, 3
	s_add_i32 s45, s45, s4
	s_and_b32 s44, s2, 56
	v_readfirstlane_b32 s3, v0
	v_and_b32_e32 v1, 15, v0
	s_waitcnt lgkmcnt(0)
	s_cmp_lt_i32 s33, 1
	v_bfe_u32 v167, v0, 4, 2
	s_cbranch_scc1 .LBB4_155
	s_lshr_b32 s2, s3, 2
	v_lshrrev_b32_e32 v7, 7, v0
	v_lshrrev_b32_e32 v2, 5, v0
	v_lshrrev_b32_e32 v3, 4, v0
	s_and_b32 s2, s2, 16
	v_lshrrev_b32_e32 v4, 6, v0
	v_and_b32_e32 v7, 1, v7
	v_and_b32_e32 v2, 4, v2
	v_or_b32_e32 v179, s2, v1
	v_and_b32_e32 v5, 4, v4
	s_load_dwordx2 s[40:41], s[0:1], 0x60
	s_bitcmp1_b32 s3, 6
	v_lshlrev_b16_e32 v7, 2, v7
	v_and_b32_e32 v8, 3, v3
	s_load_dwordx4 s[36:39], s[0:1], 0x0
	s_load_dwordx2 s[4:5], s[0:1], 0x10
	s_load_dwordx8 s[8:15], s[0:1], 0x18
	s_load_dwordx2 s[6:7], s[0:1], 0x38
	s_load_dwordx8 s[16:23], s[0:1], 0x40
	v_or_b32_e32 v178, v2, v167
	v_and_or_b32 v180, s45, 56, v5
	s_cselect_b64 s[26:27], -1, 0
	s_and_b32 s3, s45, 0x3ffffc0
	v_bitop3_b16 v3, v7, v3, 3 bitop3:0xf8
	v_bitop3_b16 v7, v7, 8, v8 bitop3:0xfe
	v_lshlrev_b32_e32 v8, 12, v5
	v_bitop3_b32 v2, v2, v179, v167 bitop3:0x36
	v_or_b32_e32 v6, s3, v180
	s_and_b32 s3, s45, 0x1ffc0
	v_and_b32_e32 v3, 0xffff, v3
	v_lshl_or_b32 v184, v2, 4, v8
	v_lshlrev_b32_e32 v2, 3, v5
	v_mov_b32_e32 v169, 0
	v_lshlrev_b32_e32 v168, 5, v179
	v_lshlrev_b32_e32 v181, 6, v6
	v_or_b32_e32 v6, s3, v180
	v_and_b32_e32 v7, 0xffff, v7
	v_or_b32_e32 v186, 8, v2
	v_or_b32_e32 v188, 16, v2
	v_bitop3_b32 v2, s2, v3, v1 bitop3:0x36
	v_lshlrev_b32_e32 v166, 3, v179
	s_waitcnt lgkmcnt(0)
	v_lshl_add_u64 v[170:171], s[38:39], 0, v[168:169]
	s_mov_b32 s39, 0x20000
	v_lshlrev_b32_e32 v189, 4, v2
	v_bitop3_b32 v2, s2, v7, v1 bitop3:0x36
	v_lshlrev_b32_e32 v193, 15, v6
	v_lshl_add_u64 v[172:173], s[4:5], 0, v[168:169]
	s_and_b32 s37, s37, 0xffff
	s_mov_b32 s38, 0x1800000
	v_add_u32_e32 v182, -1, v180
	v_add_u32_e32 v183, 4, v180
	v_lshl_add_u64 v[174:175], s[14:15], 0, v[168:169]
	v_lshl_add_u64 v[176:177], s[6:7], 0, v[168:169]
	s_and_b32 s13, s13, 0xffff
	s_mov_b32 s42, 0x800000
	s_mov_b32 s43, s39
	s_and_b32 s41, s41, 0xffff
	v_or_b32_e32 v185, 64, v181
	v_or_b32_e32 v187, 0x80, v181
	v_or_b32_e32 v190, 0xc0, v181
	v_lshl_or_b32 v191, v4, 3, 24
	v_lshlrev_b32_e32 v192, 4, v2
	v_lshlrev_b32_e32 v194, 4, v179
	v_or_b32_e32 v195, 0x8000, v193
	v_or_b32_e32 v196, 0x10000, v193
	v_or_b32_e32 v197, 0x18000, v193
	s_mov_b32 s46, 0
	s_movk_i32 s47, 0x300
	v_lshlrev_b32_e32 v198, 1, v166
	s_branch .LBB4_4

.LBB4_155:
	s_load_dword s0, s[0:1], 0x88
	s_lshl_b32 s1, s45, 6
	s_and_b32 s1, s1, 0xfffffe00
	s_or_b32 s2, s1, s44
	v_readfirstlane_b32 s4, v0
	s_waitcnt lgkmcnt(0)
	s_mul_i32 s3, s0, 0x60000
	s_mul_hi_i32 s1, s0, 0x60000
	s_add_u32 s3, s28, s3
	s_mulk_i32 s0, 0x300
	s_addc_u32 s5, s29, s1
	s_ashr_i32 s1, s0, 31
	s_lshl_b64 s[0:1], s[0:1], 2
	s_add_u32 s0, s30, s0
	s_addc_u32 s1, s31, s1
	s_lshr_b32 s6, s4, 6
	s_and_b32 s25, s25, 0xffff
	s_mul_i32 s4, s6, 0x6000
	v_and_b32_e32 v2, 63, v0
	s_mul_hi_u32 s7, s6, 0x6000
	s_add_u32 s4, s3, s4
	s_addc_u32 s5, s5, s7
	v_lshlrev_b32_e32 v56, 4, v2
	v_mov_b32_e32 v57, 0
	v_lshl_add_u64 v[54:55], s[4:5], 0, v[56:57]
	s_movk_i32 s3, 0x1000
	v_add_co_u32_e32 v50, vcc, s3, v54
	s_movk_i32 s3, 0x2000
	s_nop 0
	v_addc_co_u32_e32 v51, vcc, 0, v55, vcc
	v_add_co_u32_e32 v52, vcc, s3, v54
	global_load_dwordx4 v[2:5], v56, s[4:5] offset:1024
	global_load_dwordx4 v[6:9], v56, s[4:5] offset:2048
	v_addc_co_u32_e32 v53, vcc, 0, v55, vcc
	global_load_dwordx4 v[10:13], v56, s[4:5] offset:3072
	global_load_dwordx4 v[14:17], v[52:53], off offset:-4096
	global_load_dwordx4 v[18:21], v[50:51], off offset:1024
	global_load_dwordx4 v[22:25], v[50:51], off offset:2048
	global_load_dwordx4 v[26:29], v56, s[4:5]
	global_load_dwordx4 v[30:33], v[50:51], off offset:3072
	global_load_dwordx4 v[34:37], v[52:53], off
	global_load_dwordx4 v[38:41], v[52:53], off offset:1024
	global_load_dwordx4 v[42:45], v[52:53], off offset:2048
	global_load_dwordx4 v[46:49], v[52:53], off offset:3072
	s_movk_i32 s3, 0x3000
	v_add_co_u32_e32 v58, vcc, s3, v54
	s_movk_i32 s3, 0x4000
	s_nop 0
	v_addc_co_u32_e32 v59, vcc, 0, v55, vcc
	v_add_co_u32_e32 v140, vcc, s3, v54
	s_nop 1
	v_addc_co_u32_e32 v141, vcc, 0, v55, vcc
	s_barrier
	s_cmp_lt_u32 s94, 4
	s_cbranch_scc1 .Lmystag4_1
	s_sleep 4
.Lmystag4_1:
	global_load_dwordx4 v[50:53], v[140:141], off offset:-4096
	global_load_dwordx4 v[62:65], v[58:59], off offset:1024
	global_load_dwordx4 v[68:71], v[58:59], off offset:2048
	v_lshlrev_b32_e32 v67, 9, v1
	v_xor_b32_e32 v61, v167, v1
	v_lshl_or_b32 v66, v61, 4, v67
	ds_read_b128 v[72:75], v66
	ds_read_b128 v[76:79], v66 offset:8192
	ds_read_b128 v[80:83], v66 offset:16384
	ds_read_b128 v[84:87], v66 offset:24576
	v_mul_u32_u24_e32 v60, 0x556, v0
	v_lshrrev_b32_e32 v60, 16, v60
	s_mul_i32 s3, s6, 48
	v_lshlrev_b32_e32 v61, 3, v60
	s_movk_i32 s5, 0x47
	v_lshl_or_b32 v56, v167, 2, s3
	s_mov_b32 s3, 0xfffffd0
	v_bitop3_b32 v61, v61, s5, v60 bitop3:0xc8
	s_mov_b32 s27, 0x20000
	s_mov_b32 s26, 0x1800000
	s_mul_i32 s4, s6, 0x60
	v_mul_lo_u32 v150, v60, s3
	v_or_b32_e32 v61, s2, v61
	s_waitcnt vmcnt(8) lgkmcnt(3)
	v_mfma_f32_16x16x32_f16 v[88:91], v[26:29], v[72:75], 0
	s_waitcnt lgkmcnt(2)
	v_mfma_f32_16x16x32_f16 v[92:95], v[26:29], v[76:79], 0
	s_waitcnt lgkmcnt(1)
	v_mfma_f32_16x16x32_f16 v[96:99], v[26:29], v[80:83], 0
	s_waitcnt lgkmcnt(0)
	v_mfma_f32_16x16x32_f16 v[26:29], v[26:29], v[84:87], 0
	v_mfma_f32_16x16x32_f16 v[100:103], v[2:5], v[72:75], 0
	v_mfma_f32_16x16x32_f16 v[104:107], v[2:5], v[76:79], 0
	v_mfma_f32_16x16x32_f16 v[108:111], v[2:5], v[80:83], 0
	v_mfma_f32_16x16x32_f16 v[2:5], v[2:5], v[84:87], 0
	v_mfma_f32_16x16x32_f16 v[112:115], v[6:9], v[72:75], 0
	v_mfma_f32_16x16x32_f16 v[74:77], v[6:9], v[76:79], 0
	v_mfma_f32_16x16x32_f16 v[78:81], v[6:9], v[80:83], 0
	v_mfma_f32_16x16x32_f16 v[6:9], v[6:9], v[84:87], 0
	global_load_dwordx4 v[82:85], v[58:59], off offset:3072
	global_load_dwordx4 v[116:119], v[140:141], off
	global_load_dwordx4 v[120:123], v[140:141], off offset:1024
	v_bitop3_b32 v58, v167, v1, 4 bitop3:0x36
	v_lshl_or_b32 v72, v58, 4, v67
	ds_read_b128 v[124:127], v72
	ds_read_b128 v[128:131], v72 offset:8192
	ds_read_b128 v[132:135], v72 offset:16384
	ds_read_b128 v[136:139], v72 offset:24576
	s_waitcnt lgkmcnt(3)
	v_mfma_f32_16x16x32_f16 v[86:89], v[10:13], v[124:127], v[88:91]
	s_waitcnt lgkmcnt(2)
	v_mfma_f32_16x16x32_f16 v[90:93], v[10:13], v[128:131], v[92:95]
	s_waitcnt lgkmcnt(1)
	v_mfma_f32_16x16x32_f16 v[94:97], v[10:13], v[132:135], v[96:99]
	s_waitcnt lgkmcnt(0)
	v_mfma_f32_16x16x32_f16 v[10:13], v[10:13], v[136:139], v[26:29]
	v_mfma_f32_16x16x32_f16 v[26:29], v[14:17], v[124:127], v[100:103]
	v_mfma_f32_16x16x32_f16 v[98:101], v[14:17], v[128:131], v[104:107]
	v_mfma_f32_16x16x32_f16 v[102:105], v[14:17], v[132:135], v[108:111]
	v_mfma_f32_16x16x32_f16 v[2:5], v[14:17], v[136:139], v[2:5]
	v_mfma_f32_16x16x32_f16 v[14:17], v[18:21], v[124:127], v[112:115]
	v_mfma_f32_16x16x32_f16 v[106:109], v[18:21], v[128:131], v[74:77]
	v_mfma_f32_16x16x32_f16 v[76:79], v[18:21], v[132:135], v[78:81]
	v_mfma_f32_16x16x32_f16 v[6:9], v[18:21], v[136:139], v[6:9]
	s_movk_i32 s5, 0x5000
	v_add_co_u32_e32 v58, vcc, s5, v54
	global_load_dwordx4 v[110:113], v[140:141], off offset:2048
	global_load_dwordx4 v[124:127], v[140:141], off offset:3072
	v_addc_co_u32_e32 v59, vcc, 0, v55, vcc
	global_load_dwordx4 v[128:131], v[58:59], off
	v_bitop3_b32 v18, v167, v1, 8 bitop3:0x36
	v_lshl_or_b32 v74, v18, 4, v67
	ds_read_b128 v[18:21], v74
	ds_read_b128 v[132:135], v74 offset:8192
	ds_read_b128 v[136:139], v74 offset:16384
	ds_read_b128 v[140:143], v74 offset:24576
	s_waitcnt lgkmcnt(3)
	v_mfma_f32_16x16x32_f16 v[86:89], v[22:25], v[18:21], v[86:89]
	s_waitcnt lgkmcnt(2)
	v_mfma_f32_16x16x32_f16 v[90:93], v[22:25], v[132:135], v[90:93]
	s_waitcnt lgkmcnt(1)
	v_mfma_f32_16x16x32_f16 v[94:97], v[22:25], v[136:139], v[94:97]
	s_waitcnt lgkmcnt(0)
	v_mfma_f32_16x16x32_f16 v[10:13], v[22:25], v[140:143], v[10:13]
	s_waitcnt vmcnt(13)
	v_mfma_f32_16x16x32_f16 v[22:25], v[30:33], v[18:21], v[26:29]
	v_mfma_f32_16x16x32_f16 v[26:29], v[30:33], v[132:135], v[98:101]
	v_mfma_f32_16x16x32_f16 v[98:101], v[30:33], v[136:139], v[102:105]
	v_mfma_f32_16x16x32_f16 v[2:5], v[30:33], v[140:143], v[2:5]
	s_waitcnt vmcnt(12)
	v_mfma_f32_16x16x32_f16 v[14:17], v[34:37], v[18:21], v[14:17]
	v_mfma_f32_16x16x32_f16 v[18:21], v[34:37], v[132:135], v[106:109]
	v_mfma_f32_16x16x32_f16 v[30:33], v[34:37], v[136:139], v[76:79]
	v_mfma_f32_16x16x32_f16 v[6:9], v[34:37], v[140:143], v[6:9]
	global_load_dwordx4 v[102:105], v[58:59], off offset:1024
	global_load_dwordx4 v[106:109], v[58:59], off offset:2048
	global_load_dwordx4 v[132:135], v[58:59], off offset:3072
	v_bitop3_b32 v34, v167, v1, 12 bitop3:0x36
	v_lshl_or_b32 v75, v34, 4, v67
	ds_read_b128 v[34:37], v75
	ds_read_b128 v[76:79], v75 offset:8192
	ds_read_b128 v[136:139], v75 offset:16384
	ds_read_b128 v[140:143], v75 offset:24576
	s_waitcnt vmcnt(14) lgkmcnt(3)
	v_mfma_f32_16x16x32_f16 v[86:89], v[38:41], v[34:37], v[86:89]
	s_waitcnt lgkmcnt(2)
	v_mfma_f32_16x16x32_f16 v[90:93], v[38:41], v[76:79], v[90:93]
	s_waitcnt lgkmcnt(1)
	v_mfma_f32_16x16x32_f16 v[94:97], v[38:41], v[136:139], v[94:97]
	s_waitcnt lgkmcnt(0)
	v_mfma_f32_16x16x32_f16 v[10:13], v[38:41], v[140:143], v[10:13]
	s_waitcnt vmcnt(13)
	v_mfma_f32_16x16x32_f16 v[38:41], v[42:45], v[34:37], v[22:25]
	v_mfma_f32_16x16x32_f16 v[144:147], v[42:45], v[76:79], v[26:29]
	v_mfma_f32_16x16x32_f16 v[98:101], v[42:45], v[136:139], v[98:101]
	v_mfma_f32_16x16x32_f16 v[2:5], v[42:45], v[140:143], v[2:5]
	s_waitcnt vmcnt(12)
	v_mfma_f32_16x16x32_f16 v[14:17], v[46:49], v[34:37], v[14:17]
	v_mfma_f32_16x16x32_f16 v[18:21], v[46:49], v[76:79], v[18:21]
	v_mfma_f32_16x16x32_f16 v[30:33], v[46:49], v[136:139], v[30:33]
	v_mfma_f32_16x16x32_f16 v[6:9], v[46:49], v[140:143], v[6:9]
	s_mov_b32 s5, 0x30000
	v_add_co_u32_e32 v58, vcc, s5, v54
	s_mov_b32 s5, 0x31000
	s_nop 0
	v_addc_co_u32_e32 v59, vcc, 0, v55, vcc
	v_add_co_u32_e32 v148, vcc, s5, v54
	v_bitop3_b32 v42, v167, v1, 16 bitop3:0x36
	s_nop 0
	v_addc_co_u32_e32 v149, vcc, 0, v55, vcc
	global_load_dwordx4 v[34:37], v[148:149], off offset:-4096
	global_load_dwordx4 v[26:29], v[58:59], off offset:1024
	global_load_dwordx4 v[22:25], v[58:59], off offset:2048
	v_lshl_or_b32 v76, v42, 4, v67
	ds_read_b128 v[42:45], v76
	ds_read_b128 v[46:49], v76 offset:8192
	ds_read_b128 v[78:81], v76 offset:16384
	ds_read_b128 v[136:139], v76 offset:24576
	s_waitcnt vmcnt(14) lgkmcnt(3)
	v_mfma_f32_16x16x32_f16 v[86:89], v[50:53], v[42:45], v[86:89]
	s_waitcnt lgkmcnt(2)
	v_mfma_f32_16x16x32_f16 v[90:93], v[50:53], v[46:49], v[90:93]
	s_waitcnt lgkmcnt(1)
	v_mfma_f32_16x16x32_f16 v[94:97], v[50:53], v[78:81], v[94:97]
	s_waitcnt lgkmcnt(0)
	v_mfma_f32_16x16x32_f16 v[10:13], v[50:53], v[136:139], v[10:13]
	s_waitcnt vmcnt(13)
	v_mfma_f32_16x16x32_f16 v[38:41], v[62:65], v[42:45], v[38:41]
	v_mfma_f32_16x16x32_f16 v[50:53], v[62:65], v[46:49], v[144:147]
	v_mfma_f32_16x16x32_f16 v[98:101], v[62:65], v[78:81], v[98:101]
	v_mfma_f32_16x16x32_f16 v[62:65], v[62:65], v[136:139], v[2:5]
	s_waitcnt vmcnt(12)
	v_mfma_f32_16x16x32_f16 v[42:45], v[68:71], v[42:45], v[14:17]
	v_mfma_f32_16x16x32_f16 v[18:21], v[68:71], v[46:49], v[18:21]
	v_mfma_f32_16x16x32_f16 v[30:33], v[68:71], v[78:81], v[30:33]
	v_mfma_f32_16x16x32_f16 v[46:49], v[68:71], v[136:139], v[6:9]
	global_load_dwordx4 v[14:17], v[58:59], off offset:3072
	s_nop 1
	global_load_dwordx4 v[6:9], v[148:149], off
	global_load_dwordx4 v[2:5], v[148:149], off offset:1024
	v_bitop3_b32 v58, v167, v1, 20 bitop3:0x36
	v_lshl_or_b32 v77, v58, 4, v67
	ds_read_b128 v[68:71], v77
	ds_read_b128 v[78:81], v77 offset:8192
	ds_read_b128 v[136:139], v77 offset:16384
	ds_read_b128 v[140:143], v77 offset:24576
	s_waitcnt vmcnt(14) lgkmcnt(3)
	v_mfma_f32_16x16x32_f16 v[86:89], v[82:85], v[68:71], v[86:89]
	s_waitcnt lgkmcnt(2)
	v_mfma_f32_16x16x32_f16 v[90:93], v[82:85], v[78:81], v[90:93]
	s_waitcnt lgkmcnt(1)
	v_mfma_f32_16x16x32_f16 v[94:97], v[82:85], v[136:139], v[94:97]
	s_waitcnt lgkmcnt(0)
	v_mfma_f32_16x16x32_f16 v[82:85], v[82:85], v[140:143], v[10:13]
	s_waitcnt vmcnt(13)
	v_mfma_f32_16x16x32_f16 v[38:41], v[116:119], v[68:71], v[38:41]
	v_mfma_f32_16x16x32_f16 v[50:53], v[116:119], v[78:81], v[50:53]
	v_mfma_f32_16x16x32_f16 v[98:101], v[116:119], v[136:139], v[98:101]
	v_mfma_f32_16x16x32_f16 v[62:65], v[116:119], v[140:143], v[62:65]
	s_waitcnt vmcnt(12)
	v_mfma_f32_16x16x32_f16 v[42:45], v[120:123], v[68:71], v[42:45]
	v_mfma_f32_16x16x32_f16 v[68:71], v[120:123], v[78:81], v[18:21]
	v_mfma_f32_16x16x32_f16 v[114:117], v[120:123], v[136:139], v[30:33]
	v_mfma_f32_16x16x32_f16 v[46:49], v[120:123], v[140:143], v[46:49]
	s_mov_b32 s5, 0x33000
	v_add_co_u32_e32 v58, vcc, s5, v54
	global_load_dwordx4 v[18:21], v[148:149], off offset:2048
	global_load_dwordx4 v[10:13], v[148:149], off offset:3072
	v_addc_co_u32_e32 v59, vcc, 0, v55, vcc
	global_load_dwordx4 v[30:33], v[58:59], off offset:-4096
	v_bitop3_b32 v73, v167, v1, 24 bitop3:0x36
	v_lshl_or_b32 v78, v73, 4, v67
	ds_read_b128 v[118:121], v78
	ds_read_b128 v[136:139], v78 offset:8192
	ds_read_b128 v[140:143], v78 offset:16384
	ds_read_b128 v[144:147], v78 offset:24576
	s_mov_b32 s5, 0x32000
	v_add_co_u32_e32 v148, vcc, s5, v54
	s_nop 1
	v_addc_co_u32_e32 v149, vcc, 0, v55, vcc
	s_waitcnt vmcnt(14) lgkmcnt(3)
	v_mfma_f32_16x16x32_f16 v[86:89], v[110:113], v[118:121], v[86:89]
	s_waitcnt lgkmcnt(2)
	v_mfma_f32_16x16x32_f16 v[90:93], v[110:113], v[136:139], v[90:93]
	s_waitcnt lgkmcnt(1)
	v_mfma_f32_16x16x32_f16 v[94:97], v[110:113], v[140:143], v[94:97]
	s_waitcnt lgkmcnt(0)
	v_mfma_f32_16x16x32_f16 v[80:83], v[110:113], v[144:147], v[82:85]
	s_waitcnt vmcnt(13)
	v_mfma_f32_16x16x32_f16 v[110:113], v[124:127], v[118:121], v[38:41]
	v_mfma_f32_16x16x32_f16 v[50:53], v[124:127], v[136:139], v[50:53]
	v_mfma_f32_16x16x32_f16 v[98:101], v[124:127], v[140:143], v[98:101]
	v_mfma_f32_16x16x32_f16 v[62:65], v[124:127], v[144:147], v[62:65]
	s_waitcnt vmcnt(12)
	v_mfma_f32_16x16x32_f16 v[118:121], v[128:131], v[118:121], v[42:45]
	v_mfma_f32_16x16x32_f16 v[68:71], v[128:131], v[136:139], v[68:71]
	v_mfma_f32_16x16x32_f16 v[114:117], v[128:131], v[140:143], v[114:117]
	v_mfma_f32_16x16x32_f16 v[122:125], v[128:131], v[144:147], v[46:49]
	s_nop 2
	global_load_dwordx4 v[46:49], v[148:149], off offset:1024
	global_load_dwordx4 v[42:45], v[148:149], off offset:2048
	global_load_dwordx4 v[38:41], v[148:149], off offset:3072
	v_bitop3_b32 v73, v167, v1, 28 bitop3:0x36
	v_lshl_or_b32 v79, v73, 4, v67
	ds_read_b128 v[126:129], v79
	ds_read_b128 v[136:139], v79 offset:8192
	ds_read_b128 v[140:143], v79 offset:16384
	ds_read_b128 v[144:147], v79 offset:24576
	s_waitcnt vmcnt(14) lgkmcnt(3)
	v_mfma_f32_16x16x32_f16 v[84:87], v[102:105], v[126:129], v[86:89]
	s_waitcnt lgkmcnt(2)
	v_mfma_f32_16x16x32_f16 v[88:91], v[102:105], v[136:139], v[90:93]
	s_waitcnt lgkmcnt(1)
	v_mfma_f32_16x16x32_f16 v[92:95], v[102:105], v[140:143], v[94:97]
	s_waitcnt lgkmcnt(0)
	v_mfma_f32_16x16x32_f16 v[80:83], v[102:105], v[144:147], v[80:83]
	s_waitcnt vmcnt(13)
	v_mfma_f32_16x16x32_f16 v[102:105], v[106:109], v[126:129], v[110:113]
	v_mfma_f32_16x16x32_f16 v[110:113], v[106:109], v[136:139], v[50:53]
	v_mfma_f32_16x16x32_f16 v[96:99], v[106:109], v[140:143], v[98:101]
	v_mfma_f32_16x16x32_f16 v[62:65], v[106:109], v[144:147], v[62:65]
	s_waitcnt vmcnt(12)
	v_mfma_f32_16x16x32_f16 v[106:109], v[132:135], v[126:129], v[118:121]
	v_mfma_f32_16x16x32_f16 v[118:121], v[132:135], v[136:139], v[68:71]
	v_mfma_f32_16x16x32_f16 v[114:117], v[132:135], v[140:143], v[114:117]
	v_mfma_f32_16x16x32_f16 v[50:53], v[132:135], v[144:147], v[122:125]
	v_lshl_add_u64 v[56:57], v[56:57], 2, s[0:1]
	s_nop 1
	global_load_dwordx4 v[122:125], v[56:57], off
	global_load_dwordx4 v[126:129], v[56:57], off offset:64
	global_load_dwordx4 v[130:133], v[56:57], off offset:128
	v_lshl_or_b32 v67, v167, 3, s4
	s_movk_i32 s0, 0x310
	v_mov_b32_e32 v100, v89
	v_mov_b32_e32 v101, v90
	v_mov_b32_e32 v134, v93
	v_mov_b32_e32 v135, v94
	v_mov_b32_e32 v140, v97
	v_mov_b32_e32 v141, v98
	v_mad_u32_u24 v69, v1, s0, v67
	v_mov_b32_e32 v143, v64
	v_mov_b32_e32 v136, v81
	v_mov_b32_e32 v137, v82
	v_mov_b32_e32 v138, v111
	v_mov_b32_e32 v139, v112
	v_mov_b32_e32 v142, v63
	v_add_u32_e32 v73, 0x8000, v69
	s_barrier
	v_add_u32_e32 v70, 0xb000, v69
	v_add_u32_e32 v71, 0xe000, v69
	v_add_u32_e32 v68, 0x9300, v69
	s_movk_i32 s1, 0x600
	s_movk_i32 s6, 0x1c7
	s_waitcnt vmcnt(2)
	v_pk_add_f32 v[84:85], v[84:85], v[122:123]
	v_add_f32_e32 v1, v88, v122
	v_pk_mov_b32 v[88:89], v[122:123], v[124:125] op_sel:[1,0]
	v_add_f32_e32 v67, v91, v125
	v_add_f32_e32 v92, v92, v122
	v_add_f32_e32 v93, v95, v125
	v_add_f32_e32 v94, v80, v122
	v_add_f32_e32 v95, v83, v125
	s_waitcnt vmcnt(1)
	v_add_f32_e32 v97, v110, v126
	v_add_f32_e32 v98, v113, v129
	v_add_f32_e32 v96, v96, v126
	v_add_f32_e32 v99, v99, v129
	v_cvt_pk_f16_f32 v64, v84, v85
	v_cvt_f16_f32_e32 v1, v1
	v_pk_add_f32 v[84:85], v[100:101], v[88:89]
	v_cvt_f16_f32_e32 v67, v67
	v_cvt_f16_f32_e32 v100, v92
	v_cvt_f16_f32_e32 v101, v93
	v_cvt_f16_f32_e32 v94, v94
	v_cvt_f16_f32_e32 v95, v95
	v_cvt_f16_f32_e32 v97, v97
	v_cvt_f16_f32_e32 v98, v98
	v_pk_add_f32 v[86:87], v[86:87], v[124:125]
	v_pk_add_f32 v[80:81], v[102:103], v[126:127]
	v_pk_add_f32 v[82:83], v[104:105], v[128:129]
	v_pk_mov_b32 v[90:91], v[126:127], v[128:129] op_sel:[1,0]
	v_cvt_f16_f32_e32 v96, v96
	v_cvt_f16_f32_e32 v99, v99
	v_add_f32_e32 v102, v62, v126
	v_add_f32_e32 v103, v65, v129
	s_waitcnt vmcnt(0)
	v_pk_add_f32 v[62:63], v[106:107], v[130:131]
	v_cvt_pk_f16_f32 v65, v86, v87
	v_pk_add_f32 v[86:87], v[134:135], v[88:89]
	v_pk_add_f32 v[88:89], v[136:137], v[88:89]
	v_cvt_pk_f16_f32 v80, v80, v81
	v_cvt_pk_f16_f32 v81, v82, v83
	v_pk_add_f32 v[82:83], v[138:139], v[90:91]
	v_pk_add_f32 v[92:93], v[140:141], v[90:91]
	v_cvt_pk_f16_f32 v62, v62, v63
	v_cvt_pk_f16_f32 v63, v84, v85
	v_cvt_pk_f16_f32 v84, v86, v87
	v_cvt_pk_f16_f32 v85, v88, v89
	v_cvt_pk_f16_f32 v86, v82, v83
	v_cvt_pk_f16_f32 v87, v92, v93
	ds_write2_b64 v73, v[64:65], v[80:81] offset1:4
	v_pack_b32_f16 v64, v1, v63
	v_alignbit_b32 v65, v67, v63, 16
	v_pack_b32_f16 v80, v100, v84
	v_alignbit_b32 v81, v101, v84, 16
	v_pack_b32_f16 v82, v94, v85
	v_alignbit_b32 v83, v95, v85, 16
	v_pack_b32_f16 v84, v97, v86
	v_alignbit_b32 v85, v98, v86, 16
	v_pack_b32_f16 v86, v96, v87
	v_alignbit_b32 v87, v99, v87, 16
	ds_write2_b64 v70, v[64:65], v[84:85] offset0:32 offset1:36
	ds_write2_b64 v71, v[80:81], v[86:87] offset0:64 offset1:68
	v_pk_add_f32 v[64:65], v[108:109], v[132:133]
	v_add_f32_e32 v1, v118, v130
	v_cvt_pk_f16_f32 v63, v64, v65
	v_cvt_f16_f32_e32 v1, v1
	v_add_f32_e32 v67, v121, v133
	ds_write_b64 v69, v[62:63] offset:32832
	v_mov_b32_e32 v62, v119
	v_mov_b32_e32 v63, v120
	v_pk_mov_b32 v[64:65], v[130:131], v[132:133] op_sel:[1,0]
	v_cvt_f16_f32_e32 v67, v67
	v_pk_add_f32 v[62:63], v[62:63], v[64:65]
	v_cvt_f16_f32_e32 v102, v102
	v_cvt_pk_f16_f32 v63, v62, v63
	v_pack_b32_f16 v62, v1, v63
	v_add_f32_e32 v1, v114, v130
	v_alignbit_b32 v63, v67, v63, 16
	v_cvt_f16_f32_e32 v1, v1
	ds_write_b64 v69, v[62:63] offset:45376
	v_mov_b32_e32 v62, v115
	v_mov_b32_e32 v63, v116
	v_pk_add_f32 v[62:63], v[62:63], v[64:65]
	v_add_f32_e32 v67, v117, v133
	v_cvt_pk_f16_f32 v63, v62, v63
	v_pack_b32_f16 v62, v1, v63
	v_add_f32_e32 v1, v50, v130
	v_mov_b32_e32 v50, v51
	v_mov_b32_e32 v51, v52
	v_add_f32_e32 v52, v53, v133
	v_cvt_f16_f32_e32 v103, v103
	v_cvt_f16_f32_e32 v67, v67
	v_cvt_f16_f32_e32 v1, v1
	v_cvt_f16_f32_e32 v52, v52
	v_pk_add_f32 v[90:91], v[142:143], v[90:91]
	v_pk_add_f32 v[50:51], v[50:51], v[64:65]
	v_cvt_pk_f16_f32 v89, v90, v91
	v_cvt_pk_f16_f32 v51, v50, v51
	v_pack_b32_f16 v88, v102, v89
	v_alignbit_b32 v89, v103, v89, 16
	v_add_u32_e32 v80, 0x8000, v68
	v_alignbit_b32 v63, v67, v63, 16
	v_pack_b32_f16 v50, v1, v51
	v_alignbit_b32 v51, v52, v51, 16
	ds_write2_b64 v80, v[82:83], v[88:89] offset1:4
	ds_write_b64 v69, v[62:63] offset:57920
	ds_write_b64 v68, v[50:51] offset:32832
	s_waitcnt lgkmcnt(0)
	s_barrier
	s_cmp_lt_u32 s94, 4
	s_cbranch_scc1 .Lmystag4_3
	s_sleep 4
.Lmystag4_3:
	global_load_dwordx4 v[82:85], v[58:59], off
	global_load_dwordx4 v[86:89], v[58:59], off offset:1024
	global_load_dwordx4 v[90:93], v[58:59], off offset:2048
	v_add_lshl_u32 v52, v150, v0, 4
	v_mad_u64_u32 v[50:51], s[4:5], v61, s1, v[52:53]
	v_or_b32_e32 v1, 0x200, v0
	v_mad_u32_u24 v51, v60, s0, v52
	v_mul_u32_u24_e32 v52, 0x556, v1
	v_lshrrev_b32_e32 v53, 16, v52
	v_mul_lo_u32 v52, v53, s3
	v_add_lshl_u32 v52, v52, v1, 4
	v_lshlrev_b32_e32 v1, 3, v53
	s_movk_i32 s4, 0xc7
	ds_read_b128 v[60:63], v51 offset:32768
	v_bitop3_b32 v1, v1, s4, v53 bitop3:0xc8
	v_or_b32_e32 v1, s2, v1
	v_mad_u32_u24 v81, v53, s0, v52
	v_mad_u64_u32 v[52:53], s[4:5], v1, s1, v[52:53]
	v_or_b32_e32 v1, 0x400, v0
	v_mul_u32_u24_e32 v53, 0x556, v1
	v_lshrrev_b32_e32 v53, 16, v53
	ds_read_b128 v[94:97], v81 offset:32768
	s_waitcnt lgkmcnt(1)
	buffer_store_dwordx4 v[60:63], v50, s[24:27], 0 offen sc1
	s_waitcnt lgkmcnt(0)
	buffer_store_dwordx4 v[94:97], v52, s[24:27], 0 offen sc1
	v_lshlrev_b32_e32 v61, 3, v53
	v_mul_lo_u32 v60, v53, s3
	v_bitop3_b32 v61, v61, s6, v53 bitop3:0xc8
	v_or_b32_e32 v61, s2, v61
	v_add_lshl_u32 v62, v60, v1, 4
	v_mad_u64_u32 v[60:61], s[4:5], v61, s1, v[62:63]
	v_or_b32_e32 v1, 0x600, v0
	v_mad_u32_u24 v53, v53, s0, v62
	v_mul_u32_u24_e32 v61, 0x556, v1
	ds_read_b128 v[62:65], v53 offset:32768
	v_lshrrev_b32_e32 v67, 16, v61
	v_mul_lo_u32 v94, v67, s3
	v_add_lshl_u32 v98, v94, v1, 4
	v_lshrrev_b32_e32 v1, 13, v61
	v_mad_u32_u24 v160, v67, s0, v98
	v_and_b32_e32 v1, 0x1c0, v1
	v_bfe_u32 v61, v61, 16, 3
	ds_read_b128 v[94:97], v160 offset:32768
	v_or3_b32 v1, s2, v61, v1
	s_waitcnt lgkmcnt(1)
	buffer_store_dwordx4 v[62:65], v60, s[24:27], 0 offen sc1
	s_nop 1
	v_mad_u64_u32 v[62:63], s[4:5], v1, s1, v[98:99]
	v_or_b32_e32 v1, 0x800, v0
	v_mul_u32_u24_e32 v61, 0xaab, v1
	v_lshrrev_b32_e32 v61, 17, v61
	v_mul_lo_u32 v63, v61, s3
	v_lshlrev_b32_e32 v64, 3, v61
	s_waitcnt lgkmcnt(0)
	buffer_store_dwordx4 v[94:97], v62, s[24:27], 0 offen sc1
	v_bitop3_b32 v64, v64, s6, v61 bitop3:0xc8
	v_or_b32_e32 v64, s2, v64
	v_add_lshl_u32 v94, v63, v1, 4
	v_mad_u32_u24 v61, v61, s0, v94
	v_or_b32_e32 v0, 0xa00, v0
	v_mad_u64_u32 v[64:65], s[4:5], v64, s1, v[94:95]
	ds_read_b128 v[94:97], v61 offset:32768
	v_mul_u32_u24_e32 v1, 0xaab, v0
	v_lshrrev_b32_e32 v63, 17, v1
	v_mul_lo_u32 v65, v63, s3
	v_add_lshl_u32 v0, v65, v0, 4
	v_mad_u32_u24 v63, v63, s0, v0
	ds_read_b128 v[98:101], v63 offset:32768
	s_waitcnt lgkmcnt(1)
	buffer_store_dwordx4 v[94:97], v64, s[24:27], 0 offen sc1
	ds_read_b128 v[94:97], v66
	ds_read_b128 v[102:105], v66 offset:8192
	ds_read_b128 v[106:109], v66 offset:16384
	ds_read_b128 v[110:113], v66 offset:24576
	v_lshrrev_b32_e32 v65, 14, v1
	v_and_b32_e32 v65, 0x1c0, v65
	v_bfe_u32 v1, v1, 17, 3
	v_or3_b32 v1, s2, v1, v65
	v_mad_u64_u32 v[66:67], s[0:1], v1, s1, v[0:1]
	s_waitcnt lgkmcnt(4)
	buffer_store_dwordx4 v[98:101], v66, s[24:27], 0 offen sc1
	s_waitcnt lgkmcnt(3)
	s_nop 0
	v_mfma_f32_16x16x32_f16 v[98:101], v[34:37], v[94:97], 0
	s_waitcnt lgkmcnt(2)
	v_mfma_f32_16x16x32_f16 v[114:117], v[34:37], v[102:105], 0
	s_waitcnt lgkmcnt(1)
	v_mfma_f32_16x16x32_f16 v[118:121], v[34:37], v[106:109], 0
	s_waitcnt lgkmcnt(0)
	v_mfma_f32_16x16x32_f16 v[34:37], v[34:37], v[110:113], 0
	v_mfma_f32_16x16x32_f16 v[122:125], v[26:29], v[94:97], 0
	v_mfma_f32_16x16x32_f16 v[126:129], v[26:29], v[102:105], 0
	v_mfma_f32_16x16x32_f16 v[130:133], v[26:29], v[106:109], 0
	v_mfma_f32_16x16x32_f16 v[26:29], v[26:29], v[110:113], 0
	v_mfma_f32_16x16x32_f16 v[94:97], v[22:25], v[94:97], 0
	v_mfma_f32_16x16x32_f16 v[102:105], v[22:25], v[102:105], 0
	v_mfma_f32_16x16x32_f16 v[106:109], v[22:25], v[106:109], 0
	v_mfma_f32_16x16x32_f16 v[22:25], v[22:25], v[110:113], 0
	s_mov_b32 s0, 0x34000
	v_add_co_u32_e32 v158, vcc, s0, v54
	s_mov_b32 s0, 0x35000
	s_nop 0
	v_addc_co_u32_e32 v159, vcc, 0, v55, vcc
	v_add_co_u32_e32 v54, vcc, s0, v54
	s_nop 1
	v_addc_co_u32_e32 v55, vcc, 0, v55, vcc
	global_load_dwordx4 v[110:113], v[54:55], off offset:-4096
	global_load_dwordx4 v[134:137], v[58:59], off offset:3072
	global_load_dwordx4 v[138:141], v[158:159], off offset:1024
	ds_read_b128 v[142:145], v72
	ds_read_b128 v[146:149], v72 offset:8192
	ds_read_b128 v[150:153], v72 offset:16384
	ds_read_b128 v[154:157], v72 offset:24576
	s_waitcnt lgkmcnt(3)
	v_mfma_f32_16x16x32_f16 v[98:101], v[14:17], v[142:145], v[98:101]
	s_waitcnt lgkmcnt(2)
	v_mfma_f32_16x16x32_f16 v[114:117], v[14:17], v[146:149], v[114:117]
	s_waitcnt lgkmcnt(1)
	v_mfma_f32_16x16x32_f16 v[118:121], v[14:17], v[150:153], v[118:121]
	s_waitcnt lgkmcnt(0)
	v_mfma_f32_16x16x32_f16 v[14:17], v[14:17], v[154:157], v[34:37]
	v_mfma_f32_16x16x32_f16 v[34:37], v[6:9], v[142:145], v[122:125]
	v_mfma_f32_16x16x32_f16 v[122:125], v[6:9], v[146:149], v[126:129]
	v_mfma_f32_16x16x32_f16 v[126:129], v[6:9], v[150:153], v[130:133]
	v_mfma_f32_16x16x32_f16 v[6:9], v[6:9], v[154:157], v[26:29]
	v_mfma_f32_16x16x32_f16 v[26:29], v[2:5], v[142:145], v[94:97]
	v_mfma_f32_16x16x32_f16 v[94:97], v[2:5], v[146:149], v[102:105]
	v_mfma_f32_16x16x32_f16 v[102:105], v[2:5], v[150:153], v[106:109]
	v_mfma_f32_16x16x32_f16 v[0:3], v[2:5], v[154:157], v[22:25]
	s_nop 2
	global_load_dwordx4 v[22:25], v[158:159], off offset:2048
	global_load_dwordx4 v[106:109], v[158:159], off offset:3072
	global_load_dwordx4 v[130:133], v[54:55], off
	ds_read_b128 v[142:145], v74
	ds_read_b128 v[146:149], v74 offset:8192
	ds_read_b128 v[150:153], v74 offset:16384
	ds_read_b128 v[154:157], v74 offset:24576
	s_waitcnt lgkmcnt(3)
	v_mfma_f32_16x16x32_f16 v[98:101], v[18:21], v[142:145], v[98:101]
	s_waitcnt lgkmcnt(2)
	v_mfma_f32_16x16x32_f16 v[114:117], v[18:21], v[146:149], v[114:117]
	s_waitcnt lgkmcnt(1)
	v_mfma_f32_16x16x32_f16 v[118:121], v[18:21], v[150:153], v[118:121]
	s_waitcnt lgkmcnt(0)
	v_mfma_f32_16x16x32_f16 v[14:17], v[18:21], v[154:157], v[14:17]
	v_mfma_f32_16x16x32_f16 v[18:21], v[10:13], v[142:145], v[34:37]
	v_mfma_f32_16x16x32_f16 v[34:37], v[10:13], v[146:149], v[122:125]
	v_mfma_f32_16x16x32_f16 v[122:125], v[10:13], v[150:153], v[126:129]
	v_mfma_f32_16x16x32_f16 v[4:7], v[10:13], v[154:157], v[6:9]
	v_mfma_f32_16x16x32_f16 v[8:11], v[30:33], v[142:145], v[26:29]
	v_mfma_f32_16x16x32_f16 v[26:29], v[30:33], v[146:149], v[94:97]
	v_mfma_f32_16x16x32_f16 v[94:97], v[30:33], v[150:153], v[102:105]
	v_mfma_f32_16x16x32_f16 v[0:3], v[30:33], v[154:157], v[0:3]
	global_load_dwordx4 v[30:33], v[54:55], off offset:1024
	s_nop 0
	global_load_dwordx4 v[102:105], v[54:55], off offset:2048
	global_load_dwordx4 v[126:129], v[54:55], off offset:3072
	ds_read_b128 v[142:145], v75
	ds_read_b128 v[146:149], v75 offset:8192
	ds_read_b128 v[150:153], v75 offset:16384
	ds_read_b128 v[154:157], v75 offset:24576
	s_waitcnt lgkmcnt(3)
	v_mfma_f32_16x16x32_f16 v[98:101], v[46:49], v[142:145], v[98:101]
	s_waitcnt lgkmcnt(2)
	v_mfma_f32_16x16x32_f16 v[114:117], v[46:49], v[146:149], v[114:117]
	s_waitcnt lgkmcnt(1)
	v_mfma_f32_16x16x32_f16 v[118:121], v[46:49], v[150:153], v[118:121]
	s_waitcnt lgkmcnt(0)
	v_mfma_f32_16x16x32_f16 v[12:15], v[46:49], v[154:157], v[14:17]
	v_mfma_f32_16x16x32_f16 v[16:19], v[42:45], v[142:145], v[18:21]
	v_mfma_f32_16x16x32_f16 v[34:37], v[42:45], v[146:149], v[34:37]
	v_mfma_f32_16x16x32_f16 v[46:49], v[42:45], v[150:153], v[122:125]
	v_mfma_f32_16x16x32_f16 v[4:7], v[42:45], v[154:157], v[4:7]
	v_mfma_f32_16x16x32_f16 v[8:11], v[38:41], v[142:145], v[8:11]
	v_mfma_f32_16x16x32_f16 v[26:29], v[38:41], v[146:149], v[26:29]
	v_mfma_f32_16x16x32_f16 v[42:45], v[38:41], v[150:153], v[94:97]
	v_mfma_f32_16x16x32_f16 v[0:3], v[38:41], v[154:157], v[0:3]
	ds_read_b128 v[38:41], v76
	s_nop 0
	ds_read_b128 v[94:97], v76 offset:8192
	ds_read_b128 v[122:125], v76 offset:16384
	ds_read_b128 v[142:145], v76 offset:24576
	s_waitcnt vmcnt(17) lgkmcnt(3)
	v_mfma_f32_16x16x32_f16 v[98:101], v[82:85], v[38:41], v[98:101]
	s_waitcnt lgkmcnt(2)
	v_mfma_f32_16x16x32_f16 v[114:117], v[82:85], v[94:97], v[114:117]
	s_waitcnt lgkmcnt(1)
	v_mfma_f32_16x16x32_f16 v[118:121], v[82:85], v[122:125], v[118:121]
	s_waitcnt lgkmcnt(0)
	v_mfma_f32_16x16x32_f16 v[12:15], v[82:85], v[142:145], v[12:15]
	s_waitcnt vmcnt(16)
	v_mfma_f32_16x16x32_f16 v[16:19], v[86:89], v[38:41], v[16:19]
	v_mfma_f32_16x16x32_f16 v[34:37], v[86:89], v[94:97], v[34:37]
	v_mfma_f32_16x16x32_f16 v[46:49], v[86:89], v[122:125], v[46:49]
	v_mfma_f32_16x16x32_f16 v[4:7], v[86:89], v[142:145], v[4:7]
	s_waitcnt vmcnt(15)
	v_mfma_f32_16x16x32_f16 v[8:11], v[90:93], v[38:41], v[8:11]
	v_mfma_f32_16x16x32_f16 v[26:29], v[90:93], v[94:97], v[26:29]
	v_mfma_f32_16x16x32_f16 v[38:41], v[90:93], v[122:125], v[42:45]
	v_mfma_f32_16x16x32_f16 v[0:3], v[90:93], v[142:145], v[0:3]
	s_nop 1
	ds_read_b128 v[42:45], v77
	ds_read_b128 v[82:85], v77 offset:8192
	ds_read_b128 v[86:89], v77 offset:16384
	ds_read_b128 v[74:77], v77 offset:24576
	s_waitcnt vmcnt(7) lgkmcnt(3)
	v_mfma_f32_16x16x32_f16 v[90:93], v[134:137], v[42:45], v[98:101]
	s_waitcnt lgkmcnt(2)
	v_mfma_f32_16x16x32_f16 v[94:97], v[134:137], v[82:85], v[114:117]
	s_waitcnt lgkmcnt(1)
	v_mfma_f32_16x16x32_f16 v[98:101], v[134:137], v[86:89], v[118:121]
	s_waitcnt lgkmcnt(0)
	v_mfma_f32_16x16x32_f16 v[12:15], v[134:137], v[74:77], v[12:15]
	v_mfma_f32_16x16x32_f16 v[16:19], v[110:113], v[42:45], v[16:19]
	v_mfma_f32_16x16x32_f16 v[34:37], v[110:113], v[82:85], v[34:37]
	v_mfma_f32_16x16x32_f16 v[46:49], v[110:113], v[86:89], v[46:49]
	v_mfma_f32_16x16x32_f16 v[4:7], v[110:113], v[74:77], v[4:7]
	s_waitcnt vmcnt(6)
	v_mfma_f32_16x16x32_f16 v[8:11], v[138:141], v[42:45], v[8:11]
	v_mfma_f32_16x16x32_f16 v[26:29], v[138:141], v[82:85], v[26:29]
	v_mfma_f32_16x16x32_f16 v[38:41], v[138:141], v[86:89], v[38:41]
	v_mfma_f32_16x16x32_f16 v[0:3], v[138:141], v[74:77], v[0:3]
	ds_read_b128 v[42:45], v78
	ds_read_b128 v[74:77], v78 offset:8192
	ds_read_b128 v[82:85], v78 offset:16384
	ds_read_b128 v[86:89], v78 offset:24576
	s_waitcnt vmcnt(5) lgkmcnt(3)
	v_mfma_f32_16x16x32_f16 v[90:93], v[22:25], v[42:45], v[90:93]
	s_waitcnt lgkmcnt(2)
	v_mfma_f32_16x16x32_f16 v[94:97], v[22:25], v[74:77], v[94:97]
	s_waitcnt lgkmcnt(1)
	v_mfma_f32_16x16x32_f16 v[98:101], v[22:25], v[82:85], v[98:101]
	s_waitcnt lgkmcnt(0)
	v_mfma_f32_16x16x32_f16 v[12:15], v[22:25], v[86:89], v[12:15]
	s_waitcnt vmcnt(4)
	v_mfma_f32_16x16x32_f16 v[16:19], v[106:109], v[42:45], v[16:19]
	v_mfma_f32_16x16x32_f16 v[20:23], v[106:109], v[74:77], v[34:37]
	v_mfma_f32_16x16x32_f16 v[34:37], v[106:109], v[82:85], v[46:49]
	v_mfma_f32_16x16x32_f16 v[4:7], v[106:109], v[86:89], v[4:7]
	s_waitcnt vmcnt(3)
	v_mfma_f32_16x16x32_f16 v[8:11], v[130:133], v[42:45], v[8:11]
	v_mfma_f32_16x16x32_f16 v[24:27], v[130:133], v[74:77], v[26:29]
	v_mfma_f32_16x16x32_f16 v[38:41], v[130:133], v[82:85], v[38:41]
	v_mfma_f32_16x16x32_f16 v[0:3], v[130:133], v[86:89], v[0:3]
	ds_read_b128 v[42:45], v79
	ds_read_b128 v[46:49], v79 offset:8192
	ds_read_b128 v[74:77], v79 offset:16384
	ds_read_b128 v[82:85], v79 offset:24576
	s_waitcnt vmcnt(2) lgkmcnt(3)
	v_mfma_f32_16x16x32_f16 v[86:89], v[30:33], v[42:45], v[90:93]
	s_waitcnt lgkmcnt(2)
	v_mfma_f32_16x16x32_f16 v[90:93], v[30:33], v[46:49], v[94:97]
	s_waitcnt lgkmcnt(1)
	v_mfma_f32_16x16x32_f16 v[94:97], v[30:33], v[74:77], v[98:101]
	s_waitcnt lgkmcnt(0)
	v_mfma_f32_16x16x32_f16 v[12:15], v[30:33], v[82:85], v[12:15]
	s_waitcnt vmcnt(1)
	v_mfma_f32_16x16x32_f16 v[16:19], v[102:105], v[42:45], v[16:19]
	v_mfma_f32_16x16x32_f16 v[20:23], v[102:105], v[46:49], v[20:23]
	v_mfma_f32_16x16x32_f16 v[28:31], v[102:105], v[74:77], v[34:37]
	v_mfma_f32_16x16x32_f16 v[4:7], v[102:105], v[82:85], v[4:7]
	s_waitcnt vmcnt(0)
	v_mfma_f32_16x16x32_f16 v[8:11], v[126:129], v[42:45], v[8:11]
	v_mfma_f32_16x16x32_f16 v[24:27], v[126:129], v[46:49], v[24:27]
	v_mfma_f32_16x16x32_f16 v[32:35], v[126:129], v[74:77], v[38:41]
	v_mfma_f32_16x16x32_f16 v[0:3], v[126:129], v[82:85], v[0:3]
	s_nop 1
	global_load_dwordx4 v[36:39], v[56:57], off offset:1536
	global_load_dwordx4 v[40:43], v[56:57], off offset:1600
	global_load_dwordx4 v[44:47], v[56:57], off offset:1664
	v_mov_b32_e32 v58, v21
	v_mov_b32_e32 v59, v22
	v_mov_b32_e32 v74, v29
	v_mov_b32_e32 v56, v13
	v_mov_b32_e32 v57, v14
	v_mov_b32_e32 v75, v30
	v_mov_b32_e32 v48, v91
	v_mov_b32_e32 v49, v92
	v_mov_b32_e32 v54, v95
	v_mov_b32_e32 v55, v96
	v_mov_b32_e32 v76, v5
	v_mov_b32_e32 v77, v6
	s_barrier
	s_waitcnt vmcnt(2)
	v_pk_add_f32 v[78:79], v[86:87], v[36:37]
	v_pk_add_f32 v[82:83], v[88:89], v[38:39]
	v_add_f32_e32 v21, v90, v36
	v_pk_mov_b32 v[84:85], v[36:37], v[38:39] op_sel:[1,0]
	v_add_f32_e32 v22, v93, v39
	v_add_f32_e32 v29, v94, v36
	v_add_f32_e32 v36, v12, v36
	v_add_f32_e32 v37, v15, v39
	s_waitcnt vmcnt(1)
	v_add_f32_e32 v38, v20, v40
	v_add_f32_e32 v23, v23, v43
	v_add_f32_e32 v30, v97, v39
	v_pk_add_f32 v[12:13], v[16:17], v[40:41]
	v_pk_add_f32 v[14:15], v[18:19], v[42:43]
	v_pk_mov_b32 v[16:17], v[40:41], v[42:43] op_sel:[1,0]
	v_add_f32_e32 v28, v28, v40
	v_add_f32_e32 v31, v31, v43
	v_add_f32_e32 v39, v4, v40
	v_add_f32_e32 v40, v7, v43
	v_cvt_f16_f32_e32 v41, v21
	v_cvt_f16_f32_e32 v42, v22
	v_cvt_f16_f32_e32 v36, v36
	v_cvt_f16_f32_e32 v37, v37
	v_cvt_f16_f32_e32 v38, v38
	v_cvt_f16_f32_e32 v43, v23
	v_cvt_f16_f32_e32 v29, v29
	v_cvt_f16_f32_e32 v30, v30
	v_cvt_f16_f32_e32 v28, v28
	v_cvt_f16_f32_e32 v31, v31
	v_cvt_f16_f32_e32 v39, v39
	v_cvt_f16_f32_e32 v40, v40
	s_waitcnt vmcnt(0)
	v_pk_add_f32 v[4:5], v[8:9], v[44:45]
	v_pk_add_f32 v[6:7], v[10:11], v[46:47]
	v_pk_add_f32 v[10:11], v[48:49], v[84:85]
	v_pk_add_f32 v[20:21], v[56:57], v[84:85]
	v_cvt_pk_f16_f32 v12, v12, v13
	v_cvt_pk_f16_f32 v13, v14, v15
	v_pk_add_f32 v[14:15], v[58:59], v[16:17]
	v_cvt_pk_f16_f32 v8, v78, v79
	v_cvt_pk_f16_f32 v9, v82, v83
	v_pk_add_f32 v[18:19], v[54:55], v[84:85]
	v_pk_add_f32 v[22:23], v[74:75], v[16:17]
	v_pk_add_f32 v[16:17], v[76:77], v[16:17]
	v_cvt_pk_f16_f32 v4, v4, v5
	v_cvt_pk_f16_f32 v5, v6, v7
	v_cvt_pk_f16_f32 v6, v10, v11
	v_cvt_pk_f16_f32 v10, v20, v21
	v_cvt_pk_f16_f32 v11, v14, v15
	v_cvt_pk_f16_f32 v7, v18, v19
	v_cvt_pk_f16_f32 v14, v22, v23
	v_cvt_pk_f16_f32 v15, v16, v17
	ds_write2_b64 v73, v[8:9], v[12:13] offset1:4
	ds_write_b64 v69, v[4:5] offset:32832
	v_pack_b32_f16 v4, v41, v6
	v_alignbit_b32 v5, v42, v6, 16
	v_pack_b32_f16 v8, v36, v10
	v_alignbit_b32 v9, v37, v10, 16
	v_pack_b32_f16 v10, v38, v11
	v_alignbit_b32 v11, v43, v11, 16
	v_add_f32_e32 v24, v24, v44
	v_pack_b32_f16 v6, v29, v7
	v_alignbit_b32 v7, v30, v7, 16
	v_pack_b32_f16 v12, v28, v14
	v_alignbit_b32 v13, v31, v14, 16
	v_pack_b32_f16 v14, v39, v15
	v_alignbit_b32 v15, v40, v15, 16
	ds_write2_b64 v70, v[4:5], v[10:11] offset0:32 offset1:36
	ds_write2_b64 v71, v[6:7], v[12:13] offset0:64 offset1:68
	ds_write2_b64 v80, v[8:9], v[14:15] offset1:4
	v_add_f32_e32 v8, v27, v47
	v_cvt_f16_f32_e32 v24, v24
	v_cvt_f16_f32_e32 v8, v8
	v_mov_b32_e32 v4, v25
	v_mov_b32_e32 v5, v26
	v_pk_mov_b32 v[6:7], v[44:45], v[46:47] op_sel:[1,0]
	v_add_f32_e32 v9, v35, v47
	v_pk_add_f32 v[4:5], v[4:5], v[6:7]
	v_cvt_f16_f32_e32 v9, v9
	v_cvt_pk_f16_f32 v5, v4, v5
	v_pack_b32_f16 v4, v24, v5
	v_alignbit_b32 v5, v8, v5, 16
	ds_write_b64 v69, v[4:5] offset:45376
	v_add_f32_e32 v4, v32, v44
	v_cvt_f16_f32_e32 v8, v4
	v_mov_b32_e32 v4, v33
	v_mov_b32_e32 v5, v34
	v_pk_add_f32 v[4:5], v[4:5], v[6:7]
	v_add_f32_e32 v0, v0, v44
	v_cvt_pk_f16_f32 v5, v4, v5
	v_pack_b32_f16 v4, v8, v5
	v_alignbit_b32 v5, v9, v5, 16
	ds_write_b64 v69, v[4:5] offset:57920
	v_cvt_f16_f32_e32 v4, v0
	v_mov_b32_e32 v0, v1
	v_mov_b32_e32 v1, v2
	v_add_f32_e32 v2, v3, v47
	v_cvt_f16_f32_e32 v2, v2
	v_pk_add_f32 v[0:1], v[0:1], v[6:7]
	s_nop 0
	v_cvt_pk_f16_f32 v1, v0, v1
	v_pack_b32_f16 v0, v4, v1
	v_alignbit_b32 v1, v2, v1, 16
	ds_write_b64 v68, v[0:1] offset:32832
	s_waitcnt lgkmcnt(0)
	s_barrier
	ds_read_b128 v[0:3], v51 offset:32768
	ds_read_b128 v[4:7], v81 offset:32768
	s_waitcnt lgkmcnt(1)
	buffer_store_dwordx4 v[0:3], v50, s[24:27], 0 offen offset:768 sc1
	ds_read_b128 v[0:3], v53 offset:32768
	ds_read_b128 v[8:11], v160 offset:32768
	ds_read_b128 v[12:15], v61 offset:32768
	ds_read_b128 v[16:19], v63 offset:32768
	s_waitcnt lgkmcnt(4)
	buffer_store_dwordx4 v[4:7], v52, s[24:27], 0 offen offset:768 sc1
	s_waitcnt lgkmcnt(3)
	buffer_store_dwordx4 v[0:3], v60, s[24:27], 0 offen offset:768 sc1
	s_waitcnt lgkmcnt(2)
	buffer_store_dwordx4 v[8:11], v62, s[24:27], 0 offen offset:768 sc1
	s_waitcnt lgkmcnt(1)
	buffer_store_dwordx4 v[12:15], v64, s[24:27], 0 offen offset:768 sc1
	s_waitcnt lgkmcnt(0)
	buffer_store_dwordx4 v[16:19], v66, s[24:27], 0 offen offset:768 sc1
	s_endpgm
	.p2alignl 8, 3212836864

_Z7k_stageILi0ELi4EEv8AttnArgsPKDF16_PKfPDF16_iii:
	v_readfirstlane_b32 s94, v0
	s_nop 0
	s_lshr_b32 s94, s94, 6
	s_load_dwordx4 s[8:11], s[0:1], 0x70
	s_load_dwordx2 s[20:21], s[0:1], 0x80
	s_load_dwordx4 s[12:15], s[0:1], 0x88
	s_lshl_b32 s5, s2, 5
	s_waitcnt lgkmcnt(0)
	s_and_b32 s15, s5, 0xe0
	s_lshr_b32 s5, s2, 3
	s_add_i32 s15, s15, s5
	s_and_b32 s2, s2, 56
	v_readfirstlane_b32 s4, v0
	v_and_b32_e32 v1, 15, v0
	s_cmp_lt_i32 s14, 1
	v_bfe_u32 v158, v0, 4, 2
	s_cbranch_scc1 .LBB5_79
	s_bfe_u32 s5, s4, 0x10006
	s_lshl_b32 s6, s5, 4
	s_mul_i32 s16, s3, 40
	s_mul_hi_i32 s7, s3, 40
	s_add_u32 s22, s0, s16
	s_addc_u32 s23, s1, s7
	s_load_dwordx4 s[16:19], s[22:23], 0x0
	s_load_dwordx2 s[0:1], s[22:23], 0x10
	v_or_b32_e32 v159, s6, v1
	v_lshlrev_b32_e32 v18, 5, v159
	s_waitcnt lgkmcnt(0)
	global_load_dwordx4 v[2:5], v18, s[18:19]
	global_load_dwordx4 v[6:9], v18, s[0:1]
	global_load_dwordx4 v[10:13], v18, s[18:19] offset:16
	global_load_dwordx4 v[14:17], v18, s[0:1] offset:16
	v_bfe_u32 v21, v0, 7, 1
	v_lshrrev_b32_e32 v19, 4, v0
	v_lshlrev_b16_e32 v23, 2, v21
	v_lshrrev_b32_e32 v18, 5, v0
	v_lshrrev_b32_e32 v20, 6, v0
	v_and_b32_e32 v24, 3, v19
	v_bitop3_b16 v19, v23, v19, 3 bitop3:0xf8
	s_movk_i32 s0, 0x3000
	v_and_b32_e32 v18, 4, v18
	v_and_b32_e32 v22, 4, v20
	v_lshlrev_b32_e32 v20, 12, v20
	v_lshlrev_b32_e32 v21, 11, v21
	v_and_b32_e32 v19, 0xffff, v19
	s_bitcmp1_b32 s4, 6
	v_or_b32_e32 v161, v18, v158
	v_and_or_b32 v162, s15, 56, v22
	v_bitop3_b16 v23, v23, 8, v24 bitop3:0xfe
	v_lshlrev_b32_e32 v24, 3, v22
	v_lshl_or_b32 v22, v22, 12, v21
	v_or3_b32 v163, v20, v21, s0
	v_bitop3_b32 v18, v18, v159, v158 bitop3:0x36
	v_bitop3_b32 v19, s6, v19, v1 bitop3:0x36
	s_cselect_b64 s[24:25], -1, 0
	s_and_b32 s0, s15, 0x1ffc0
	s_movk_i32 s1, 0x2000
	v_lshl_or_b32 v168, v18, 4, v22
	v_lshlrev_b32_e32 v18, 4, v19
	v_or_b32_e32 v19, s0, v162
	v_add3_u32 v170, v22, v18, s1
	v_lshl_or_b32 v18, v19, 6, s2
	v_add_u32_e32 v18, v161, v18
	v_mul_u32_u24_e32 v18, 0x600, v18
	v_and_b32_e32 v20, 0xffff, v23
	v_lshl_or_b32 v18, s5, 8, v18
	v_lshlrev_b32_e32 v160, 9, v158
	v_bitop3_b32 v20, s6, v20, v1 bitop3:0x36
	v_lshl_or_b32 v18, v1, 4, v18
	v_add_u32_e32 v164, -1, v162
	v_add_u32_e32 v165, 4, v162
	v_or3_b32 v166, v161, v24, 8
	v_or_b32_e32 v167, 0x1000, v22
	v_lshl_or_b32 v169, v20, 4, v160
	s_and_b32 s17, s17, 0xffff
	s_mov_b32 s19, 0x20000
	s_mov_b32 s18, 0x1800000
	v_add_u32_e32 v171, 0xfffe7c00, v18
	s_mov_b32 s30, s2
	s_waitcnt vmcnt(3)
	v_cvt_pk_f16_f32 v172, v2, v3
	s_waitcnt vmcnt(2)
	v_cvt_pk_f16_f32 v173, v6, v7
	v_cvt_pk_f16_f32 v174, v4, v5
	v_cvt_pk_f16_f32 v175, v8, v9
	s_waitcnt vmcnt(1)
	v_cvt_pk_f16_f32 v176, v10, v11
	s_waitcnt vmcnt(0)
	v_cvt_pk_f16_f32 v177, v14, v15
	v_cvt_pk_f16_f32 v178, v12, v13
	v_cvt_pk_f16_f32 v179, v16, v17
	s_branch .LBB5_4

.LBB5_79:
	s_mul_i32 s0, s13, s3
	s_lshl_b32 s1, s15, 6
	s_add_i32 s0, s0, s12
	s_and_b32 s1, s1, 0xfffffe00
	s_or_b32 s6, s1, s2
	s_mul_i32 s2, s0, 0x60000
	s_mul_hi_i32 s1, s0, 0x60000
	s_add_u32 s2, s8, s2
	s_mulk_i32 s0, 0x300
	s_addc_u32 s7, s9, s1
	s_ashr_i32 s1, s0, 31
	s_lshl_b64 s[0:1], s[0:1], 2
	s_add_u32 s4, s10, s0
	s_addc_u32 s5, s11, s1
	s_mul_i32 s0, s3, 0x1800000
	s_mul_hi_i32 s1, s3, 0x1800000
	s_add_u32 s0, s20, s0
	v_readfirstlane_b32 s3, v0
	s_addc_u32 s1, s21, s1
	s_lshr_b32 s8, s3, 6
	s_and_b32 s1, s1, 0xffff
	s_mul_i32 s9, s8, 0x6000
	v_and_b32_e32 v2, 63, v0
	s_mul_hi_u32 s3, s8, 0x6000
	s_add_u32 s2, s2, s9
	s_addc_u32 s3, s7, s3
	v_lshlrev_b32_e32 v56, 4, v2
	v_mov_b32_e32 v57, 0
	v_lshl_add_u64 v[54:55], s[2:3], 0, v[56:57]
	s_movk_i32 s7, 0x1000
	v_add_co_u32_e32 v50, vcc, s7, v54
	s_movk_i32 s7, 0x2000
	s_nop 0
	v_addc_co_u32_e32 v51, vcc, 0, v55, vcc
	v_add_co_u32_e32 v52, vcc, s7, v54
	global_load_dwordx4 v[2:5], v56, s[2:3] offset:1024
	global_load_dwordx4 v[6:9], v56, s[2:3] offset:2048
	v_addc_co_u32_e32 v53, vcc, 0, v55, vcc
	global_load_dwordx4 v[10:13], v56, s[2:3] offset:3072
	global_load_dwordx4 v[14:17], v[52:53], off offset:-4096
	global_load_dwordx4 v[18:21], v[50:51], off offset:1024
	global_load_dwordx4 v[22:25], v[50:51], off offset:2048
	global_load_dwordx4 v[26:29], v56, s[2:3]
	global_load_dwordx4 v[30:33], v[50:51], off offset:3072
	global_load_dwordx4 v[34:37], v[52:53], off
	global_load_dwordx4 v[38:41], v[52:53], off offset:1024
	global_load_dwordx4 v[42:45], v[52:53], off offset:2048
	global_load_dwordx4 v[46:49], v[52:53], off offset:3072
	s_movk_i32 s2, 0x3000
	v_add_co_u32_e32 v58, vcc, s2, v54
	s_movk_i32 s2, 0x4000
	s_nop 0
	v_addc_co_u32_e32 v59, vcc, 0, v55, vcc
	v_add_co_u32_e32 v140, vcc, s2, v54
	s_waitcnt lgkmcnt(0)
	s_nop 0
	v_addc_co_u32_e32 v141, vcc, 0, v55, vcc
	s_barrier
	s_cmp_lt_u32 s94, 4
	s_cbranch_scc1 .Lmystag5_1
	s_sleep 4
.Lmystag5_1:
	global_load_dwordx4 v[50:53], v[140:141], off offset:-4096
	global_load_dwordx4 v[62:65], v[58:59], off offset:1024
	global_load_dwordx4 v[68:71], v[58:59], off offset:2048
	v_lshlrev_b32_e32 v67, 9, v1
	v_xor_b32_e32 v61, v158, v1
	v_lshl_or_b32 v66, v61, 4, v67
	ds_read_b128 v[72:75], v66
	ds_read_b128 v[76:79], v66 offset:8192
	ds_read_b128 v[80:83], v66 offset:16384
	ds_read_b128 v[84:87], v66 offset:24576
	v_mul_u32_u24_e32 v60, 0x556, v0
	v_lshrrev_b32_e32 v60, 16, v60
	s_mul_i32 s7, s8, 48
	v_lshlrev_b32_e32 v61, 3, v60
	s_movk_i32 s9, 0x47
	v_lshl_or_b32 v56, v158, 2, s7
	s_mov_b32 s7, 0xfffffd0
	v_bitop3_b32 v61, v61, s9, v60 bitop3:0xc8
	s_mov_b32 s2, 0x1800000
	s_mov_b32 s3, 0x20000
	s_mulk_i32 s8, 0x60
	v_mul_lo_u32 v150, v60, s7
	v_or_b32_e32 v61, s6, v61
	s_waitcnt vmcnt(8) lgkmcnt(3)
	v_mfma_f32_16x16x32_f16 v[88:91], v[26:29], v[72:75], 0
	s_waitcnt lgkmcnt(2)
	v_mfma_f32_16x16x32_f16 v[92:95], v[26:29], v[76:79], 0
	s_waitcnt lgkmcnt(1)
	v_mfma_f32_16x16x32_f16 v[96:99], v[26:29], v[80:83], 0
	s_waitcnt lgkmcnt(0)
	v_mfma_f32_16x16x32_f16 v[26:29], v[26:29], v[84:87], 0
	v_mfma_f32_16x16x32_f16 v[100:103], v[2:5], v[72:75], 0
	v_mfma_f32_16x16x32_f16 v[104:107], v[2:5], v[76:79], 0
	v_mfma_f32_16x16x32_f16 v[108:111], v[2:5], v[80:83], 0
	v_mfma_f32_16x16x32_f16 v[2:5], v[2:5], v[84:87], 0
	v_mfma_f32_16x16x32_f16 v[112:115], v[6:9], v[72:75], 0
	v_mfma_f32_16x16x32_f16 v[74:77], v[6:9], v[76:79], 0
	v_mfma_f32_16x16x32_f16 v[78:81], v[6:9], v[80:83], 0
	v_mfma_f32_16x16x32_f16 v[6:9], v[6:9], v[84:87], 0
	global_load_dwordx4 v[82:85], v[58:59], off offset:3072
	global_load_dwordx4 v[116:119], v[140:141], off
	global_load_dwordx4 v[120:123], v[140:141], off offset:1024
	v_bitop3_b32 v58, v158, v1, 4 bitop3:0x36
	v_lshl_or_b32 v72, v58, 4, v67
	ds_read_b128 v[124:127], v72
	ds_read_b128 v[128:131], v72 offset:8192
	ds_read_b128 v[132:135], v72 offset:16384
	ds_read_b128 v[136:139], v72 offset:24576
	s_waitcnt lgkmcnt(3)
	v_mfma_f32_16x16x32_f16 v[86:89], v[10:13], v[124:127], v[88:91]
	s_waitcnt lgkmcnt(2)
	v_mfma_f32_16x16x32_f16 v[90:93], v[10:13], v[128:131], v[92:95]
	s_waitcnt lgkmcnt(1)
	v_mfma_f32_16x16x32_f16 v[94:97], v[10:13], v[132:135], v[96:99]
	s_waitcnt lgkmcnt(0)
	v_mfma_f32_16x16x32_f16 v[10:13], v[10:13], v[136:139], v[26:29]
	v_mfma_f32_16x16x32_f16 v[26:29], v[14:17], v[124:127], v[100:103]
	v_mfma_f32_16x16x32_f16 v[98:101], v[14:17], v[128:131], v[104:107]
	v_mfma_f32_16x16x32_f16 v[102:105], v[14:17], v[132:135], v[108:111]
	v_mfma_f32_16x16x32_f16 v[2:5], v[14:17], v[136:139], v[2:5]
	v_mfma_f32_16x16x32_f16 v[14:17], v[18:21], v[124:127], v[112:115]
	v_mfma_f32_16x16x32_f16 v[106:109], v[18:21], v[128:131], v[74:77]
	v_mfma_f32_16x16x32_f16 v[76:79], v[18:21], v[132:135], v[78:81]
	v_mfma_f32_16x16x32_f16 v[6:9], v[18:21], v[136:139], v[6:9]
	s_movk_i32 s9, 0x5000
	v_add_co_u32_e32 v58, vcc, s9, v54
	global_load_dwordx4 v[110:113], v[140:141], off offset:2048
	global_load_dwordx4 v[124:127], v[140:141], off offset:3072
	v_addc_co_u32_e32 v59, vcc, 0, v55, vcc
	global_load_dwordx4 v[128:131], v[58:59], off
	v_bitop3_b32 v18, v158, v1, 8 bitop3:0x36
	v_lshl_or_b32 v74, v18, 4, v67
	ds_read_b128 v[18:21], v74
	ds_read_b128 v[132:135], v74 offset:8192
	ds_read_b128 v[136:139], v74 offset:16384
	ds_read_b128 v[140:143], v74 offset:24576
	s_waitcnt lgkmcnt(3)
	v_mfma_f32_16x16x32_f16 v[86:89], v[22:25], v[18:21], v[86:89]
	s_waitcnt lgkmcnt(2)
	v_mfma_f32_16x16x32_f16 v[90:93], v[22:25], v[132:135], v[90:93]
	s_waitcnt lgkmcnt(1)
	v_mfma_f32_16x16x32_f16 v[94:97], v[22:25], v[136:139], v[94:97]
	s_waitcnt lgkmcnt(0)
	v_mfma_f32_16x16x32_f16 v[10:13], v[22:25], v[140:143], v[10:13]
	s_waitcnt vmcnt(13)
	v_mfma_f32_16x16x32_f16 v[22:25], v[30:33], v[18:21], v[26:29]
	v_mfma_f32_16x16x32_f16 v[26:29], v[30:33], v[132:135], v[98:101]
	v_mfma_f32_16x16x32_f16 v[98:101], v[30:33], v[136:139], v[102:105]
	v_mfma_f32_16x16x32_f16 v[2:5], v[30:33], v[140:143], v[2:5]
	s_waitcnt vmcnt(12)
	v_mfma_f32_16x16x32_f16 v[14:17], v[34:37], v[18:21], v[14:17]
	v_mfma_f32_16x16x32_f16 v[18:21], v[34:37], v[132:135], v[106:109]
	v_mfma_f32_16x16x32_f16 v[30:33], v[34:37], v[136:139], v[76:79]
	v_mfma_f32_16x16x32_f16 v[6:9], v[34:37], v[140:143], v[6:9]
	global_load_dwordx4 v[102:105], v[58:59], off offset:1024
	global_load_dwordx4 v[106:109], v[58:59], off offset:2048
	global_load_dwordx4 v[132:135], v[58:59], off offset:3072
	v_bitop3_b32 v34, v158, v1, 12 bitop3:0x36
	v_lshl_or_b32 v75, v34, 4, v67
	ds_read_b128 v[34:37], v75
	ds_read_b128 v[76:79], v75 offset:8192
	ds_read_b128 v[136:139], v75 offset:16384
	ds_read_b128 v[140:143], v75 offset:24576
	s_waitcnt vmcnt(14) lgkmcnt(3)
	v_mfma_f32_16x16x32_f16 v[86:89], v[38:41], v[34:37], v[86:89]
	s_waitcnt lgkmcnt(2)
	v_mfma_f32_16x16x32_f16 v[90:93], v[38:41], v[76:79], v[90:93]
	s_waitcnt lgkmcnt(1)
	v_mfma_f32_16x16x32_f16 v[94:97], v[38:41], v[136:139], v[94:97]
	s_waitcnt lgkmcnt(0)
	v_mfma_f32_16x16x32_f16 v[10:13], v[38:41], v[140:143], v[10:13]
	s_waitcnt vmcnt(13)
	v_mfma_f32_16x16x32_f16 v[38:41], v[42:45], v[34:37], v[22:25]
	v_mfma_f32_16x16x32_f16 v[144:147], v[42:45], v[76:79], v[26:29]
	v_mfma_f32_16x16x32_f16 v[98:101], v[42:45], v[136:139], v[98:101]
	v_mfma_f32_16x16x32_f16 v[2:5], v[42:45], v[140:143], v[2:5]
	s_waitcnt vmcnt(12)
	v_mfma_f32_16x16x32_f16 v[14:17], v[46:49], v[34:37], v[14:17]
	v_mfma_f32_16x16x32_f16 v[18:21], v[46:49], v[76:79], v[18:21]
	v_mfma_f32_16x16x32_f16 v[30:33], v[46:49], v[136:139], v[30:33]
	v_mfma_f32_16x16x32_f16 v[6:9], v[46:49], v[140:143], v[6:9]
	s_mov_b32 s9, 0x30000
	v_add_co_u32_e32 v58, vcc, s9, v54
	s_mov_b32 s9, 0x31000
	s_nop 0
	v_addc_co_u32_e32 v59, vcc, 0, v55, vcc
	v_add_co_u32_e32 v148, vcc, s9, v54
	v_bitop3_b32 v42, v158, v1, 16 bitop3:0x36
	s_nop 0
	v_addc_co_u32_e32 v149, vcc, 0, v55, vcc
	global_load_dwordx4 v[34:37], v[148:149], off offset:-4096
	global_load_dwordx4 v[26:29], v[58:59], off offset:1024
	global_load_dwordx4 v[22:25], v[58:59], off offset:2048
	v_lshl_or_b32 v76, v42, 4, v67
	ds_read_b128 v[42:45], v76
	ds_read_b128 v[46:49], v76 offset:8192
	ds_read_b128 v[78:81], v76 offset:16384
	ds_read_b128 v[136:139], v76 offset:24576
	s_waitcnt vmcnt(14) lgkmcnt(3)
	v_mfma_f32_16x16x32_f16 v[86:89], v[50:53], v[42:45], v[86:89]
	s_waitcnt lgkmcnt(2)
	v_mfma_f32_16x16x32_f16 v[90:93], v[50:53], v[46:49], v[90:93]
	s_waitcnt lgkmcnt(1)
	v_mfma_f32_16x16x32_f16 v[94:97], v[50:53], v[78:81], v[94:97]
	s_waitcnt lgkmcnt(0)
	v_mfma_f32_16x16x32_f16 v[10:13], v[50:53], v[136:139], v[10:13]
	s_waitcnt vmcnt(13)
	v_mfma_f32_16x16x32_f16 v[38:41], v[62:65], v[42:45], v[38:41]
	v_mfma_f32_16x16x32_f16 v[50:53], v[62:65], v[46:49], v[144:147]
	v_mfma_f32_16x16x32_f16 v[98:101], v[62:65], v[78:81], v[98:101]
	v_mfma_f32_16x16x32_f16 v[62:65], v[62:65], v[136:139], v[2:5]
	s_waitcnt vmcnt(12)
	v_mfma_f32_16x16x32_f16 v[42:45], v[68:71], v[42:45], v[14:17]
	v_mfma_f32_16x16x32_f16 v[18:21], v[68:71], v[46:49], v[18:21]
	v_mfma_f32_16x16x32_f16 v[30:33], v[68:71], v[78:81], v[30:33]
	v_mfma_f32_16x16x32_f16 v[46:49], v[68:71], v[136:139], v[6:9]
	global_load_dwordx4 v[14:17], v[58:59], off offset:3072
	s_nop 1
	global_load_dwordx4 v[6:9], v[148:149], off
	global_load_dwordx4 v[2:5], v[148:149], off offset:1024
	v_bitop3_b32 v58, v158, v1, 20 bitop3:0x36
	v_lshl_or_b32 v77, v58, 4, v67
	ds_read_b128 v[68:71], v77
	ds_read_b128 v[78:81], v77 offset:8192
	ds_read_b128 v[136:139], v77 offset:16384
	ds_read_b128 v[140:143], v77 offset:24576
	s_waitcnt vmcnt(14) lgkmcnt(3)
	v_mfma_f32_16x16x32_f16 v[86:89], v[82:85], v[68:71], v[86:89]
	s_waitcnt lgkmcnt(2)
	v_mfma_f32_16x16x32_f16 v[90:93], v[82:85], v[78:81], v[90:93]
	s_waitcnt lgkmcnt(1)
	v_mfma_f32_16x16x32_f16 v[94:97], v[82:85], v[136:139], v[94:97]
	s_waitcnt lgkmcnt(0)
	v_mfma_f32_16x16x32_f16 v[82:85], v[82:85], v[140:143], v[10:13]
	s_waitcnt vmcnt(13)
	v_mfma_f32_16x16x32_f16 v[38:41], v[116:119], v[68:71], v[38:41]
	v_mfma_f32_16x16x32_f16 v[50:53], v[116:119], v[78:81], v[50:53]
	v_mfma_f32_16x16x32_f16 v[98:101], v[116:119], v[136:139], v[98:101]
	v_mfma_f32_16x16x32_f16 v[62:65], v[116:119], v[140:143], v[62:65]
	s_waitcnt vmcnt(12)
	v_mfma_f32_16x16x32_f16 v[42:45], v[120:123], v[68:71], v[42:45]
	v_mfma_f32_16x16x32_f16 v[68:71], v[120:123], v[78:81], v[18:21]
	v_mfma_f32_16x16x32_f16 v[114:117], v[120:123], v[136:139], v[30:33]
	v_mfma_f32_16x16x32_f16 v[46:49], v[120:123], v[140:143], v[46:49]
	s_mov_b32 s9, 0x33000
	v_add_co_u32_e32 v58, vcc, s9, v54
	global_load_dwordx4 v[18:21], v[148:149], off offset:2048
	global_load_dwordx4 v[10:13], v[148:149], off offset:3072
	v_addc_co_u32_e32 v59, vcc, 0, v55, vcc
	global_load_dwordx4 v[30:33], v[58:59], off offset:-4096
	v_bitop3_b32 v73, v158, v1, 24 bitop3:0x36
	v_lshl_or_b32 v78, v73, 4, v67
	ds_read_b128 v[118:121], v78
	ds_read_b128 v[136:139], v78 offset:8192
	ds_read_b128 v[140:143], v78 offset:16384
	ds_read_b128 v[144:147], v78 offset:24576
	s_mov_b32 s9, 0x32000
	v_add_co_u32_e32 v148, vcc, s9, v54
	s_nop 1
	v_addc_co_u32_e32 v149, vcc, 0, v55, vcc
	s_waitcnt vmcnt(14) lgkmcnt(3)
	v_mfma_f32_16x16x32_f16 v[86:89], v[110:113], v[118:121], v[86:89]
	s_waitcnt lgkmcnt(2)
	v_mfma_f32_16x16x32_f16 v[90:93], v[110:113], v[136:139], v[90:93]
	s_waitcnt lgkmcnt(1)
	v_mfma_f32_16x16x32_f16 v[94:97], v[110:113], v[140:143], v[94:97]
	s_waitcnt lgkmcnt(0)
	v_mfma_f32_16x16x32_f16 v[80:83], v[110:113], v[144:147], v[82:85]
	s_waitcnt vmcnt(13)
	v_mfma_f32_16x16x32_f16 v[110:113], v[124:127], v[118:121], v[38:41]
	v_mfma_f32_16x16x32_f16 v[50:53], v[124:127], v[136:139], v[50:53]
	v_mfma_f32_16x16x32_f16 v[98:101], v[124:127], v[140:143], v[98:101]
	v_mfma_f32_16x16x32_f16 v[62:65], v[124:127], v[144:147], v[62:65]
	s_waitcnt vmcnt(12)
	v_mfma_f32_16x16x32_f16 v[118:121], v[128:131], v[118:121], v[42:45]
	v_mfma_f32_16x16x32_f16 v[68:71], v[128:131], v[136:139], v[68:71]
	v_mfma_f32_16x16x32_f16 v[114:117], v[128:131], v[140:143], v[114:117]
	v_mfma_f32_16x16x32_f16 v[122:125], v[128:131], v[144:147], v[46:49]
	s_nop 2
	global_load_dwordx4 v[46:49], v[148:149], off offset:1024
	global_load_dwordx4 v[42:45], v[148:149], off offset:2048
	global_load_dwordx4 v[38:41], v[148:149], off offset:3072
	v_bitop3_b32 v73, v158, v1, 28 bitop3:0x36
	v_lshl_or_b32 v79, v73, 4, v67
	ds_read_b128 v[126:129], v79
	ds_read_b128 v[136:139], v79 offset:8192
	ds_read_b128 v[140:143], v79 offset:16384
	ds_read_b128 v[144:147], v79 offset:24576
	s_waitcnt vmcnt(14) lgkmcnt(3)
	v_mfma_f32_16x16x32_f16 v[84:87], v[102:105], v[126:129], v[86:89]
	s_waitcnt lgkmcnt(2)
	v_mfma_f32_16x16x32_f16 v[88:91], v[102:105], v[136:139], v[90:93]
	s_waitcnt lgkmcnt(1)
	v_mfma_f32_16x16x32_f16 v[92:95], v[102:105], v[140:143], v[94:97]
	s_waitcnt lgkmcnt(0)
	v_mfma_f32_16x16x32_f16 v[80:83], v[102:105], v[144:147], v[80:83]
	s_waitcnt vmcnt(13)
	v_mfma_f32_16x16x32_f16 v[102:105], v[106:109], v[126:129], v[110:113]
	v_mfma_f32_16x16x32_f16 v[110:113], v[106:109], v[136:139], v[50:53]
	v_mfma_f32_16x16x32_f16 v[96:99], v[106:109], v[140:143], v[98:101]
	v_mfma_f32_16x16x32_f16 v[62:65], v[106:109], v[144:147], v[62:65]
	s_waitcnt vmcnt(12)
	v_mfma_f32_16x16x32_f16 v[106:109], v[132:135], v[126:129], v[118:121]
	v_mfma_f32_16x16x32_f16 v[118:121], v[132:135], v[136:139], v[68:71]
	v_mfma_f32_16x16x32_f16 v[114:117], v[132:135], v[140:143], v[114:117]
	v_mfma_f32_16x16x32_f16 v[50:53], v[132:135], v[144:147], v[122:125]
	v_lshl_add_u64 v[56:57], v[56:57], 2, s[4:5]
	s_nop 1
	global_load_dwordx4 v[122:125], v[56:57], off
	global_load_dwordx4 v[126:129], v[56:57], off offset:64
	global_load_dwordx4 v[130:133], v[56:57], off offset:128
	v_lshl_or_b32 v67, v158, 3, s8
	s_movk_i32 s4, 0x310
	v_mov_b32_e32 v100, v89
	v_mov_b32_e32 v101, v90
	v_mov_b32_e32 v134, v93
	v_mov_b32_e32 v135, v94
	v_mov_b32_e32 v140, v97
	v_mov_b32_e32 v141, v98
	v_mad_u32_u24 v69, v1, s4, v67
	v_mov_b32_e32 v143, v64
	v_mov_b32_e32 v136, v81
	v_mov_b32_e32 v137, v82
	v_mov_b32_e32 v138, v111
	v_mov_b32_e32 v139, v112
	v_mov_b32_e32 v142, v63
	v_add_u32_e32 v73, 0x8000, v69
	s_barrier
	v_add_u32_e32 v70, 0xb000, v69
	v_add_u32_e32 v71, 0xe000, v69
	v_add_u32_e32 v68, 0x9300, v69
	s_movk_i32 s5, 0x600
	s_movk_i32 s10, 0x1c7
	s_waitcnt vmcnt(2)
	v_pk_add_f32 v[84:85], v[84:85], v[122:123]
	v_add_f32_e32 v1, v88, v122
	v_pk_mov_b32 v[88:89], v[122:123], v[124:125] op_sel:[1,0]
	v_add_f32_e32 v67, v91, v125
	v_add_f32_e32 v92, v92, v122
	v_add_f32_e32 v93, v95, v125
	v_add_f32_e32 v94, v80, v122
	v_add_f32_e32 v95, v83, v125
	s_waitcnt vmcnt(1)
	v_add_f32_e32 v97, v110, v126
	v_add_f32_e32 v98, v113, v129
	v_add_f32_e32 v96, v96, v126
	v_add_f32_e32 v99, v99, v129
	v_cvt_pk_f16_f32 v64, v84, v85
	v_cvt_f16_f32_e32 v1, v1
	v_pk_add_f32 v[84:85], v[100:101], v[88:89]
	v_cvt_f16_f32_e32 v67, v67
	v_cvt_f16_f32_e32 v100, v92
	v_cvt_f16_f32_e32 v101, v93
	v_cvt_f16_f32_e32 v94, v94
	v_cvt_f16_f32_e32 v95, v95
	v_cvt_f16_f32_e32 v97, v97
	v_cvt_f16_f32_e32 v98, v98
	v_pk_add_f32 v[86:87], v[86:87], v[124:125]
	v_pk_add_f32 v[80:81], v[102:103], v[126:127]
	v_pk_add_f32 v[82:83], v[104:105], v[128:129]
	v_pk_mov_b32 v[90:91], v[126:127], v[128:129] op_sel:[1,0]
	v_cvt_f16_f32_e32 v96, v96
	v_cvt_f16_f32_e32 v99, v99
	v_add_f32_e32 v102, v62, v126
	v_add_f32_e32 v103, v65, v129
	s_waitcnt vmcnt(0)
	v_pk_add_f32 v[62:63], v[106:107], v[130:131]
	v_cvt_pk_f16_f32 v65, v86, v87
	v_pk_add_f32 v[86:87], v[134:135], v[88:89]
	v_pk_add_f32 v[88:89], v[136:137], v[88:89]
	v_cvt_pk_f16_f32 v80, v80, v81
	v_cvt_pk_f16_f32 v81, v82, v83
	v_pk_add_f32 v[82:83], v[138:139], v[90:91]
	v_pk_add_f32 v[92:93], v[140:141], v[90:91]
	v_cvt_pk_f16_f32 v62, v62, v63
	v_cvt_pk_f16_f32 v63, v84, v85
	v_cvt_pk_f16_f32 v84, v86, v87
	v_cvt_pk_f16_f32 v85, v88, v89
	v_cvt_pk_f16_f32 v86, v82, v83
	v_cvt_pk_f16_f32 v87, v92, v93
	ds_write2_b64 v73, v[64:65], v[80:81] offset1:4
	v_pack_b32_f16 v64, v1, v63
	v_alignbit_b32 v65, v67, v63, 16
	v_pack_b32_f16 v80, v100, v84
	v_alignbit_b32 v81, v101, v84, 16
	v_pack_b32_f16 v82, v94, v85
	v_alignbit_b32 v83, v95, v85, 16
	v_pack_b32_f16 v84, v97, v86
	v_alignbit_b32 v85, v98, v86, 16
	v_pack_b32_f16 v86, v96, v87
	v_alignbit_b32 v87, v99, v87, 16
	ds_write2_b64 v70, v[64:65], v[84:85] offset0:32 offset1:36
	ds_write2_b64 v71, v[80:81], v[86:87] offset0:64 offset1:68
	v_pk_add_f32 v[64:65], v[108:109], v[132:133]
	v_add_f32_e32 v1, v118, v130
	v_cvt_pk_f16_f32 v63, v64, v65
	v_cvt_f16_f32_e32 v1, v1
	v_add_f32_e32 v67, v121, v133
	ds_write_b64 v69, v[62:63] offset:32832
	v_mov_b32_e32 v62, v119
	v_mov_b32_e32 v63, v120
	v_pk_mov_b32 v[64:65], v[130:131], v[132:133] op_sel:[1,0]
	v_cvt_f16_f32_e32 v67, v67
	v_pk_add_f32 v[62:63], v[62:63], v[64:65]
	v_cvt_f16_f32_e32 v102, v102
	v_cvt_pk_f16_f32 v63, v62, v63
	v_pack_b32_f16 v62, v1, v63
	v_add_f32_e32 v1, v114, v130
	v_alignbit_b32 v63, v67, v63, 16
	v_cvt_f16_f32_e32 v1, v1
	ds_write_b64 v69, v[62:63] offset:45376
	v_mov_b32_e32 v62, v115
	v_mov_b32_e32 v63, v116
	v_pk_add_f32 v[62:63], v[62:63], v[64:65]
	v_add_f32_e32 v67, v117, v133
	v_cvt_pk_f16_f32 v63, v62, v63
	v_pack_b32_f16 v62, v1, v63
	v_add_f32_e32 v1, v50, v130
	v_mov_b32_e32 v50, v51
	v_mov_b32_e32 v51, v52
	v_add_f32_e32 v52, v53, v133
	v_cvt_f16_f32_e32 v103, v103
	v_cvt_f16_f32_e32 v67, v67
	v_cvt_f16_f32_e32 v1, v1
	v_cvt_f16_f32_e32 v52, v52
	v_pk_add_f32 v[90:91], v[142:143], v[90:91]
	v_pk_add_f32 v[50:51], v[50:51], v[64:65]
	v_cvt_pk_f16_f32 v89, v90, v91
	v_cvt_pk_f16_f32 v51, v50, v51
	v_pack_b32_f16 v88, v102, v89
	v_alignbit_b32 v89, v103, v89, 16
	v_add_u32_e32 v80, 0x8000, v68
	v_alignbit_b32 v63, v67, v63, 16
	v_pack_b32_f16 v50, v1, v51
	v_alignbit_b32 v51, v52, v51, 16
	ds_write2_b64 v80, v[82:83], v[88:89] offset1:4
	ds_write_b64 v69, v[62:63] offset:57920
	ds_write_b64 v68, v[50:51] offset:32832
	s_waitcnt lgkmcnt(0)
	s_barrier
	s_cmp_lt_u32 s94, 4
	s_cbranch_scc1 .Lmystag5_3
	s_sleep 4
.Lmystag5_3:
	global_load_dwordx4 v[82:85], v[58:59], off
	global_load_dwordx4 v[86:89], v[58:59], off offset:1024
	global_load_dwordx4 v[90:93], v[58:59], off offset:2048
	v_add_lshl_u32 v52, v150, v0, 4
	v_mad_u64_u32 v[50:51], s[8:9], v61, s5, v[52:53]
	v_or_b32_e32 v1, 0x200, v0
	v_mad_u32_u24 v51, v60, s4, v52
	v_mul_u32_u24_e32 v52, 0x556, v1
	v_lshrrev_b32_e32 v53, 16, v52
	v_mul_lo_u32 v52, v53, s7
	v_add_lshl_u32 v52, v52, v1, 4
	v_lshlrev_b32_e32 v1, 3, v53
	s_movk_i32 s8, 0xc7
	ds_read_b128 v[60:63], v51 offset:32768
	v_bitop3_b32 v1, v1, s8, v53 bitop3:0xc8
	v_or_b32_e32 v1, s6, v1
	v_mad_u32_u24 v81, v53, s4, v52
	v_mad_u64_u32 v[52:53], s[8:9], v1, s5, v[52:53]
	v_or_b32_e32 v1, 0x400, v0
	v_mul_u32_u24_e32 v53, 0x556, v1
	v_lshrrev_b32_e32 v53, 16, v53
	ds_read_b128 v[94:97], v81 offset:32768
	s_waitcnt lgkmcnt(1)
	buffer_store_dwordx4 v[60:63], v50, s[0:3], 0 offen sc1
	s_waitcnt lgkmcnt(0)
	buffer_store_dwordx4 v[94:97], v52, s[0:3], 0 offen sc1
	v_lshlrev_b32_e32 v61, 3, v53
	v_mul_lo_u32 v60, v53, s7
	v_bitop3_b32 v61, v61, s10, v53 bitop3:0xc8
	v_or_b32_e32 v61, s6, v61
	v_add_lshl_u32 v62, v60, v1, 4
	v_mad_u64_u32 v[60:61], s[8:9], v61, s5, v[62:63]
	v_or_b32_e32 v1, 0x600, v0
	v_mad_u32_u24 v53, v53, s4, v62
	v_mul_u32_u24_e32 v61, 0x556, v1
	ds_read_b128 v[62:65], v53 offset:32768
	v_lshrrev_b32_e32 v67, 16, v61
	v_mul_lo_u32 v94, v67, s7
	v_add_lshl_u32 v98, v94, v1, 4
	v_lshrrev_b32_e32 v1, 13, v61
	v_mad_u32_u24 v160, v67, s4, v98
	v_and_b32_e32 v1, 0x1c0, v1
	v_bfe_u32 v61, v61, 16, 3
	ds_read_b128 v[94:97], v160 offset:32768
	v_or3_b32 v1, s6, v61, v1
	s_waitcnt lgkmcnt(1)
	buffer_store_dwordx4 v[62:65], v60, s[0:3], 0 offen sc1
	s_nop 1
	v_mad_u64_u32 v[62:63], s[8:9], v1, s5, v[98:99]
	v_or_b32_e32 v1, 0x800, v0
	v_mul_u32_u24_e32 v61, 0xaab, v1
	v_lshrrev_b32_e32 v61, 17, v61
	v_mul_lo_u32 v63, v61, s7
	v_lshlrev_b32_e32 v64, 3, v61
	s_waitcnt lgkmcnt(0)
	buffer_store_dwordx4 v[94:97], v62, s[0:3], 0 offen sc1
	v_bitop3_b32 v64, v64, s10, v61 bitop3:0xc8
	v_or_b32_e32 v64, s6, v64
	v_add_lshl_u32 v94, v63, v1, 4
	v_mad_u32_u24 v61, v61, s4, v94
	v_or_b32_e32 v0, 0xa00, v0
	v_mad_u64_u32 v[64:65], s[8:9], v64, s5, v[94:95]
	ds_read_b128 v[94:97], v61 offset:32768
	v_mul_u32_u24_e32 v1, 0xaab, v0
	v_lshrrev_b32_e32 v63, 17, v1
	v_mul_lo_u32 v65, v63, s7
	v_add_lshl_u32 v0, v65, v0, 4
	v_mad_u32_u24 v63, v63, s4, v0
	ds_read_b128 v[98:101], v63 offset:32768
	s_waitcnt lgkmcnt(1)
	buffer_store_dwordx4 v[94:97], v64, s[0:3], 0 offen sc1
	ds_read_b128 v[94:97], v66
	ds_read_b128 v[102:105], v66 offset:8192
	ds_read_b128 v[106:109], v66 offset:16384
	ds_read_b128 v[110:113], v66 offset:24576
	v_lshrrev_b32_e32 v65, 14, v1
	v_and_b32_e32 v65, 0x1c0, v65
	v_bfe_u32 v1, v1, 17, 3
	v_or3_b32 v1, s6, v1, v65
	v_mad_u64_u32 v[66:67], s[4:5], v1, s5, v[0:1]
	s_waitcnt lgkmcnt(4)
	buffer_store_dwordx4 v[98:101], v66, s[0:3], 0 offen sc1
	s_waitcnt lgkmcnt(3)
	s_nop 0
	v_mfma_f32_16x16x32_f16 v[98:101], v[34:37], v[94:97], 0
	s_waitcnt lgkmcnt(2)
	v_mfma_f32_16x16x32_f16 v[114:117], v[34:37], v[102:105], 0
	s_waitcnt lgkmcnt(1)
	v_mfma_f32_16x16x32_f16 v[118:121], v[34:37], v[106:109], 0
	s_waitcnt lgkmcnt(0)
	v_mfma_f32_16x16x32_f16 v[34:37], v[34:37], v[110:113], 0
	v_mfma_f32_16x16x32_f16 v[122:125], v[26:29], v[94:97], 0
	v_mfma_f32_16x16x32_f16 v[126:129], v[26:29], v[102:105], 0
	v_mfma_f32_16x16x32_f16 v[130:133], v[26:29], v[106:109], 0
	v_mfma_f32_16x16x32_f16 v[26:29], v[26:29], v[110:113], 0
	v_mfma_f32_16x16x32_f16 v[94:97], v[22:25], v[94:97], 0
	v_mfma_f32_16x16x32_f16 v[102:105], v[22:25], v[102:105], 0
	v_mfma_f32_16x16x32_f16 v[106:109], v[22:25], v[106:109], 0
	v_mfma_f32_16x16x32_f16 v[22:25], v[22:25], v[110:113], 0
	s_mov_b32 s4, 0x34000
	v_add_co_u32_e32 v158, vcc, s4, v54
	s_mov_b32 s4, 0x35000
	s_nop 0
	v_addc_co_u32_e32 v159, vcc, 0, v55, vcc
	v_add_co_u32_e32 v54, vcc, s4, v54
	s_nop 1
	v_addc_co_u32_e32 v55, vcc, 0, v55, vcc
	global_load_dwordx4 v[110:113], v[54:55], off offset:-4096
	global_load_dwordx4 v[134:137], v[58:59], off offset:3072
	global_load_dwordx4 v[138:141], v[158:159], off offset:1024
	ds_read_b128 v[142:145], v72
	ds_read_b128 v[146:149], v72 offset:8192
	ds_read_b128 v[150:153], v72 offset:16384
	ds_read_b128 v[154:157], v72 offset:24576
	s_waitcnt lgkmcnt(3)
	v_mfma_f32_16x16x32_f16 v[98:101], v[14:17], v[142:145], v[98:101]
	s_waitcnt lgkmcnt(2)
	v_mfma_f32_16x16x32_f16 v[114:117], v[14:17], v[146:149], v[114:117]
	s_waitcnt lgkmcnt(1)
	v_mfma_f32_16x16x32_f16 v[118:121], v[14:17], v[150:153], v[118:121]
	s_waitcnt lgkmcnt(0)
	v_mfma_f32_16x16x32_f16 v[14:17], v[14:17], v[154:157], v[34:37]
	v_mfma_f32_16x16x32_f16 v[34:37], v[6:9], v[142:145], v[122:125]
	v_mfma_f32_16x16x32_f16 v[122:125], v[6:9], v[146:149], v[126:129]
	v_mfma_f32_16x16x32_f16 v[126:129], v[6:9], v[150:153], v[130:133]
	v_mfma_f32_16x16x32_f16 v[6:9], v[6:9], v[154:157], v[26:29]
	v_mfma_f32_16x16x32_f16 v[26:29], v[2:5], v[142:145], v[94:97]
	v_mfma_f32_16x16x32_f16 v[94:97], v[2:5], v[146:149], v[102:105]
	v_mfma_f32_16x16x32_f16 v[102:105], v[2:5], v[150:153], v[106:109]
	v_mfma_f32_16x16x32_f16 v[0:3], v[2:5], v[154:157], v[22:25]
	s_nop 2
	global_load_dwordx4 v[22:25], v[158:159], off offset:2048
	global_load_dwordx4 v[106:109], v[158:159], off offset:3072
	global_load_dwordx4 v[130:133], v[54:55], off
	ds_read_b128 v[142:145], v74
	ds_read_b128 v[146:149], v74 offset:8192
	ds_read_b128 v[150:153], v74 offset:16384
	ds_read_b128 v[154:157], v74 offset:24576
	s_waitcnt lgkmcnt(3)
	v_mfma_f32_16x16x32_f16 v[98:101], v[18:21], v[142:145], v[98:101]
	s_waitcnt lgkmcnt(2)
	v_mfma_f32_16x16x32_f16 v[114:117], v[18:21], v[146:149], v[114:117]
	s_waitcnt lgkmcnt(1)
	v_mfma_f32_16x16x32_f16 v[118:121], v[18:21], v[150:153], v[118:121]
	s_waitcnt lgkmcnt(0)
	v_mfma_f32_16x16x32_f16 v[14:17], v[18:21], v[154:157], v[14:17]
	v_mfma_f32_16x16x32_f16 v[18:21], v[10:13], v[142:145], v[34:37]
	v_mfma_f32_16x16x32_f16 v[34:37], v[10:13], v[146:149], v[122:125]
	v_mfma_f32_16x16x32_f16 v[122:125], v[10:13], v[150:153], v[126:129]
	v_mfma_f32_16x16x32_f16 v[4:7], v[10:13], v[154:157], v[6:9]
	v_mfma_f32_16x16x32_f16 v[8:11], v[30:33], v[142:145], v[26:29]
	v_mfma_f32_16x16x32_f16 v[26:29], v[30:33], v[146:149], v[94:97]
	v_mfma_f32_16x16x32_f16 v[94:97], v[30:33], v[150:153], v[102:105]
	v_mfma_f32_16x16x32_f16 v[0:3], v[30:33], v[154:157], v[0:3]
	global_load_dwordx4 v[30:33], v[54:55], off offset:1024
	s_nop 0
	global_load_dwordx4 v[102:105], v[54:55], off offset:2048
	global_load_dwordx4 v[126:129], v[54:55], off offset:3072
	ds_read_b128 v[142:145], v75
	ds_read_b128 v[146:149], v75 offset:8192
	ds_read_b128 v[150:153], v75 offset:16384
	ds_read_b128 v[154:157], v75 offset:24576
	s_waitcnt lgkmcnt(3)
	v_mfma_f32_16x16x32_f16 v[98:101], v[46:49], v[142:145], v[98:101]
	s_waitcnt lgkmcnt(2)
	v_mfma_f32_16x16x32_f16 v[114:117], v[46:49], v[146:149], v[114:117]
	s_waitcnt lgkmcnt(1)
	v_mfma_f32_16x16x32_f16 v[118:121], v[46:49], v[150:153], v[118:121]
	s_waitcnt lgkmcnt(0)
	v_mfma_f32_16x16x32_f16 v[12:15], v[46:49], v[154:157], v[14:17]
	v_mfma_f32_16x16x32_f16 v[16:19], v[42:45], v[142:145], v[18:21]
	v_mfma_f32_16x16x32_f16 v[34:37], v[42:45], v[146:149], v[34:37]
	v_mfma_f32_16x16x32_f16 v[46:49], v[42:45], v[150:153], v[122:125]
	v_mfma_f32_16x16x32_f16 v[4:7], v[42:45], v[154:157], v[4:7]
	v_mfma_f32_16x16x32_f16 v[8:11], v[38:41], v[142:145], v[8:11]
	v_mfma_f32_16x16x32_f16 v[26:29], v[38:41], v[146:149], v[26:29]
	v_mfma_f32_16x16x32_f16 v[42:45], v[38:41], v[150:153], v[94:97]
	v_mfma_f32_16x16x32_f16 v[0:3], v[38:41], v[154:157], v[0:3]
	ds_read_b128 v[38:41], v76
	s_nop 0
	ds_read_b128 v[94:97], v76 offset:8192
	ds_read_b128 v[122:125], v76 offset:16384
	ds_read_b128 v[142:145], v76 offset:24576
	s_waitcnt vmcnt(17) lgkmcnt(3)
	v_mfma_f32_16x16x32_f16 v[98:101], v[82:85], v[38:41], v[98:101]
	s_waitcnt lgkmcnt(2)
	v_mfma_f32_16x16x32_f16 v[114:117], v[82:85], v[94:97], v[114:117]
	s_waitcnt lgkmcnt(1)
	v_mfma_f32_16x16x32_f16 v[118:121], v[82:85], v[122:125], v[118:121]
	s_waitcnt lgkmcnt(0)
	v_mfma_f32_16x16x32_f16 v[12:15], v[82:85], v[142:145], v[12:15]
	s_waitcnt vmcnt(16)
	v_mfma_f32_16x16x32_f16 v[16:19], v[86:89], v[38:41], v[16:19]
	v_mfma_f32_16x16x32_f16 v[34:37], v[86:89], v[94:97], v[34:37]
	v_mfma_f32_16x16x32_f16 v[46:49], v[86:89], v[122:125], v[46:49]
	v_mfma_f32_16x16x32_f16 v[4:7], v[86:89], v[142:145], v[4:7]
	s_waitcnt vmcnt(15)
	v_mfma_f32_16x16x32_f16 v[8:11], v[90:93], v[38:41], v[8:11]
	v_mfma_f32_16x16x32_f16 v[26:29], v[90:93], v[94:97], v[26:29]
	v_mfma_f32_16x16x32_f16 v[38:41], v[90:93], v[122:125], v[42:45]
	v_mfma_f32_16x16x32_f16 v[0:3], v[90:93], v[142:145], v[0:3]
	s_nop 1
	ds_read_b128 v[42:45], v77
	ds_read_b128 v[82:85], v77 offset:8192
	ds_read_b128 v[86:89], v77 offset:16384
	ds_read_b128 v[74:77], v77 offset:24576
	s_waitcnt vmcnt(7) lgkmcnt(3)
	v_mfma_f32_16x16x32_f16 v[90:93], v[134:137], v[42:45], v[98:101]
	s_waitcnt lgkmcnt(2)
	v_mfma_f32_16x16x32_f16 v[94:97], v[134:137], v[82:85], v[114:117]
	s_waitcnt lgkmcnt(1)
	v_mfma_f32_16x16x32_f16 v[98:101], v[134:137], v[86:89], v[118:121]
	s_waitcnt lgkmcnt(0)
	v_mfma_f32_16x16x32_f16 v[12:15], v[134:137], v[74:77], v[12:15]
	v_mfma_f32_16x16x32_f16 v[16:19], v[110:113], v[42:45], v[16:19]
	v_mfma_f32_16x16x32_f16 v[34:37], v[110:113], v[82:85], v[34:37]
	v_mfma_f32_16x16x32_f16 v[46:49], v[110:113], v[86:89], v[46:49]
	v_mfma_f32_16x16x32_f16 v[4:7], v[110:113], v[74:77], v[4:7]
	s_waitcnt vmcnt(6)
	v_mfma_f32_16x16x32_f16 v[8:11], v[138:141], v[42:45], v[8:11]
	v_mfma_f32_16x16x32_f16 v[26:29], v[138:141], v[82:85], v[26:29]
	v_mfma_f32_16x16x32_f16 v[38:41], v[138:141], v[86:89], v[38:41]
	v_mfma_f32_16x16x32_f16 v[0:3], v[138:141], v[74:77], v[0:3]
	ds_read_b128 v[42:45], v78
	ds_read_b128 v[74:77], v78 offset:8192
	ds_read_b128 v[82:85], v78 offset:16384
	ds_read_b128 v[86:89], v78 offset:24576
	s_waitcnt vmcnt(5) lgkmcnt(3)
	v_mfma_f32_16x16x32_f16 v[90:93], v[22:25], v[42:45], v[90:93]
	s_waitcnt lgkmcnt(2)
	v_mfma_f32_16x16x32_f16 v[94:97], v[22:25], v[74:77], v[94:97]
	s_waitcnt lgkmcnt(1)
	v_mfma_f32_16x16x32_f16 v[98:101], v[22:25], v[82:85], v[98:101]
	s_waitcnt lgkmcnt(0)
	v_mfma_f32_16x16x32_f16 v[12:15], v[22:25], v[86:89], v[12:15]
	s_waitcnt vmcnt(4)
	v_mfma_f32_16x16x32_f16 v[16:19], v[106:109], v[42:45], v[16:19]
	v_mfma_f32_16x16x32_f16 v[20:23], v[106:109], v[74:77], v[34:37]
	v_mfma_f32_16x16x32_f16 v[34:37], v[106:109], v[82:85], v[46:49]
	v_mfma_f32_16x16x32_f16 v[4:7], v[106:109], v[86:89], v[4:7]
	s_waitcnt vmcnt(3)
	v_mfma_f32_16x16x32_f16 v[8:11], v[130:133], v[42:45], v[8:11]
	v_mfma_f32_16x16x32_f16 v[24:27], v[130:133], v[74:77], v[26:29]
	v_mfma_f32_16x16x32_f16 v[38:41], v[130:133], v[82:85], v[38:41]
	v_mfma_f32_16x16x32_f16 v[0:3], v[130:133], v[86:89], v[0:3]
	ds_read_b128 v[42:45], v79
	ds_read_b128 v[46:49], v79 offset:8192
	ds_read_b128 v[74:77], v79 offset:16384
	ds_read_b128 v[82:85], v79 offset:24576
	s_waitcnt vmcnt(2) lgkmcnt(3)
	v_mfma_f32_16x16x32_f16 v[86:89], v[30:33], v[42:45], v[90:93]
	s_waitcnt lgkmcnt(2)
	v_mfma_f32_16x16x32_f16 v[90:93], v[30:33], v[46:49], v[94:97]
	s_waitcnt lgkmcnt(1)
	v_mfma_f32_16x16x32_f16 v[94:97], v[30:33], v[74:77], v[98:101]
	s_waitcnt lgkmcnt(0)
	v_mfma_f32_16x16x32_f16 v[12:15], v[30:33], v[82:85], v[12:15]
	s_waitcnt vmcnt(1)
	v_mfma_f32_16x16x32_f16 v[16:19], v[102:105], v[42:45], v[16:19]
	v_mfma_f32_16x16x32_f16 v[20:23], v[102:105], v[46:49], v[20:23]
	v_mfma_f32_16x16x32_f16 v[28:31], v[102:105], v[74:77], v[34:37]
	v_mfma_f32_16x16x32_f16 v[4:7], v[102:105], v[82:85], v[4:7]
	s_waitcnt vmcnt(0)
	v_mfma_f32_16x16x32_f16 v[8:11], v[126:129], v[42:45], v[8:11]
	v_mfma_f32_16x16x32_f16 v[24:27], v[126:129], v[46:49], v[24:27]
	v_mfma_f32_16x16x32_f16 v[32:35], v[126:129], v[74:77], v[38:41]
	v_mfma_f32_16x16x32_f16 v[0:3], v[126:129], v[82:85], v[0:3]
	s_nop 1
	global_load_dwordx4 v[36:39], v[56:57], off offset:1536
	global_load_dwordx4 v[40:43], v[56:57], off offset:1600
	global_load_dwordx4 v[44:47], v[56:57], off offset:1664
	v_mov_b32_e32 v58, v21
	v_mov_b32_e32 v59, v22
	v_mov_b32_e32 v74, v29
	v_mov_b32_e32 v56, v13
	v_mov_b32_e32 v57, v14
	v_mov_b32_e32 v75, v30
	v_mov_b32_e32 v48, v91
	v_mov_b32_e32 v49, v92
	v_mov_b32_e32 v54, v95
	v_mov_b32_e32 v55, v96
	v_mov_b32_e32 v76, v5
	v_mov_b32_e32 v77, v6
	s_barrier
	s_waitcnt vmcnt(2)
	v_pk_add_f32 v[78:79], v[86:87], v[36:37]
	v_pk_add_f32 v[82:83], v[88:89], v[38:39]
	v_add_f32_e32 v21, v90, v36
	v_pk_mov_b32 v[84:85], v[36:37], v[38:39] op_sel:[1,0]
	v_add_f32_e32 v22, v93, v39
	v_add_f32_e32 v29, v94, v36
	v_add_f32_e32 v36, v12, v36
	v_add_f32_e32 v37, v15, v39
	s_waitcnt vmcnt(1)
	v_add_f32_e32 v38, v20, v40
	v_add_f32_e32 v23, v23, v43
	v_add_f32_e32 v30, v97, v39
	v_pk_add_f32 v[12:13], v[16:17], v[40:41]
	v_pk_add_f32 v[14:15], v[18:19], v[42:43]
	v_pk_mov_b32 v[16:17], v[40:41], v[42:43] op_sel:[1,0]
	v_add_f32_e32 v28, v28, v40
	v_add_f32_e32 v31, v31, v43
	v_add_f32_e32 v39, v4, v40
	v_add_f32_e32 v40, v7, v43
	v_cvt_f16_f32_e32 v41, v21
	v_cvt_f16_f32_e32 v42, v22
	v_cvt_f16_f32_e32 v36, v36
	v_cvt_f16_f32_e32 v37, v37
	v_cvt_f16_f32_e32 v38, v38
	v_cvt_f16_f32_e32 v43, v23
	v_cvt_f16_f32_e32 v29, v29
	v_cvt_f16_f32_e32 v30, v30
	v_cvt_f16_f32_e32 v28, v28
	v_cvt_f16_f32_e32 v31, v31
	v_cvt_f16_f32_e32 v39, v39
	v_cvt_f16_f32_e32 v40, v40
	s_waitcnt vmcnt(0)
	v_pk_add_f32 v[4:5], v[8:9], v[44:45]
	v_pk_add_f32 v[6:7], v[10:11], v[46:47]
	v_pk_add_f32 v[10:11], v[48:49], v[84:85]
	v_pk_add_f32 v[20:21], v[56:57], v[84:85]
	v_cvt_pk_f16_f32 v12, v12, v13
	v_cvt_pk_f16_f32 v13, v14, v15
	v_pk_add_f32 v[14:15], v[58:59], v[16:17]
	v_cvt_pk_f16_f32 v8, v78, v79
	v_cvt_pk_f16_f32 v9, v82, v83
	v_pk_add_f32 v[18:19], v[54:55], v[84:85]
	v_pk_add_f32 v[22:23], v[74:75], v[16:17]
	v_pk_add_f32 v[16:17], v[76:77], v[16:17]
	v_cvt_pk_f16_f32 v4, v4, v5
	v_cvt_pk_f16_f32 v5, v6, v7
	v_cvt_pk_f16_f32 v6, v10, v11
	v_cvt_pk_f16_f32 v10, v20, v21
	v_cvt_pk_f16_f32 v11, v14, v15
	v_cvt_pk_f16_f32 v7, v18, v19
	v_cvt_pk_f16_f32 v14, v22, v23
	v_cvt_pk_f16_f32 v15, v16, v17
	ds_write2_b64 v73, v[8:9], v[12:13] offset1:4
	ds_write_b64 v69, v[4:5] offset:32832
	v_pack_b32_f16 v4, v41, v6
	v_alignbit_b32 v5, v42, v6, 16
	v_pack_b32_f16 v8, v36, v10
	v_alignbit_b32 v9, v37, v10, 16
	v_pack_b32_f16 v10, v38, v11
	v_alignbit_b32 v11, v43, v11, 16
	v_add_f32_e32 v24, v24, v44
	v_pack_b32_f16 v6, v29, v7
	v_alignbit_b32 v7, v30, v7, 16
	v_pack_b32_f16 v12, v28, v14
	v_alignbit_b32 v13, v31, v14, 16
	v_pack_b32_f16 v14, v39, v15
	v_alignbit_b32 v15, v40, v15, 16
	ds_write2_b64 v70, v[4:5], v[10:11] offset0:32 offset1:36
	ds_write2_b64 v71, v[6:7], v[12:13] offset0:64 offset1:68
	ds_write2_b64 v80, v[8:9], v[14:15] offset1:4
	v_add_f32_e32 v8, v27, v47
	v_cvt_f16_f32_e32 v24, v24
	v_cvt_f16_f32_e32 v8, v8
	v_mov_b32_e32 v4, v25
	v_mov_b32_e32 v5, v26
	v_pk_mov_b32 v[6:7], v[44:45], v[46:47] op_sel:[1,0]
	v_add_f32_e32 v9, v35, v47
	v_pk_add_f32 v[4:5], v[4:5], v[6:7]
	v_cvt_f16_f32_e32 v9, v9
	v_cvt_pk_f16_f32 v5, v4, v5
	v_pack_b32_f16 v4, v24, v5
	v_alignbit_b32 v5, v8, v5, 16
	ds_write_b64 v69, v[4:5] offset:45376
	v_add_f32_e32 v4, v32, v44
	v_cvt_f16_f32_e32 v8, v4
	v_mov_b32_e32 v4, v33
	v_mov_b32_e32 v5, v34
	v_pk_add_f32 v[4:5], v[4:5], v[6:7]
	v_add_f32_e32 v0, v0, v44
	v_cvt_pk_f16_f32 v5, v4, v5
	v_pack_b32_f16 v4, v8, v5
	v_alignbit_b32 v5, v9, v5, 16
	ds_write_b64 v69, v[4:5] offset:57920
	v_cvt_f16_f32_e32 v4, v0
	v_mov_b32_e32 v0, v1
	v_mov_b32_e32 v1, v2
	v_add_f32_e32 v2, v3, v47
	v_cvt_f16_f32_e32 v2, v2
	v_pk_add_f32 v[0:1], v[0:1], v[6:7]
	s_nop 0
	v_cvt_pk_f16_f32 v1, v0, v1
	v_pack_b32_f16 v0, v4, v1
	v_alignbit_b32 v1, v2, v1, 16
	ds_write_b64 v68, v[0:1] offset:32832
	s_waitcnt lgkmcnt(0)
	s_barrier
	ds_read_b128 v[0:3], v51 offset:32768
	ds_read_b128 v[4:7], v81 offset:32768
	s_waitcnt lgkmcnt(1)
	buffer_store_dwordx4 v[0:3], v50, s[0:3], 0 offen offset:768 sc1
	ds_read_b128 v[0:3], v53 offset:32768
	ds_read_b128 v[8:11], v160 offset:32768
	ds_read_b128 v[12:15], v61 offset:32768
	ds_read_b128 v[16:19], v63 offset:32768
	s_waitcnt lgkmcnt(4)
	buffer_store_dwordx4 v[4:7], v52, s[0:3], 0 offen offset:768 sc1
	s_waitcnt lgkmcnt(3)
	buffer_store_dwordx4 v[0:3], v60, s[0:3], 0 offen offset:768 sc1
	s_waitcnt lgkmcnt(2)
	buffer_store_dwordx4 v[8:11], v62, s[0:3], 0 offen offset:768 sc1
	s_waitcnt lgkmcnt(1)
	buffer_store_dwordx4 v[12:15], v64, s[0:3], 0 offen offset:768 sc1
	s_waitcnt lgkmcnt(0)
	buffer_store_dwordx4 v[16:19], v66, s[0:3], 0 offen offset:768 sc1
	s_endpgm
	.p2alignl 8, 3212836864
